# E6: E5 + counted lgkmcnt waits re-derived in the gla_a / cmp_fin / gla_c / router loops
# speedup vs baseline: 1.0083x; 1.0007x over previous
.LBB0_359:
	s_waitcnt lgkmcnt(0)
	s_or_b64 exec, exec, s[0:1]
	s_waitcnt lgkmcnt(0)
	s_barrier
	ds_read_b128 v[2:5], v63
	ds_read_b128 v[6:9], v63 offset:16
	ds_read_b128 v[10:13], v63 offset:32
	ds_read_b128 v[14:17], v63 offset:48
	s_waitcnt lgkmcnt(3)
	v_mov_b32_e32 v18, v2
	s_waitcnt lgkmcnt(2)
	v_mov_b32_e32 v19, v6
	v_mov_b32_e32 v6, v3
	s_waitcnt vmcnt(1)
	v_pk_mul_f32 v[2:3], v[48:49], v[6:7]
	v_mov_b32_e32 v6, v4
	s_waitcnt vmcnt(0)
	v_pk_fma_f32 v[2:3], v[50:51], v[18:19], v[2:3]
	v_mov_b32_e32 v7, v8
	v_pk_fma_f32 v[2:3], v[46:47], v[6:7], v[2:3]
	v_mov_b32_e32 v8, v5
	v_pk_fma_f32 v[2:3], v[44:45], v[8:9], v[2:3]
	s_nop 0
	v_add_f32_e32 v0, v33, v2
	v_add_f32_e32 v0, v0, v3
	s_waitcnt lgkmcnt(0)
	v_mov_b32_e32 v3, v14
	v_mov_b32_e32 v14, v11
	v_mov_b32_e32 v2, v10
	v_pk_mul_f32 v[4:5], v[38:39], v[14:15]
	s_nop 0
	v_pk_fma_f32 v[2:3], v[42:43], v[2:3], v[4:5]
	v_mov_b32_e32 v4, v12
	v_mov_b32_e32 v5, v16
	v_pk_fma_f32 v[2:3], v[40:41], v[4:5], v[2:3]
	v_mov_b32_e32 v16, v13
	v_pk_fma_f32 v[2:3], v[36:37], v[16:17], v[2:3]
	s_nop 0
	v_add_f32_e32 v0, v0, v2
	v_add_f32_e32 v0, v0, v3
	v_mul_f32_e64 v2, |v0|, s3
	v_exp_f32_e32 v2, v2
	v_min_f32_e32 v0, 0, v0
	v_add_f32_e32 v2, 1.0, v2
	v_cmp_gt_f32_e32 vcc, s21, v2
	s_nop 1
	v_cndmask_b32_e64 v3, 0, 32, vcc
	v_ldexp_f32 v2, v2, v3
	v_log_f32_e32 v14, v2
	ds_read_b128 v[2:5], v63 offset:64
	ds_read_b128 v[6:9], v63 offset:80
	v_mul_f32_e32 v10, 0x3f317217, v14
	v_fma_f32 v15, v14, s36, -v10
	s_waitcnt lgkmcnt(0)
	v_mov_b32_e32 v11, v6
	v_mov_b32_e32 v6, v3
	v_mov_b32_e32 v10, v2
	v_pk_mul_f32 v[2:3], v[48:49], v[6:7]
	v_mov_b32_e32 v6, v4
	v_pk_fma_f32 v[2:3], v[50:51], v[10:11], v[2:3]
	v_mov_b32_e32 v7, v8
	v_pk_fma_f32 v[6:7], v[46:47], v[6:7], v[2:3]
	v_mov_b32_e32 v8, v5
	ds_read_b128 v[2:5], v63 offset:96
	ds_read_b128 v[10:13], v63 offset:112
	v_pk_fma_f32 v[6:7], v[44:45], v[8:9], v[6:7]
	v_fmac_f32_e32 v15, 0x3377d1cf, v14
	v_add_f32_e32 v6, v33, v6
	v_add_f32_e32 v8, v6, v7
	s_waitcnt lgkmcnt(0)
	v_mov_b32_e32 v7, v10
	v_mov_b32_e32 v10, v3
	v_mov_b32_e32 v6, v2
	v_pk_mul_f32 v[2:3], v[38:39], v[10:11]
	v_fmac_f32_e32 v15, 0x3f317217, v14
	v_pk_fma_f32 v[2:3], v[42:43], v[6:7], v[2:3]
	v_mov_b32_e32 v6, v4
	v_mov_b32_e32 v7, v12
	v_pk_fma_f32 v[2:3], v[40:41], v[6:7], v[2:3]
	v_mov_b32_e32 v12, v5
	v_pk_fma_f32 v[2:3], v[36:37], v[12:13], v[2:3]
	v_cmp_lt_f32_e64 s[0:1], |v14|, s37
	v_add_f32_e32 v2, v8, v2
	v_add_f32_e32 v3, v2, v3
	v_mul_f32_e64 v2, |v3|, s3
	v_exp_f32_e32 v2, v2
	v_cndmask_b32_e64 v4, v14, v15, s[0:1]
	v_cndmask_b32_e32 v5, 0, v80, vcc
	v_sub_f32_e32 v4, v4, v5
	v_add_f32_e32 v2, 1.0, v2
	v_cmp_gt_f32_e32 vcc, s21, v2
	v_sub_f32_e32 v0, v0, v4
	s_nop 0
	v_cndmask_b32_e64 v5, 0, 32, vcc
	v_ldexp_f32 v2, v2, v5
	ds_read_b128 v[4:7], v63 offset:128
	ds_read_b128 v[8:11], v63 offset:144
	v_log_f32_e32 v16, v2
	v_fma_f32 v2, v0, s38, 0
	v_min_f32_e32 v0, 0, v3
	s_waitcnt lgkmcnt(1)
	v_mov_b32_e32 v12, v4
	s_waitcnt lgkmcnt(0)
	v_mov_b32_e32 v13, v8
	v_mov_b32_e32 v8, v5
	v_pk_mul_f32 v[4:5], v[48:49], v[8:9]
	v_mov_b32_e32 v8, v6
	v_pk_fma_f32 v[4:5], v[50:51], v[12:13], v[4:5]
	v_mov_b32_e32 v9, v10
	v_pk_fma_f32 v[8:9], v[46:47], v[8:9], v[4:5]
	v_mov_b32_e32 v10, v7
	ds_read_b128 v[4:7], v63 offset:160
	ds_read_b128 v[12:15], v63 offset:176
	v_pk_fma_f32 v[8:9], v[44:45], v[10:11], v[8:9]
	v_mul_f32_e32 v3, 0x3f317217, v16
	v_add_f32_e32 v8, v33, v8
	v_add_f32_e32 v10, v8, v9
	s_waitcnt lgkmcnt(0)
	v_mov_b32_e32 v9, v12
	v_mov_b32_e32 v12, v5
	v_mov_b32_e32 v8, v4
	v_pk_mul_f32 v[4:5], v[38:39], v[12:13]
	v_fma_f32 v3, v16, s36, -v3
	v_pk_fma_f32 v[4:5], v[42:43], v[8:9], v[4:5]
	v_mov_b32_e32 v8, v6
	v_mov_b32_e32 v9, v14
	v_pk_fma_f32 v[4:5], v[40:41], v[8:9], v[4:5]
	v_mov_b32_e32 v14, v7
	v_pk_fma_f32 v[4:5], v[36:37], v[14:15], v[4:5]
	v_fmac_f32_e32 v3, 0x3377d1cf, v16
	v_add_f32_e32 v4, v10, v4
	v_add_f32_e32 v4, v4, v5
	v_mul_f32_e64 v5, |v4|, s3
	v_exp_f32_e32 v5, v5
	v_fmac_f32_e32 v3, 0x3f317217, v16
	v_cmp_lt_f32_e64 s[0:1], |v16|, s37
	v_cndmask_b32_e32 v6, 0, v80, vcc
	v_add_f32_e32 v5, 1.0, v5
	v_cndmask_b32_e64 v3, v16, v3, s[0:1]
	v_cmp_gt_f32_e32 vcc, s21, v5
	v_sub_f32_e32 v3, v3, v6
	v_sub_f32_e32 v0, v0, v3
	v_cndmask_b32_e64 v6, 0, 32, vcc
	v_ldexp_f32 v5, v5, v6
	v_log_f32_e32 v16, v5
	v_fmamk_f32 v3, v0, 0x3d800000, v2
	v_min_f32_e32 v0, 0, v4
	ds_read_b128 v[4:7], v63 offset:192
	ds_read_b128 v[8:11], v63 offset:208
	v_mul_f32_e32 v12, 0x3f317217, v16
	v_fma_f32 v17, v16, s36, -v12
	v_fmac_f32_e32 v17, 0x3377d1cf, v16
	s_waitcnt lgkmcnt(1)
	v_mov_b32_e32 v12, v4
	s_waitcnt lgkmcnt(0)
	v_mov_b32_e32 v13, v8
	v_mov_b32_e32 v8, v5
	v_pk_mul_f32 v[4:5], v[48:49], v[8:9]
	v_mov_b32_e32 v8, v6
	v_pk_fma_f32 v[4:5], v[50:51], v[12:13], v[4:5]
	v_mov_b32_e32 v9, v10
	v_pk_fma_f32 v[8:9], v[46:47], v[8:9], v[4:5]
	v_mov_b32_e32 v10, v7
	ds_read_b128 v[4:7], v63 offset:224
	ds_read_b128 v[12:15], v63 offset:240
	v_pk_fma_f32 v[8:9], v[44:45], v[10:11], v[8:9]
	v_fmac_f32_e32 v17, 0x3f317217, v16
	v_add_f32_e32 v8, v33, v8
	v_add_f32_e32 v10, v8, v9
	s_waitcnt lgkmcnt(0)
	v_mov_b32_e32 v9, v12
	v_mov_b32_e32 v12, v5
	v_mov_b32_e32 v8, v4
	v_pk_mul_f32 v[4:5], v[38:39], v[12:13]
	v_cmp_lt_f32_e64 s[0:1], |v16|, s37
	v_pk_fma_f32 v[4:5], v[42:43], v[8:9], v[4:5]
	v_mov_b32_e32 v8, v6
	v_mov_b32_e32 v9, v14
	v_pk_fma_f32 v[4:5], v[40:41], v[8:9], v[4:5]
	v_mov_b32_e32 v14, v7
	v_pk_fma_f32 v[4:5], v[36:37], v[14:15], v[4:5]
	v_cndmask_b32_e64 v6, v16, v17, s[0:1]
	v_add_f32_e32 v4, v10, v4
	v_add_f32_e32 v5, v4, v5
	v_mul_f32_e64 v4, |v5|, s3
	v_exp_f32_e32 v4, v4
	v_cndmask_b32_e32 v7, 0, v80, vcc
	v_sub_f32_e32 v6, v6, v7
	v_sub_f32_e32 v0, v0, v6
	v_add_f32_e32 v4, 1.0, v4
	v_cmp_gt_f32_e32 vcc, s21, v4
	s_nop 1
	v_cndmask_b32_e64 v7, 0, 32, vcc
	v_ldexp_f32 v4, v4, v7
	ds_read_b128 v[6:9], v63 offset:256
	ds_read_b128 v[10:13], v63 offset:272
	v_log_f32_e32 v18, v4
	v_fmamk_f32 v4, v0, 0x3d800000, v3
	v_min_f32_e32 v0, 0, v5
	s_waitcnt lgkmcnt(1)
	v_mov_b32_e32 v14, v6
	s_waitcnt lgkmcnt(0)
	v_mov_b32_e32 v15, v10
	v_mov_b32_e32 v10, v7
	v_pk_mul_f32 v[6:7], v[48:49], v[10:11]
	v_mov_b32_e32 v10, v8
	v_pk_fma_f32 v[6:7], v[50:51], v[14:15], v[6:7]
	v_mov_b32_e32 v11, v12
	v_pk_fma_f32 v[10:11], v[46:47], v[10:11], v[6:7]
	v_mov_b32_e32 v12, v9
	ds_read_b128 v[6:9], v63 offset:288
	ds_read_b128 v[14:17], v63 offset:304
	v_pk_fma_f32 v[10:11], v[44:45], v[12:13], v[10:11]
	v_mul_f32_e32 v5, 0x3f317217, v18
	v_add_f32_e32 v10, v33, v10
	v_add_f32_e32 v12, v10, v11
	s_waitcnt lgkmcnt(0)
	v_mov_b32_e32 v11, v14
	v_mov_b32_e32 v14, v7
	v_mov_b32_e32 v10, v6
	v_pk_mul_f32 v[6:7], v[38:39], v[14:15]
	v_fma_f32 v5, v18, s36, -v5
	v_pk_fma_f32 v[6:7], v[42:43], v[10:11], v[6:7]
	v_mov_b32_e32 v10, v8
	v_mov_b32_e32 v11, v16
	v_pk_fma_f32 v[6:7], v[40:41], v[10:11], v[6:7]
	v_mov_b32_e32 v16, v9
	v_pk_fma_f32 v[6:7], v[36:37], v[16:17], v[6:7]
	v_fmac_f32_e32 v5, 0x3377d1cf, v18
	v_add_f32_e32 v6, v12, v6
	v_add_f32_e32 v6, v6, v7
	v_mul_f32_e64 v7, |v6|, s3
	v_exp_f32_e32 v7, v7
	v_fmac_f32_e32 v5, 0x3f317217, v18
	v_cmp_lt_f32_e64 s[0:1], |v18|, s37
	v_cndmask_b32_e32 v8, 0, v80, vcc
	v_add_f32_e32 v7, 1.0, v7
	v_cndmask_b32_e64 v5, v18, v5, s[0:1]
	v_cmp_gt_f32_e32 vcc, s21, v7
	v_sub_f32_e32 v5, v5, v8
	v_sub_f32_e32 v0, v0, v5
	v_cndmask_b32_e64 v8, 0, 32, vcc
	v_ldexp_f32 v7, v7, v8
	v_log_f32_e32 v18, v7
	v_fmamk_f32 v5, v0, 0x3d800000, v4
	v_min_f32_e32 v0, 0, v6
	ds_read_b128 v[6:9], v63 offset:320
	ds_read_b128 v[10:13], v63 offset:336
	v_mul_f32_e32 v14, 0x3f317217, v18
	v_fma_f32 v19, v18, s36, -v14
	v_fmac_f32_e32 v19, 0x3377d1cf, v18
	s_waitcnt lgkmcnt(1)
	v_mov_b32_e32 v14, v6
	s_waitcnt lgkmcnt(0)
	v_mov_b32_e32 v15, v10
	v_mov_b32_e32 v10, v7
	v_pk_mul_f32 v[6:7], v[48:49], v[10:11]
	v_mov_b32_e32 v10, v8
	v_pk_fma_f32 v[6:7], v[50:51], v[14:15], v[6:7]
	v_mov_b32_e32 v11, v12
	v_pk_fma_f32 v[10:11], v[46:47], v[10:11], v[6:7]
	v_mov_b32_e32 v12, v9
	ds_read_b128 v[6:9], v63 offset:352
	ds_read_b128 v[14:17], v63 offset:368
	v_pk_fma_f32 v[10:11], v[44:45], v[12:13], v[10:11]
	v_fmac_f32_e32 v19, 0x3f317217, v18
	v_add_f32_e32 v10, v33, v10
	v_add_f32_e32 v12, v10, v11
	s_waitcnt lgkmcnt(0)
	v_mov_b32_e32 v11, v14
	v_mov_b32_e32 v14, v7
	v_mov_b32_e32 v10, v6
	v_pk_mul_f32 v[6:7], v[38:39], v[14:15]
	v_cmp_lt_f32_e64 s[0:1], |v18|, s37
	v_pk_fma_f32 v[6:7], v[42:43], v[10:11], v[6:7]
	v_mov_b32_e32 v10, v8
	v_mov_b32_e32 v11, v16
	v_pk_fma_f32 v[6:7], v[40:41], v[10:11], v[6:7]
	v_mov_b32_e32 v16, v9
	v_pk_fma_f32 v[6:7], v[36:37], v[16:17], v[6:7]
	v_cndmask_b32_e64 v8, v18, v19, s[0:1]
	v_add_f32_e32 v6, v12, v6
	v_add_f32_e32 v7, v6, v7
	v_mul_f32_e64 v6, |v7|, s3
	v_exp_f32_e32 v6, v6
	v_cndmask_b32_e32 v9, 0, v80, vcc
	v_sub_f32_e32 v8, v8, v9
	v_sub_f32_e32 v0, v0, v8
	v_add_f32_e32 v6, 1.0, v6
	v_cmp_gt_f32_e32 vcc, s21, v6
	s_nop 1
	v_cndmask_b32_e64 v9, 0, 32, vcc
	v_ldexp_f32 v6, v6, v9
	ds_read_b128 v[8:11], v63 offset:384
	ds_read_b128 v[12:15], v63 offset:400
	v_log_f32_e32 v20, v6
	v_fmamk_f32 v6, v0, 0x3d800000, v5
	v_min_f32_e32 v0, 0, v7
	s_waitcnt lgkmcnt(1)
	v_mov_b32_e32 v16, v8
	s_waitcnt lgkmcnt(0)
	v_mov_b32_e32 v17, v12
	v_mov_b32_e32 v12, v9
	v_pk_mul_f32 v[8:9], v[48:49], v[12:13]
	v_mov_b32_e32 v12, v10
	v_pk_fma_f32 v[8:9], v[50:51], v[16:17], v[8:9]
	v_mov_b32_e32 v13, v14
	v_pk_fma_f32 v[12:13], v[46:47], v[12:13], v[8:9]
	v_mov_b32_e32 v14, v11
	ds_read_b128 v[8:11], v63 offset:416
	ds_read_b128 v[16:19], v63 offset:432
	v_pk_fma_f32 v[12:13], v[44:45], v[14:15], v[12:13]
	v_mul_f32_e32 v7, 0x3f317217, v20
	v_add_f32_e32 v12, v33, v12
	v_add_f32_e32 v14, v12, v13
	s_waitcnt lgkmcnt(0)
	v_mov_b32_e32 v13, v16
	v_mov_b32_e32 v16, v9
	v_mov_b32_e32 v12, v8
	v_pk_mul_f32 v[8:9], v[38:39], v[16:17]
	v_fma_f32 v7, v20, s36, -v7
	v_pk_fma_f32 v[8:9], v[42:43], v[12:13], v[8:9]
	v_mov_b32_e32 v12, v10
	v_mov_b32_e32 v13, v18
	v_pk_fma_f32 v[8:9], v[40:41], v[12:13], v[8:9]
	v_mov_b32_e32 v18, v11
	v_pk_fma_f32 v[8:9], v[36:37], v[18:19], v[8:9]
	v_fmac_f32_e32 v7, 0x3377d1cf, v20
	v_add_f32_e32 v8, v14, v8
	v_add_f32_e32 v8, v8, v9
	v_mul_f32_e64 v9, |v8|, s3
	v_exp_f32_e32 v9, v9
	v_fmac_f32_e32 v7, 0x3f317217, v20
	v_cmp_lt_f32_e64 s[0:1], |v20|, s37
	v_cndmask_b32_e32 v10, 0, v80, vcc
	v_add_f32_e32 v9, 1.0, v9
	v_cndmask_b32_e64 v7, v20, v7, s[0:1]
	v_cmp_gt_f32_e32 vcc, s21, v9
	v_sub_f32_e32 v7, v7, v10
	v_sub_f32_e32 v0, v0, v7
	v_cndmask_b32_e64 v10, 0, 32, vcc
	v_ldexp_f32 v9, v9, v10
	v_log_f32_e32 v20, v9
	v_fmamk_f32 v7, v0, 0x3d800000, v6
	v_min_f32_e32 v0, 0, v8
	ds_read_b128 v[8:11], v63 offset:448
	ds_read_b128 v[12:15], v63 offset:464
	v_mul_f32_e32 v16, 0x3f317217, v20
	v_fma_f32 v21, v20, s36, -v16
	v_fmac_f32_e32 v21, 0x3377d1cf, v20
	s_waitcnt lgkmcnt(1)
	v_mov_b32_e32 v16, v8
	s_waitcnt lgkmcnt(0)
	v_mov_b32_e32 v17, v12
	v_mov_b32_e32 v12, v9
	v_pk_mul_f32 v[8:9], v[48:49], v[12:13]
	v_mov_b32_e32 v12, v10
	v_pk_fma_f32 v[8:9], v[50:51], v[16:17], v[8:9]
	v_mov_b32_e32 v13, v14
	v_pk_fma_f32 v[12:13], v[46:47], v[12:13], v[8:9]
	v_mov_b32_e32 v14, v11
	ds_read_b128 v[8:11], v63 offset:480
	ds_read_b128 v[16:19], v63 offset:496
	v_pk_fma_f32 v[12:13], v[44:45], v[14:15], v[12:13]
	v_fmac_f32_e32 v21, 0x3f317217, v20
	v_add_f32_e32 v12, v33, v12
	v_add_f32_e32 v14, v12, v13
	s_waitcnt lgkmcnt(0)
	v_mov_b32_e32 v13, v16
	v_mov_b32_e32 v16, v9
	v_mov_b32_e32 v12, v8
	v_pk_mul_f32 v[8:9], v[38:39], v[16:17]
	v_cmp_lt_f32_e64 s[0:1], |v20|, s37
	v_pk_fma_f32 v[8:9], v[42:43], v[12:13], v[8:9]
	v_mov_b32_e32 v12, v10
	v_mov_b32_e32 v13, v18
	v_pk_fma_f32 v[8:9], v[40:41], v[12:13], v[8:9]
	v_mov_b32_e32 v18, v11
	v_pk_fma_f32 v[8:9], v[36:37], v[18:19], v[8:9]
	v_cndmask_b32_e64 v10, v20, v21, s[0:1]
	v_add_f32_e32 v8, v14, v8
	v_add_f32_e32 v9, v8, v9
	v_mul_f32_e64 v8, |v9|, s3
	v_exp_f32_e32 v8, v8
	v_cndmask_b32_e32 v11, 0, v80, vcc
	v_sub_f32_e32 v10, v10, v11
	v_sub_f32_e32 v0, v0, v10
	v_add_f32_e32 v8, 1.0, v8
	v_cmp_gt_f32_e32 vcc, s21, v8
	s_nop 1
	v_cndmask_b32_e64 v11, 0, 32, vcc
	v_ldexp_f32 v8, v8, v11
	ds_read_b128 v[10:13], v63 offset:512
	ds_read_b128 v[14:17], v63 offset:528
	v_log_f32_e32 v22, v8
	v_fmamk_f32 v8, v0, 0x3d800000, v7
	v_min_f32_e32 v0, 0, v9
	s_waitcnt lgkmcnt(1)
	v_mov_b32_e32 v18, v10
	s_waitcnt lgkmcnt(0)
	v_mov_b32_e32 v19, v14
	v_mov_b32_e32 v14, v11
	v_pk_mul_f32 v[10:11], v[48:49], v[14:15]
	v_mov_b32_e32 v14, v12
	v_pk_fma_f32 v[10:11], v[50:51], v[18:19], v[10:11]
	v_mov_b32_e32 v15, v16
	v_pk_fma_f32 v[14:15], v[46:47], v[14:15], v[10:11]
	v_mov_b32_e32 v16, v13
	ds_read_b128 v[10:13], v63 offset:544
	ds_read_b128 v[18:21], v63 offset:560
	v_pk_fma_f32 v[14:15], v[44:45], v[16:17], v[14:15]
	v_mul_f32_e32 v9, 0x3f317217, v22
	v_add_f32_e32 v14, v33, v14
	v_add_f32_e32 v16, v14, v15
	s_waitcnt lgkmcnt(0)
	v_mov_b32_e32 v15, v18
	v_mov_b32_e32 v18, v11
	v_mov_b32_e32 v14, v10
	v_pk_mul_f32 v[10:11], v[38:39], v[18:19]
	v_fma_f32 v9, v22, s36, -v9
	v_pk_fma_f32 v[10:11], v[42:43], v[14:15], v[10:11]
	v_mov_b32_e32 v14, v12
	v_mov_b32_e32 v15, v20
	v_pk_fma_f32 v[10:11], v[40:41], v[14:15], v[10:11]
	v_mov_b32_e32 v20, v13
	v_pk_fma_f32 v[10:11], v[36:37], v[20:21], v[10:11]
	v_fmac_f32_e32 v9, 0x3377d1cf, v22
	v_add_f32_e32 v10, v16, v10
	v_add_f32_e32 v10, v10, v11
	v_mul_f32_e64 v11, |v10|, s3
	v_exp_f32_e32 v11, v11
	v_fmac_f32_e32 v9, 0x3f317217, v22
	v_cmp_lt_f32_e64 s[0:1], |v22|, s37
	v_cndmask_b32_e32 v12, 0, v80, vcc
	v_add_f32_e32 v11, 1.0, v11
	v_cndmask_b32_e64 v9, v22, v9, s[0:1]
	v_cmp_gt_f32_e32 vcc, s21, v11
	v_sub_f32_e32 v9, v9, v12
	v_sub_f32_e32 v0, v0, v9
	v_cndmask_b32_e64 v12, 0, 32, vcc
	v_ldexp_f32 v11, v11, v12
	v_log_f32_e32 v22, v11
	v_fmamk_f32 v9, v0, 0x3d800000, v8
	v_min_f32_e32 v0, 0, v10
	ds_read_b128 v[10:13], v63 offset:576
	ds_read_b128 v[14:17], v63 offset:592
	v_mul_f32_e32 v18, 0x3f317217, v22
	v_fma_f32 v23, v22, s36, -v18
	v_fmac_f32_e32 v23, 0x3377d1cf, v22
	s_waitcnt lgkmcnt(1)
	v_mov_b32_e32 v18, v10
	s_waitcnt lgkmcnt(0)
	v_mov_b32_e32 v19, v14
	v_mov_b32_e32 v14, v11
	v_pk_mul_f32 v[10:11], v[48:49], v[14:15]
	v_mov_b32_e32 v14, v12
	v_pk_fma_f32 v[10:11], v[50:51], v[18:19], v[10:11]
	v_mov_b32_e32 v15, v16
	v_pk_fma_f32 v[14:15], v[46:47], v[14:15], v[10:11]
	v_mov_b32_e32 v16, v13
	ds_read_b128 v[10:13], v63 offset:608
	ds_read_b128 v[18:21], v63 offset:624
	v_pk_fma_f32 v[14:15], v[44:45], v[16:17], v[14:15]
	v_fmac_f32_e32 v23, 0x3f317217, v22
	v_add_f32_e32 v14, v33, v14
	v_add_f32_e32 v16, v14, v15
	s_waitcnt lgkmcnt(0)
	v_mov_b32_e32 v15, v18
	v_mov_b32_e32 v18, v11
	v_mov_b32_e32 v14, v10
	v_pk_mul_f32 v[10:11], v[38:39], v[18:19]
	v_cmp_lt_f32_e64 s[0:1], |v22|, s37
	v_pk_fma_f32 v[10:11], v[42:43], v[14:15], v[10:11]
	v_mov_b32_e32 v14, v12
	v_mov_b32_e32 v15, v20
	v_pk_fma_f32 v[10:11], v[40:41], v[14:15], v[10:11]
	v_mov_b32_e32 v20, v13
	v_pk_fma_f32 v[10:11], v[36:37], v[20:21], v[10:11]
	v_cndmask_b32_e64 v12, v22, v23, s[0:1]
	v_add_f32_e32 v10, v16, v10
	v_add_f32_e32 v10, v10, v11
	v_mul_f32_e64 v11, |v10|, s3
	v_exp_f32_e32 v11, v11
	v_cndmask_b32_e32 v13, 0, v80, vcc
	v_sub_f32_e32 v12, v12, v13
	v_sub_f32_e32 v0, v0, v12
	v_add_f32_e32 v11, 1.0, v11
	v_cmp_gt_f32_e32 vcc, s21, v11
	v_min_f32_e32 v23, 0, v10
	v_fmamk_f32 v0, v0, 0x3d800000, v9
	v_cndmask_b32_e64 v13, 0, 32, vcc
	v_ldexp_f32 v11, v11, v13
	v_log_f32_e32 v22, v11
	ds_read_b128 v[10:13], v63 offset:640
	ds_read_b128 v[14:17], v63 offset:656
	v_mul_f32_e32 v18, 0x3f317217, v22
	v_fma_f32 v24, v22, s36, -v18
	s_waitcnt lgkmcnt(0)
	v_mov_b32_e32 v19, v14
	v_mov_b32_e32 v14, v11
	v_mov_b32_e32 v18, v10
	v_pk_mul_f32 v[10:11], v[48:49], v[14:15]
	v_mov_b32_e32 v14, v12
	v_pk_fma_f32 v[10:11], v[50:51], v[18:19], v[10:11]
	v_mov_b32_e32 v15, v16
	v_pk_fma_f32 v[14:15], v[46:47], v[14:15], v[10:11]
	v_mov_b32_e32 v16, v13
	ds_read_b128 v[10:13], v63 offset:672
	ds_read_b128 v[18:21], v63 offset:688
	v_pk_fma_f32 v[14:15], v[44:45], v[16:17], v[14:15]
	v_fmac_f32_e32 v24, 0x3377d1cf, v22
	v_add_f32_e32 v14, v33, v14
	v_add_f32_e32 v16, v14, v15
	s_waitcnt lgkmcnt(0)
	v_mov_b32_e32 v15, v18
	v_mov_b32_e32 v18, v11
	v_mov_b32_e32 v14, v10
	v_pk_mul_f32 v[10:11], v[38:39], v[18:19]
	v_fmac_f32_e32 v24, 0x3f317217, v22
	v_pk_fma_f32 v[10:11], v[42:43], v[14:15], v[10:11]
	v_mov_b32_e32 v14, v12
	v_mov_b32_e32 v15, v20
	v_pk_fma_f32 v[10:11], v[40:41], v[14:15], v[10:11]
	v_mov_b32_e32 v20, v13
	v_pk_fma_f32 v[10:11], v[36:37], v[20:21], v[10:11]
	v_cmp_lt_f32_e64 s[0:1], |v22|, s37
	v_add_f32_e32 v10, v16, v10
	v_add_f32_e32 v10, v10, v11
	v_mul_f32_e64 v11, |v10|, s3
	v_exp_f32_e32 v11, v11
	v_cndmask_b32_e64 v12, v22, v24, s[0:1]
	v_cndmask_b32_e32 v13, 0, v80, vcc
	v_sub_f32_e32 v12, v12, v13
	v_add_f32_e32 v11, 1.0, v11
	v_cmp_gt_f32_e32 vcc, s21, v11
	v_min_f32_e32 v24, 0, v10
	s_nop 0
	v_cndmask_b32_e64 v13, 0, 32, vcc
	v_ldexp_f32 v11, v11, v13
	v_log_f32_e32 v22, v11
	v_sub_f32_e32 v11, v23, v12
	v_fmamk_f32 v23, v11, 0x3d800000, v0
	ds_read_b128 v[10:13], v63 offset:704
	ds_read_b128 v[14:17], v63 offset:720
	v_mul_f32_e32 v18, 0x3f317217, v22
	v_fma_f32 v25, v22, s36, -v18
	v_fmac_f32_e32 v25, 0x3377d1cf, v22
	s_waitcnt lgkmcnt(1)
	v_mov_b32_e32 v18, v10
	s_waitcnt lgkmcnt(0)
	v_mov_b32_e32 v19, v14
	v_mov_b32_e32 v14, v11
	v_pk_mul_f32 v[10:11], v[48:49], v[14:15]
	v_mov_b32_e32 v14, v12
	v_pk_fma_f32 v[10:11], v[50:51], v[18:19], v[10:11]
	v_mov_b32_e32 v15, v16
	v_pk_fma_f32 v[14:15], v[46:47], v[14:15], v[10:11]
	v_mov_b32_e32 v16, v13
	ds_read_b128 v[10:13], v63 offset:736
	ds_read_b128 v[18:21], v63 offset:752
	v_pk_fma_f32 v[14:15], v[44:45], v[16:17], v[14:15]
	v_fmac_f32_e32 v25, 0x3f317217, v22
	v_add_f32_e32 v14, v33, v14
	v_add_f32_e32 v16, v14, v15
	s_waitcnt lgkmcnt(0)
	v_mov_b32_e32 v15, v18
	v_mov_b32_e32 v18, v11
	v_mov_b32_e32 v14, v10
	v_pk_mul_f32 v[10:11], v[38:39], v[18:19]
	v_cmp_lt_f32_e64 s[0:1], |v22|, s37
	v_pk_fma_f32 v[10:11], v[42:43], v[14:15], v[10:11]
	v_mov_b32_e32 v14, v12
	v_mov_b32_e32 v15, v20
	v_pk_fma_f32 v[10:11], v[40:41], v[14:15], v[10:11]
	v_mov_b32_e32 v20, v13
	v_pk_fma_f32 v[10:11], v[36:37], v[20:21], v[10:11]
	v_cndmask_b32_e64 v12, v22, v25, s[0:1]
	v_add_f32_e32 v10, v16, v10
	v_add_f32_e32 v10, v10, v11
	v_mul_f32_e64 v11, |v10|, s3
	v_exp_f32_e32 v11, v11
	v_cndmask_b32_e32 v13, 0, v80, vcc
	v_sub_f32_e32 v12, v12, v13
	v_min_f32_e32 v25, 0, v10
	v_add_f32_e32 v11, 1.0, v11
	v_cmp_gt_f32_e32 vcc, s21, v11
	s_nop 1
	v_cndmask_b32_e64 v13, 0, 32, vcc
	v_ldexp_f32 v11, v11, v13
	v_log_f32_e32 v22, v11
	v_sub_f32_e32 v11, v24, v12
	v_fmamk_f32 v24, v11, 0x3d800000, v23
	ds_read_b128 v[10:13], v63 offset:768
	ds_read_b128 v[14:17], v63 offset:784
	v_mul_f32_e32 v18, 0x3f317217, v22
	v_fma_f32 v26, v22, s36, -v18
	v_fmac_f32_e32 v26, 0x3377d1cf, v22
	s_waitcnt lgkmcnt(1)
	v_mov_b32_e32 v18, v10
	s_waitcnt lgkmcnt(0)
	v_mov_b32_e32 v19, v14
	v_mov_b32_e32 v14, v11
	v_pk_mul_f32 v[10:11], v[48:49], v[14:15]
	v_mov_b32_e32 v14, v12
	v_pk_fma_f32 v[10:11], v[50:51], v[18:19], v[10:11]
	v_mov_b32_e32 v15, v16
	v_pk_fma_f32 v[14:15], v[46:47], v[14:15], v[10:11]
	v_mov_b32_e32 v16, v13
	ds_read_b128 v[10:13], v63 offset:800
	ds_read_b128 v[18:21], v63 offset:816
	v_pk_fma_f32 v[14:15], v[44:45], v[16:17], v[14:15]
	v_fmac_f32_e32 v26, 0x3f317217, v22
	v_add_f32_e32 v14, v33, v14
	v_add_f32_e32 v16, v14, v15
	s_waitcnt lgkmcnt(0)
	v_mov_b32_e32 v15, v18
	v_mov_b32_e32 v18, v11
	v_mov_b32_e32 v14, v10
	v_pk_mul_f32 v[10:11], v[38:39], v[18:19]
	v_cmp_lt_f32_e64 s[0:1], |v22|, s37
	v_pk_fma_f32 v[10:11], v[42:43], v[14:15], v[10:11]
	v_mov_b32_e32 v14, v12
	v_mov_b32_e32 v15, v20
	v_pk_fma_f32 v[10:11], v[40:41], v[14:15], v[10:11]
	v_mov_b32_e32 v20, v13
	v_pk_fma_f32 v[10:11], v[36:37], v[20:21], v[10:11]
	v_cndmask_b32_e64 v12, v22, v26, s[0:1]
	v_add_f32_e32 v10, v16, v10
	v_add_f32_e32 v10, v10, v11
	v_mul_f32_e64 v11, |v10|, s3
	v_exp_f32_e32 v11, v11
	v_cndmask_b32_e32 v13, 0, v80, vcc
	v_sub_f32_e32 v12, v12, v13
	v_min_f32_e32 v26, 0, v10
	v_add_f32_e32 v11, 1.0, v11
	v_cmp_gt_f32_e32 vcc, s21, v11
	s_nop 1
	v_cndmask_b32_e64 v13, 0, 32, vcc
	v_ldexp_f32 v11, v11, v13
	v_log_f32_e32 v22, v11
	v_sub_f32_e32 v11, v25, v12
	v_fmamk_f32 v25, v11, 0x3d800000, v24
	ds_read_b128 v[10:13], v63 offset:832
	ds_read_b128 v[14:17], v63 offset:848
	v_mul_f32_e32 v18, 0x3f317217, v22
	v_fma_f32 v27, v22, s36, -v18
	v_fmac_f32_e32 v27, 0x3377d1cf, v22
	s_waitcnt lgkmcnt(1)
	v_mov_b32_e32 v18, v10
	s_waitcnt lgkmcnt(0)
	v_mov_b32_e32 v19, v14
	v_mov_b32_e32 v14, v11
	v_pk_mul_f32 v[10:11], v[48:49], v[14:15]
	v_mov_b32_e32 v14, v12
	v_pk_fma_f32 v[10:11], v[50:51], v[18:19], v[10:11]
	v_mov_b32_e32 v15, v16
	v_pk_fma_f32 v[14:15], v[46:47], v[14:15], v[10:11]
	v_mov_b32_e32 v16, v13
	ds_read_b128 v[10:13], v63 offset:864
	ds_read_b128 v[18:21], v63 offset:880
	v_pk_fma_f32 v[14:15], v[44:45], v[16:17], v[14:15]
	v_fmac_f32_e32 v27, 0x3f317217, v22
	v_add_f32_e32 v14, v33, v14
	v_add_f32_e32 v16, v14, v15
	s_waitcnt lgkmcnt(0)
	v_mov_b32_e32 v15, v18
	v_mov_b32_e32 v18, v11
	v_mov_b32_e32 v14, v10
	v_pk_mul_f32 v[10:11], v[38:39], v[18:19]
	v_cmp_lt_f32_e64 s[0:1], |v22|, s37
	v_pk_fma_f32 v[10:11], v[42:43], v[14:15], v[10:11]
	v_mov_b32_e32 v14, v12
	v_mov_b32_e32 v15, v20
	v_pk_fma_f32 v[10:11], v[40:41], v[14:15], v[10:11]
	v_mov_b32_e32 v20, v13
	v_pk_fma_f32 v[10:11], v[36:37], v[20:21], v[10:11]
	v_cndmask_b32_e64 v12, v22, v27, s[0:1]
	v_add_f32_e32 v10, v16, v10
	v_add_f32_e32 v10, v10, v11
	v_mul_f32_e64 v11, |v10|, s3
	v_exp_f32_e32 v11, v11
	v_cndmask_b32_e32 v13, 0, v80, vcc
	v_sub_f32_e32 v12, v12, v13
	v_min_f32_e32 v27, 0, v10
	v_add_f32_e32 v11, 1.0, v11
	v_cmp_gt_f32_e32 vcc, s21, v11
	s_nop 1
	v_cndmask_b32_e64 v13, 0, 32, vcc
	v_ldexp_f32 v11, v11, v13
	v_log_f32_e32 v22, v11
	v_sub_f32_e32 v11, v26, v12
	v_fmamk_f32 v26, v11, 0x3d800000, v25
	ds_read_b128 v[10:13], v63 offset:896
	ds_read_b128 v[14:17], v63 offset:912
	v_mul_f32_e32 v18, 0x3f317217, v22
	v_fma_f32 v28, v22, s36, -v18
	v_fmac_f32_e32 v28, 0x3377d1cf, v22
	s_waitcnt lgkmcnt(1)
	v_mov_b32_e32 v18, v10
	s_waitcnt lgkmcnt(0)
	v_mov_b32_e32 v19, v14
	v_mov_b32_e32 v14, v11
	v_pk_mul_f32 v[10:11], v[48:49], v[14:15]
	v_mov_b32_e32 v14, v12
	v_pk_fma_f32 v[10:11], v[50:51], v[18:19], v[10:11]
	v_mov_b32_e32 v15, v16
	v_pk_fma_f32 v[14:15], v[46:47], v[14:15], v[10:11]
	v_mov_b32_e32 v16, v13
	ds_read_b128 v[10:13], v63 offset:928
	ds_read_b128 v[18:21], v63 offset:944
	v_pk_fma_f32 v[14:15], v[44:45], v[16:17], v[14:15]
	v_fmac_f32_e32 v28, 0x3f317217, v22
	v_add_f32_e32 v14, v33, v14
	v_add_f32_e32 v16, v14, v15
	s_waitcnt lgkmcnt(0)
	v_mov_b32_e32 v15, v18
	v_mov_b32_e32 v18, v11
	v_mov_b32_e32 v14, v10
	v_pk_mul_f32 v[10:11], v[38:39], v[18:19]
	v_cmp_lt_f32_e64 s[0:1], |v22|, s37
	v_pk_fma_f32 v[10:11], v[42:43], v[14:15], v[10:11]
	v_mov_b32_e32 v14, v12
	v_mov_b32_e32 v15, v20
	v_pk_fma_f32 v[10:11], v[40:41], v[14:15], v[10:11]
	v_mov_b32_e32 v20, v13
	v_pk_fma_f32 v[10:11], v[36:37], v[20:21], v[10:11]
	v_cndmask_b32_e64 v12, v22, v28, s[0:1]
	v_add_f32_e32 v10, v16, v10
	v_add_f32_e32 v10, v10, v11
	v_mul_f32_e64 v11, |v10|, s3
	v_exp_f32_e32 v11, v11
	v_cndmask_b32_e32 v13, 0, v80, vcc
	v_sub_f32_e32 v12, v12, v13
	v_min_f32_e32 v28, 0, v10
	v_add_f32_e32 v11, 1.0, v11
	v_cmp_gt_f32_e32 vcc, s21, v11
	s_nop 1
	v_cndmask_b32_e64 v13, 0, 32, vcc
	v_ldexp_f32 v11, v11, v13
	v_log_f32_e32 v22, v11
	v_sub_f32_e32 v11, v27, v12
	v_fmamk_f32 v27, v11, 0x3d800000, v26
	ds_read_b128 v[10:13], v63 offset:960
	ds_read_b128 v[14:17], v63 offset:976
	v_mul_f32_e32 v18, 0x3f317217, v22
	v_fma_f32 v29, v22, s36, -v18
	v_fmac_f32_e32 v29, 0x3377d1cf, v22
	s_waitcnt lgkmcnt(1)
	v_mov_b32_e32 v18, v10
	s_waitcnt lgkmcnt(0)
	v_mov_b32_e32 v19, v14
	v_mov_b32_e32 v14, v11
	v_pk_mul_f32 v[10:11], v[48:49], v[14:15]
	v_mov_b32_e32 v14, v12
	v_pk_fma_f32 v[10:11], v[50:51], v[18:19], v[10:11]
	v_mov_b32_e32 v15, v16
	v_pk_fma_f32 v[14:15], v[46:47], v[14:15], v[10:11]
	v_mov_b32_e32 v16, v13
	ds_read_b128 v[10:13], v63 offset:992
	ds_read_b128 v[18:21], v63 offset:1008
	v_pk_fma_f32 v[14:15], v[44:45], v[16:17], v[14:15]
	v_fmac_f32_e32 v29, 0x3f317217, v22
	v_add_f32_e32 v14, v33, v14
	v_add_f32_e32 v16, v14, v15
	s_waitcnt lgkmcnt(0)
	v_mov_b32_e32 v15, v18
	v_mov_b32_e32 v18, v11
	v_mov_b32_e32 v14, v10
	v_pk_mul_f32 v[10:11], v[38:39], v[18:19]
	v_cmp_lt_f32_e64 s[0:1], |v22|, s37
	v_pk_fma_f32 v[10:11], v[42:43], v[14:15], v[10:11]
	v_mov_b32_e32 v14, v12
	v_mov_b32_e32 v15, v20
	v_pk_fma_f32 v[10:11], v[40:41], v[14:15], v[10:11]
	v_mov_b32_e32 v20, v13
	v_pk_fma_f32 v[10:11], v[36:37], v[20:21], v[10:11]
	v_cndmask_b32_e64 v12, v22, v29, s[0:1]
	v_add_f32_e32 v10, v16, v10
	v_add_f32_e32 v10, v10, v11
	v_mul_f32_e64 v11, |v10|, s3
	v_exp_f32_e32 v11, v11
	v_cndmask_b32_e32 v13, 0, v80, vcc
	v_sub_f32_e32 v12, v12, v13
	v_sub_f32_e32 v12, v28, v12
	v_add_f32_e32 v11, 1.0, v11
	v_cmp_gt_f32_e32 vcc, s21, v11
	v_fmamk_f32 v16, v12, 0x3d800000, v27
	v_min_f32_e32 v10, 0, v10
	v_cndmask_b32_e64 v13, 0, 32, vcc
	v_ldexp_f32 v11, v11, v13
	v_log_f32_e32 v11, v11
	s_nop 0
	v_mul_f32_e32 v12, 0x3f317217, v11
	v_fma_f32 v12, v11, s36, -v12
	v_fmac_f32_e32 v12, 0x3377d1cf, v11
	v_fmac_f32_e32 v12, 0x3f317217, v11
	v_cmp_lt_f32_e64 s[0:1], |v11|, s37
	s_nop 1
	v_cndmask_b32_e64 v11, v11, v12, s[0:1]
	v_cndmask_b32_e32 v12, 0, v80, vcc
	v_sub_f32_e32 v11, v11, v12
	v_sub_f32_e32 v10, v10, v11
	v_fmamk_f32 v11, v10, 0x3d800000, v16
	ds_write_b32 v64, v11
	s_waitcnt lgkmcnt(0)
	s_barrier
	ds_read2st64_b32 v[12:13], v65 offset1:2
	ds_read2st64_b32 v[14:15], v65 offset0:4 offset1:6
	s_waitcnt lgkmcnt(1)
	v_add_f32_e32 v10, 0, v12
	v_cndmask_b32_e64 v12, 0, v10, s[6:7]
	v_add_f32_e32 v17, v13, v12
	v_cndmask_b32_e64 v12, v12, v17, s[8:9]
	s_waitcnt lgkmcnt(0)
	v_add_f32_e32 v17, v14, v12
	v_cndmask_b32_e64 v12, v12, v17, s[10:11]
	v_add_f32_e32 v17, v15, v12
	v_cndmask_b32_e64 v17, v12, v17, s[12:13]
	v_add_f32_e32 v12, v2, v17
	v_add_f32_e32 v2, v10, v13
	v_add_f32_e32 v30, v16, v17
	v_add_f32_e32 v10, v2, v14
	v_mov_b32_e32 v16, v15
	v_add_f32_e32 v18, v3, v17
	v_pk_add_f32 v[2:3], v[10:11], v[16:17]
	v_add_f32_e32 v19, v4, v17
	v_add_f32_e32 v20, v5, v17
	v_sub_f32_e32 v4, v2, v12
	v_sub_f32_e32 v5, v2, v18
	v_mul_f32_e32 v4, 0x3fb8aa3b, v4
	v_mul_f32_e32 v5, 0x3fb8aa3b, v5
	v_exp_f32_e32 v4, v4
	v_exp_f32_e32 v5, v5
	v_add_f32_e32 v21, v6, v17
	v_add_f32_e32 v22, v7, v17
	v_add_f32_e32 v28, v8, v17
	v_add_f32_e32 v29, v9, v17
	ds_read_u16 v6, v72
	ds_read_u16 v7, v72 offset:256
	ds_read_u16 v8, v72 offset:512
	ds_read_u16 v9, v72 offset:768
	ds_read_u16 v10, v72 offset:1024
	ds_read_u16 v11, v72 offset:1280
	ds_read_u16 v12, v72 offset:1536
	ds_read_u16 v13, v72 offset:1792
	s_waitcnt lgkmcnt(6)
	v_lshlrev_b32_e32 v7, 16, v7
	v_lshlrev_b32_e32 v6, 16, v6
	v_pk_mul_f32 v[4:5], v[4:5], v[6:7]
	v_sub_f32_e32 v6, v2, v19
	v_sub_f32_e32 v7, v2, v20
	v_mul_f32_e32 v6, 0x3fb8aa3b, v6
	v_mul_f32_e32 v7, 0x3fb8aa3b, v7
	v_exp_f32_e32 v6, v6
	v_exp_f32_e32 v7, v7
	v_cvt_pk_bf16_f32 v4, v4, v5
	v_sub_f32_e32 v5, v2, v21
	s_waitcnt lgkmcnt(4)
	v_lshlrev_b32_e32 v9, 16, v9
	v_lshlrev_b32_e32 v8, 16, v8
	v_mul_f32_e32 v5, 0x3fb8aa3b, v5
	v_pk_mul_f32 v[6:7], v[6:7], v[8:9]
	v_exp_f32_e32 v8, v5
	v_sub_f32_e32 v5, v2, v22
	v_mul_f32_e32 v5, 0x3fb8aa3b, v5
	v_exp_f32_e32 v9, v5
	v_cvt_pk_bf16_f32 v5, v6, v7
	s_waitcnt lgkmcnt(2)
	v_lshlrev_b32_e32 v7, 16, v11
	v_lshlrev_b32_e32 v6, 16, v10
	v_pk_mul_f32 v[6:7], v[8:9], v[6:7]
	v_sub_f32_e32 v8, v2, v28
	v_sub_f32_e32 v9, v2, v29
	v_mul_f32_e32 v8, 0x3fb8aa3b, v8
	v_mul_f32_e32 v9, 0x3fb8aa3b, v9
	v_exp_f32_e32 v8, v8
	v_exp_f32_e32 v9, v9
	v_add_f32_e32 v0, v0, v17
	s_waitcnt lgkmcnt(0)
	v_lshlrev_b32_e32 v11, 16, v13
	v_lshlrev_b32_e32 v10, 16, v12
	v_sub_f32_e32 v0, v2, v0
	v_add_f32_e32 v23, v23, v17
	v_pk_mul_f32 v[8:9], v[8:9], v[10:11]
	v_mul_f32_e32 v0, 0x3fb8aa3b, v0
	v_cvt_pk_bf16_f32 v6, v6, v7
	v_cvt_pk_bf16_f32 v7, v8, v9
	v_exp_f32_e32 v8, v0
	v_sub_f32_e32 v0, v2, v23
	v_mul_f32_e32 v0, 0x3fb8aa3b, v0
	v_exp_f32_e32 v9, v0
	v_add_f32_e32 v24, v24, v17
	v_add_f32_e32 v25, v25, v17
	v_add_f32_e32 v26, v26, v17
	v_add_f32_e32 v27, v27, v17
	ds_read_u16 v0, v72 offset:2048
	ds_read_u16 v10, v72 offset:2304
	ds_read_u16 v12, v72 offset:2560
	ds_read_u16 v13, v72 offset:2816
	ds_read_u16 v14, v72 offset:3072
	ds_read_u16 v15, v72 offset:3328
	ds_read_u16 v16, v72 offset:3584
	ds_read_u16 v17, v72 offset:3840
	s_waitcnt lgkmcnt(6)
	v_lshlrev_b32_e32 v11, 16, v10
	v_lshlrev_b32_e32 v10, 16, v0
	v_sub_f32_e32 v0, v2, v24
	v_mul_f32_e32 v0, 0x3fb8aa3b, v0
	v_pk_mul_f32 v[8:9], v[8:9], v[10:11]
	v_exp_f32_e32 v10, v0
	v_sub_f32_e32 v0, v2, v25
	v_mul_f32_e32 v0, 0x3fb8aa3b, v0
	v_exp_f32_e32 v11, v0
	v_sub_f32_e32 v0, v2, v26
	s_waitcnt lgkmcnt(4)
	v_lshlrev_b32_e32 v13, 16, v13
	v_lshlrev_b32_e32 v12, 16, v12
	v_mul_f32_e32 v0, 0x3fb8aa3b, v0
	v_pk_mul_f32 v[10:11], v[10:11], v[12:13]
	v_exp_f32_e32 v12, v0
	v_sub_f32_e32 v0, v2, v27
	v_mul_f32_e32 v0, 0x3fb8aa3b, v0
	v_exp_f32_e32 v13, v0
	v_sub_f32_e32 v0, v2, v30
	v_cvt_pk_bf16_f32 v8, v8, v9
	v_cvt_pk_bf16_f32 v9, v10, v11
	s_waitcnt lgkmcnt(2)
	v_lshlrev_b32_e32 v11, 16, v15
	v_lshlrev_b32_e32 v10, 16, v14
	v_mul_f32_e32 v0, 0x3fb8aa3b, v0
	v_pk_mul_f32 v[10:11], v[12:13], v[10:11]
	v_exp_f32_e32 v12, v0
	v_sub_f32_e32 v0, v2, v3
	v_mul_f32_e32 v0, 0x3fb8aa3b, v0
	v_exp_f32_e32 v13, v0
	s_waitcnt lgkmcnt(0)
	v_lshlrev_b32_e32 v15, 16, v17
	v_lshlrev_b32_e32 v14, 16, v16
	v_cvt_pk_bf16_f32 v10, v10, v11
	v_pk_mul_f32 v[12:13], v[12:13], v[14:15]
	s_nop 0
	v_cvt_pk_bf16_f32 v11, v12, v13
	ds_write_b128 v73, v[4:7]
	ds_write_b128 v74, v[8:11]
	s_and_saveexec_b64 s[0:1], s[14:15]
	s_cbranch_execz .LBB0_361
	v_mul_f32_e32 v0, 0x3fb8aa3b, v2
	v_exp_f32_e32 v0, v0
	v_ashrrev_i32_e32 v33, 31, v32
	v_lshl_add_u64 v[2:3], v[32:33], 2, s[22:23]
	global_store_dword v[2:3], v0, off
.LBB0_361:
	s_or_b64 exec, exec, s[0:1]
	ds_read_u16 v0, v75 offset:16384
	ds_read_u16 v5, v75 offset:19968
	ds_read_u16 v4, v75 offset:18944
	ds_read_u16 v3, v75 offset:17920
	ds_read_u16 v2, v75 offset:16896
	ds_read_u16 v6, v75 offset:17408
	ds_read_u16 v7, v75 offset:18432
	ds_read_u16 v8, v75 offset:19456
	v_readlane_b32 s0, v252, 6
	s_add_i32 s0, s0, s2
	s_waitcnt lgkmcnt(3)
	v_lshl_or_b32 v2, v2, 16, v0
	s_waitcnt lgkmcnt(2)
	v_lshl_or_b32 v3, v3, 16, v6
	s_waitcnt lgkmcnt(1)
	v_lshl_or_b32 v4, v4, 16, v7
	s_waitcnt lgkmcnt(0)
	v_lshl_or_b32 v5, v5, 16, v8
	ds_read_u16 v0, v75 offset:20480
	ds_read_u16 v6, v75 offset:21504
	ds_read_u16 v7, v75 offset:22528
	ds_read_u16 v8, v75 offset:23552
	ds_read_u16 v9, v75 offset:24064
	ds_read_u16 v10, v75 offset:23040
	ds_read_u16 v11, v75 offset:22016
	ds_read_u16 v12, v75 offset:20992
	ds_read_u16 v13, v75 offset:24576
	ds_read_u16 v14, v75 offset:25600
	ds_read_u16 v15, v75 offset:26624
	ds_read_u16 v16, v75 offset:27648
	ds_read_u16 v17, v75 offset:28160
	ds_read_u16 v18, v75 offset:27136
	ds_read_u16 v19, v75 offset:26112
	ds_read_u16 v20, v75 offset:25088
	ds_read_u16 v21, v75 offset:28672
	ds_read_u16 v22, v75 offset:29696
	ds_read_u16 v23, v75 offset:30720
	ds_read_u16 v24, v75 offset:31744
	ds_read_u16 v25, v75 offset:32256
	ds_read_u16 v26, v75 offset:31232
	ds_read_u16 v27, v75 offset:30208
	ds_read_u16 v28, v75 offset:29184
	s_sub_i32 s0, s0, 32
	s_cmpk_lt_i32 s0, 0x800
	v_readlane_b32 s1, v252, 7
	s_cselect_b32 s0, s0, s2
	ds_write_b128 v76, v[2:5]
	s_waitcnt lgkmcnt(15)
	v_lshl_or_b32 v2, v12, 16, v0
	v_lshl_or_b32 v3, v11, 16, v6
	v_lshl_or_b32 v4, v10, 16, v7
	v_lshl_or_b32 v5, v9, 16, v8
	s_lshl_b32 s1, s0, 4
	s_lshl_b32 s43, s0, 6
	ds_write_b128 v77, v[2:5]
	s_waitcnt lgkmcnt(10)
	v_lshl_or_b32 v2, v20, 16, v13
	v_lshl_or_b32 v3, v19, 16, v14
	v_lshl_or_b32 v4, v18, 16, v15
	v_lshl_or_b32 v5, v17, 16, v16
	s_and_b32 s1, s1, 0xfffff000
	s_and_b32 s43, s43, 0xfc0
	ds_write_b128 v78, v[2:5]
	s_waitcnt lgkmcnt(3)
	v_lshl_or_b32 v2, v28, 16, v21
	v_lshl_or_b32 v3, v27, 16, v22
	v_lshl_or_b32 v4, v26, 16, v23
	v_lshl_or_b32 v5, v25, 16, v24
	s_or_b32 s44, s1, s43
	s_bfe_u32 s43, s0, 0x20006
	ds_write_b128 v79, v[2:5]
	v_lshl_or_b32 v0, s43, 8, v52
	v_add_u32_e32 v2, s44, v1
	v_add_u32_e32 v3, s44, v53
	v_lshl_or_b32 v2, v2, 10, v0
	v_lshl_or_b32 v0, v3, 10, v0
	s_waitcnt lgkmcnt(0)
	s_barrier
	global_load_dwordx4 v[2:5], v2, s[16:17]
	s_nop 0
	global_load_dwordx4 v[6:9], v0, s[16:17]
	v_lshl_or_b32 v0, s43, 9, v54
	v_add_u32_e32 v10, s44, v55
	v_add_u32_e32 v11, s44, v56
	v_add_u32_e32 v18, s44, v57
	v_lshl_or_b32 v10, v10, 11, v0
	v_lshl_or_b32 v14, v11, 11, v0
	v_lshl_or_b32 v18, v18, 11, v0
	v_add_u32_e32 v19, s44, v58
	global_load_dwordx4 v[10:13], v10, s[18:19]
	s_nop 0
	global_load_dwordx4 v[14:17], v14, s[18:19]
	v_lshl_or_b32 v0, v19, 11, v0
	global_load_dwordx4 v[18:21], v18, s[18:19]
	s_nop 0
	global_load_dwordx4 v[22:25], v0, s[18:19]
	v_mov_b32_e32 v26, 0
	v_mov_b32_e32 v27, 0
	v_mov_b32_e32 v28, 0
	v_mov_b32_e32 v29, 0
	s_and_saveexec_b64 s[0:1], s[4:5]
	s_cbranch_execz .LBB0_356
	v_add_u32_e32 v0, s44, v59
	v_lshl_or_b32 v0, v0, 7, v60
	global_load_dwordx4 v[26:29], v0, s[24:25]
	s_branch .LBB0_356

.LBB0_367:
	v_bfe_u32 v138, v14, 4, 2
	s_lshl_b32 s4, s4, 5
	v_and_b32_e32 v0, 15, v14
	v_lshlrev_b32_e32 v17, 4, v138
	v_lshlrev_b32_e32 v14, 2, v14
	s_and_b32 s19, s4, 0x60
	v_lshl_or_b32 v1, s5, 6, v0
	v_lshl_or_b32 v0, v0, 6, v17
	s_lshl_b32 s5, s5, 13
	v_and_b32_e32 v14, 32, v14
	s_lshl_b32 s4, s19, 7
	v_bitop3_b32 v17, v0, s5, v14 bitop3:0xde
	v_bitop3_b32 v0, v0, s4, v14 bitop3:0xde
	s_mov_b64 s[4:5], 0x80
	s_add_i32 m0, s15, 0x18000
	v_lshl_add_u64 v[8:9], v[8:9], 0, s[4:5]
	s_waitcnt vmcnt(2)
	s_barrier
	global_load_lds_dwordx4 v[8:9], off
	v_lshl_add_u64 v[6:7], v[6:7], 0, s[4:5]
	s_add_i32 m0, s15, 0x1a000
	s_add_i32 s20, s15, 0x8000
	s_add_i32 s21, s15, 0xa000
	global_load_lds_dwordx4 v[6:7], off
	v_lshl_add_u64 v[4:5], v[4:5], 0, s[4:5]
	s_mov_b32 m0, s20
	s_add_u32 s12, s0, 0x80080
	global_load_lds_dwordx4 v[4:5], off
	v_lshl_add_u64 v[2:3], v[2:3], 0, s[4:5]
	s_mov_b32 m0, s21
	s_addc_u32 s13, s1, 0
	global_load_lds_dwordx4 v[2:3], off
	s_add_i32 m0, s15, 0x1c000
	v_lshl_add_u64 v[2:3], s[12:13], 0, v[132:133]
	global_load_lds_dwordx4 v[2:3], off
	v_lshl_add_u64 v[2:3], s[12:13], 0, v[130:131]
	s_add_i32 m0, s15, 0x1e000
	s_add_u32 s6, s6, s7
	global_load_lds_dwordx4 v[2:3], off
	v_lshlrev_b32_e32 v2, 15, v13
	v_and_b32_e32 v2, 0xffff0000, v2
	s_addc_u32 s7, 0, 0
	v_lshl_add_u32 v2, v15, 12, v2
	v_and_b32_e32 v3, 1, v13
	v_readlane_b32 s12, v252, 2
	v_lshl_or_b32 v2, v3, 6, v2
	v_readlane_b32 s13, v252, 3
	s_add_u32 s6, s12, s6
	v_lshl_add_u32 v2, v16, 1, v2
	v_mov_b32_e32 v3, v133
	s_addc_u32 s7, s13, s7
	s_mov_b64 s[10:11], 0x80080
	v_lshl_add_u64 v[2:3], s[6:7], 0, v[2:3]
	v_lshl_add_u64 v[134:135], v[2:3], 0, s[10:11]
	v_lshlrev_b32_e32 v2, 15, v10
	v_and_b32_e32 v2, 0xffff0000, v2
	v_lshl_add_u32 v2, v11, 12, v2
	v_and_b32_e32 v3, 1, v10
	v_lshl_or_b32 v2, v3, 6, v2
	s_waitcnt vmcnt(6)
	v_lshl_add_u32 v2, v12, 1, v2
	v_mov_b32_e32 v3, v133
	s_add_i32 s25, 0, 0x10000
	s_add_i32 s27, 0, 0x14000
	s_add_i32 s29, 0, 0x18000
	s_add_i32 s31, 0, 0x1c000
	v_lshl_add_u64 v[2:3], s[6:7], 0, v[2:3]
	v_add_u32_e32 v139, s25, v0
	v_add_u32_e32 v140, s27, v0
	s_add_i32 s25, s25, s8
	s_add_i32 s27, s27, s8
	v_add_u32_e32 v142, s29, v0
	v_add_u32_e32 v143, s31, v0
	s_add_i32 s29, s29, s8
	s_add_i32 s31, s31, s8
	v_lshl_add_u64 v[136:137], v[2:3], 0, s[10:11]
	s_mov_b32 s22, -2
	s_mov_b64 s[6:7], 0
	v_add_u32_e32 v141, 0, v17
	s_add_i32 s23, s15, 0xc000
	s_add_i32 s24, s15, 0xe000
	s_add_i32 s26, s25, 0x2000
	s_add_i32 s28, s27, 0x2000
	s_add_i32 s30, s29, 0x2000
	s_add_i32 s33, s31, 0x2000
	v_mov_b32_e32 v2, v133
	v_mov_b32_e32 v3, v133
	v_mov_b32_e32 v4, v133
	v_mov_b32_e32 v5, v133
	v_mov_b32_e32 v6, v133
	v_mov_b32_e32 v7, v133
	v_mov_b32_e32 v8, v133
	v_mov_b32_e32 v9, v133
	v_mov_b32_e32 v10, v133
	v_mov_b32_e32 v11, v133
	v_mov_b32_e32 v12, v133
	v_mov_b32_e32 v13, v133
	v_mov_b32_e32 v14, v133
	v_mov_b32_e32 v15, v133
	v_mov_b32_e32 v16, v133
	v_mov_b32_e32 v17, v133
	s_waitcnt vmcnt(0)
	v_mov_b32_e32 v22, v133
	v_mov_b32_e32 v23, v133
	v_mov_b32_e32 v24, v133
	v_mov_b32_e32 v25, v133
	v_mov_b32_e32 v30, v133
	v_mov_b32_e32 v31, v133
	v_mov_b32_e32 v32, v133
	v_mov_b32_e32 v33, v133
	v_mov_b32_e32 v38, v133
	v_mov_b32_e32 v39, v133
	v_mov_b32_e32 v40, v133
	v_mov_b32_e32 v41, v133
	v_mov_b32_e32 v46, v133
	v_mov_b32_e32 v47, v133
	v_mov_b32_e32 v48, v133
	v_mov_b32_e32 v49, v133
	v_mov_b32_e32 v18, v133
	v_mov_b32_e32 v19, v133
	v_mov_b32_e32 v20, v133
	v_mov_b32_e32 v21, v133
	v_mov_b32_e32 v26, v133
	v_mov_b32_e32 v27, v133
	v_mov_b32_e32 v28, v133
	v_mov_b32_e32 v29, v133
	v_mov_b32_e32 v34, v133
	v_mov_b32_e32 v35, v133
	v_mov_b32_e32 v36, v133
	v_mov_b32_e32 v37, v133
	v_mov_b32_e32 v42, v133
	v_mov_b32_e32 v43, v133
	v_mov_b32_e32 v44, v133
	v_mov_b32_e32 v45, v133
	v_mov_b32_e32 v50, v133
	v_mov_b32_e32 v51, v133
	v_mov_b32_e32 v52, v133
	v_mov_b32_e32 v53, v133
	v_mov_b32_e32 v54, v133
	v_mov_b32_e32 v55, v133
	v_mov_b32_e32 v56, v133
	v_mov_b32_e32 v57, v133
	v_mov_b32_e32 v58, v133
	v_mov_b32_e32 v59, v133
	v_mov_b32_e32 v60, v133
	v_mov_b32_e32 v61, v133
	v_mov_b32_e32 v62, v133
	v_mov_b32_e32 v63, v133
	v_mov_b32_e32 v64, v133
	v_mov_b32_e32 v65, v133
	v_mov_b32_e32 v66, v133
	v_mov_b32_e32 v67, v133
	v_mov_b32_e32 v68, v133
	v_mov_b32_e32 v69, v133
	v_mov_b32_e32 v70, v133
	v_mov_b32_e32 v71, v133
	v_mov_b32_e32 v72, v133
	v_mov_b32_e32 v73, v133
	v_mov_b32_e32 v74, v133
	v_mov_b32_e32 v75, v133
	v_mov_b32_e32 v76, v133
	v_mov_b32_e32 v77, v133
	v_mov_b32_e32 v78, v133
	v_mov_b32_e32 v79, v133
	v_mov_b32_e32 v80, v133
	v_mov_b32_e32 v81, v133
	v_mov_b32_e32 v86, v133
	v_mov_b32_e32 v87, v133
	v_mov_b32_e32 v88, v133
	v_mov_b32_e32 v89, v133
	v_mov_b32_e32 v94, v133
	v_mov_b32_e32 v95, v133
	v_mov_b32_e32 v96, v133
	v_mov_b32_e32 v97, v133
	v_mov_b32_e32 v102, v133
	v_mov_b32_e32 v103, v133
	v_mov_b32_e32 v104, v133
	v_mov_b32_e32 v105, v133
	v_mov_b32_e32 v110, v133
	v_mov_b32_e32 v111, v133
	v_mov_b32_e32 v112, v133
	v_mov_b32_e32 v113, v133
	v_mov_b32_e32 v82, v133
	v_mov_b32_e32 v83, v133
	v_mov_b32_e32 v84, v133
	v_mov_b32_e32 v85, v133
	v_mov_b32_e32 v90, v133
	v_mov_b32_e32 v91, v133
	v_mov_b32_e32 v92, v133
	v_mov_b32_e32 v93, v133
	v_mov_b32_e32 v98, v133
	v_mov_b32_e32 v99, v133
	v_mov_b32_e32 v100, v133
	v_mov_b32_e32 v101, v133
	v_mov_b32_e32 v106, v133
	v_mov_b32_e32 v107, v133
	v_mov_b32_e32 v108, v133
	v_mov_b32_e32 v109, v133
	v_mov_b32_e32 v114, v133
	v_mov_b32_e32 v115, v133
	v_mov_b32_e32 v116, v133
	v_mov_b32_e32 v117, v133
	v_mov_b32_e32 v118, v133
	v_mov_b32_e32 v119, v133
	v_mov_b32_e32 v120, v133
	v_mov_b32_e32 v121, v133
	v_mov_b32_e32 v122, v133
	v_mov_b32_e32 v123, v133
	v_mov_b32_e32 v124, v133
	v_mov_b32_e32 v125, v133
	v_mov_b32_e32 v126, v133
	v_mov_b32_e32 v127, v133
	v_mov_b32_e32 v128, v133
	v_mov_b32_e32 v129, v133
	s_barrier
	s_nop 0
	s_nop 0
	s_nop 0
	s_nop 0
	s_nop 0
	s_nop 0
	s_nop 0
	s_nop 0
	s_nop 0
	s_nop 0
	s_nop 0
	s_nop 0
	s_nop 0
	s_nop 0
	s_nop 0

.LBB0_444:
	s_or_b64 exec, exec, s[0:1]
	v_mul_i32_i24_e32 v0, 0xff0, v10
	v_sub_u32_e32 v0, v11, v0
	v_mul_i32_i24_e32 v11, 0xffff8081, v0
	v_add_u16_sdwa v11, v11, v0 dst_sel:DWORD dst_unused:UNUSED_PAD src0_sel:WORD_1 src1_sel:DWORD
	v_lshrrev_b16_e32 v13, 15, v11
	v_ashrrev_i16_e32 v11, 7, v11
	v_add_u16_e32 v13, v11, v13
	v_mul_lo_u16_e32 v11, 0xff, v13
	v_sub_u16_e32 v148, v0, v11
	v_ashrrev_i32_e32 v11, 31, v10
	v_lshlrev_b32_sdwa v150, v16, sext(v13) dst_sel:DWORD dst_unused:UNUSED_PAD src0_sel:DWORD src1_sel:WORD_0
	v_ashrrev_i32_e32 v151, 31, v150
	v_lshlrev_b64 v[10:11], 22, v[10:11]
	v_lshl_add_u64 v[10:11], s[2:3], 0, v[10:11]
	v_lshlrev_b64 v[150:151], 10, v[150:151]
	v_lshl_add_u64 v[150:151], v[10:11], 0, v[150:151]
	v_bfe_i32 v10, v148, 0, 16
	v_ashrrev_i32_e32 v11, 31, v10
	v_lshlrev_b64 v[152:153], 10, v[10:11]
	v_lshl_add_u64 v[150:151], v[150:151], 0, v[152:153]
	v_lshl_add_u64 v[150:151], v[2:3], 2, v[150:151]
	global_load_dword v0, v[150:151], off
	global_load_dword v149, v[150:151], off offset:1536
	v_cmp_gt_u32_e32 vcc, s8, v12
	v_cmp_lt_u32_e64 s[0:1], s24, v12
	v_bfe_i32 v12, v13, 0, 16
	v_cndmask_b32_e32 v150, v1, v5, vcc
	s_waitcnt vmcnt(0)
	v_add_f32_e32 v0, v0, v149
	v_add_f32_e32 v0, v150, v0
	v_mul_f32_e32 v149, 0x3d372713, v0
	v_mul_f32_e32 v149, v0, v149
	v_fma_f32 v149, v0, v149, v0
	v_mul_f32_e32 v149, 0x3f4c422a, v149
	v_add_f32_e32 v149, v149, v149
	v_mul_f32_e32 v149, 0x3fb8aa3b, v149
	v_exp_f32_e32 v149, v149
	v_mul_f32_e32 v0, 0.5, v0
	v_add_f32_e32 v13, 1.0, v149
	v_div_scale_f32 v149, s[26:27], v13, v13, 2.0
	v_rcp_f32_e32 v150, v149
	v_div_scale_f32 v151, vcc, 2.0, v13, 2.0
	v_fma_f32 v152, -v149, v150, 1.0
	v_fmac_f32_e32 v150, v152, v150
	v_mul_f32_e32 v152, v151, v150
	v_fma_f32 v153, -v149, v152, v151
	v_fmac_f32_e32 v152, v153, v150
	v_fma_f32 v149, -v149, v152, v151
	v_div_fmas_f32 v149, v149, v150, v152
	v_div_fixup_f32 v13, v149, v13, 2.0
	v_sub_f32_e32 v13, 1.0, v13
	v_add_f32_e32 v13, 1.0, v13
	v_mul_f32_e32 v0, v0, v13
	ds_write_b32 v14, v0
	s_waitcnt lgkmcnt(0)
	s_barrier
	ds_read_b128 v[150:153], v4
	ds_read_b128 v[154:157], v4 offset:16
	ds_read_b128 v[158:161], v4 offset:32
	ds_read_b128 v[162:165], v4 offset:48
	ds_read_b128 v[166:169], v4 offset:64
	ds_read_b128 v[170:173], v4 offset:80
	ds_read_b128 v[174:177], v4 offset:96
	ds_read_b128 v[178:181], v4 offset:112
	ds_read_b128 v[182:185], v4 offset:128
	ds_read_b128 v[186:189], v4 offset:144
	ds_read_b128 v[190:193], v4 offset:160
	ds_read_b128 v[194:197], v4 offset:176
	ds_read_b128 v[198:201], v4 offset:192
	ds_read_b128 v[202:205], v4 offset:208
	ds_read_b128 v[206:209], v4 offset:224
	ds_read_b128 v[210:213], v4 offset:240
	ds_read_b128 v[214:217], v4 offset:256
	ds_read_b128 v[218:221], v4 offset:272
	s_waitcnt lgkmcnt(15)
	v_fma_f32 v0, v26, v150, 0
	v_fma_f32 v13, v25, v151, 0
	v_fma_f32 v149, v24, v152, 0
	v_fma_f32 v222, v23, v153, 0
	s_waitcnt lgkmcnt(15)
	v_fmac_f32_e32 v0, v22, v154
	v_fmac_f32_e32 v13, v21, v155
	v_fmac_f32_e32 v149, v20, v156
	v_fmac_f32_e32 v222, v19, v157
	s_waitcnt lgkmcnt(15)
	v_fmac_f32_e32 v0, v147, v158
	v_fmac_f32_e32 v13, v42, v159
	v_fmac_f32_e32 v149, v41, v160
	v_fmac_f32_e32 v222, v40, v161
	s_waitcnt lgkmcnt(14)
	v_fmac_f32_e32 v0, v39, v162
	v_fmac_f32_e32 v13, v38, v163
	v_fmac_f32_e32 v149, v37, v164
	v_fmac_f32_e32 v222, v36, v165
	s_waitcnt lgkmcnt(13)
	v_fmac_f32_e32 v0, v145, v166
	v_fmac_f32_e32 v13, v144, v167
	v_fmac_f32_e32 v149, v143, v168
	v_fmac_f32_e32 v222, v142, v169
	s_waitcnt lgkmcnt(12)
	v_fmac_f32_e32 v0, v141, v170
	v_fmac_f32_e32 v13, v35, v171
	v_fmac_f32_e32 v149, v34, v172
	v_fmac_f32_e32 v222, v33, v173
	s_waitcnt lgkmcnt(11)
	v_fmac_f32_e32 v0, v32, v174
	v_fmac_f32_e32 v13, v27, v175
	v_fmac_f32_e32 v149, v53, v176
	v_fmac_f32_e32 v222, v52, v177
	s_waitcnt lgkmcnt(10)
	v_fmac_f32_e32 v0, v51, v178
	v_fmac_f32_e32 v13, v50, v179
	v_fmac_f32_e32 v149, v49, v180
	v_fmac_f32_e32 v222, v48, v181
	s_waitcnt lgkmcnt(9)
	v_fmac_f32_e32 v0, v31, v182
	v_fmac_f32_e32 v13, v30, v183
	v_fmac_f32_e32 v149, v29, v184
	v_fmac_f32_e32 v222, v28, v185
	s_waitcnt lgkmcnt(8)
	v_fmac_f32_e32 v0, v58, v186
	v_fmac_f32_e32 v13, v57, v187
	v_fmac_f32_e32 v149, v56, v188
	v_fmac_f32_e32 v222, v55, v189
	s_waitcnt lgkmcnt(7)
	v_fmac_f32_e32 v0, v54, v190
	v_fmac_f32_e32 v13, v44, v191
	v_fmac_f32_e32 v149, v43, v192
	v_fmac_f32_e32 v222, v66, v193
	s_waitcnt lgkmcnt(6)
	v_fmac_f32_e32 v0, v65, v194
	v_fmac_f32_e32 v13, v64, v195
	v_fmac_f32_e32 v149, v63, v196
	v_fmac_f32_e32 v222, v62, v197
	s_waitcnt lgkmcnt(5)
	v_fmac_f32_e32 v0, v47, v198
	v_fmac_f32_e32 v13, v46, v199
	v_fmac_f32_e32 v149, v45, v200
	v_fmac_f32_e32 v222, v99, v201
	s_waitcnt lgkmcnt(4)
	v_fmac_f32_e32 v0, v98, v202
	v_fmac_f32_e32 v13, v97, v203
	v_fmac_f32_e32 v149, v96, v204
	v_fmac_f32_e32 v222, v95, v205
	ds_read_b128 v[150:153], v4 offset:288
	ds_read_b128 v[154:157], v4 offset:304
	s_waitcnt lgkmcnt(5)
	v_fmac_f32_e32 v0, v61, v206
	v_fmac_f32_e32 v13, v60, v207
	v_fmac_f32_e32 v149, v59, v208
	v_fmac_f32_e32 v222, v72, v209
	s_waitcnt lgkmcnt(4)
	v_fmac_f32_e32 v0, v71, v210
	v_fmac_f32_e32 v13, v70, v211
	v_fmac_f32_e32 v149, v69, v212
	v_fmac_f32_e32 v222, v68, v213
	s_waitcnt lgkmcnt(3)
	v_fmac_f32_e32 v0, v67, v214
	v_fmac_f32_e32 v13, v74, v215
	v_fmac_f32_e32 v149, v73, v216
	v_fmac_f32_e32 v222, v79, v217
	s_waitcnt lgkmcnt(2)
	v_fmac_f32_e32 v0, v78, v218
	v_fmac_f32_e32 v13, v77, v219
	v_fmac_f32_e32 v149, v76, v220
	v_fmac_f32_e32 v222, v75, v221
	s_waitcnt lgkmcnt(1)
	v_fmac_f32_e32 v0, v85, v150
	v_fmac_f32_e32 v13, v82, v151
	v_fmac_f32_e32 v149, v81, v152
	v_fmac_f32_e32 v222, v80, v153
	ds_read_b128 v[150:153], v4 offset:320
	s_waitcnt lgkmcnt(1)
	v_fmac_f32_e32 v0, v93, v154
	v_fmac_f32_e32 v13, v92, v155
	v_fmac_f32_e32 v149, v91, v156
	v_fmac_f32_e32 v222, v90, v157
	ds_read_b128 v[154:157], v4 offset:336
	s_waitcnt lgkmcnt(1)
	v_fmac_f32_e32 v0, v84, v150
	v_fmac_f32_e32 v13, v83, v151
	v_fmac_f32_e32 v149, v106, v152
	v_fmac_f32_e32 v222, v105, v153
	ds_read_b128 v[150:153], v4 offset:352
	s_waitcnt lgkmcnt(1)
	v_fmac_f32_e32 v0, v104, v154
	v_fmac_f32_e32 v13, v103, v155
	v_fmac_f32_e32 v149, v102, v156
	v_fmac_f32_e32 v222, v101, v157
	ds_read_b128 v[154:157], v4 offset:368
	s_waitcnt lgkmcnt(1)
	v_fmac_f32_e32 v0, v100, v150
	v_fmac_f32_e32 v13, v89, v151
	v_fmac_f32_e32 v149, v88, v152
	v_fmac_f32_e32 v222, v87, v153
	ds_read_b128 v[150:153], v4 offset:384
	s_waitcnt lgkmcnt(1)
	v_fmac_f32_e32 v0, v86, v154
	v_fmac_f32_e32 v13, v136, v155
	v_fmac_f32_e32 v149, v135, v156
	v_fmac_f32_e32 v222, v134, v157
	ds_read_b128 v[154:157], v4 offset:400
	s_waitcnt lgkmcnt(1)
	v_fmac_f32_e32 v0, v94, v150
	v_fmac_f32_e32 v13, v113, v151
	v_fmac_f32_e32 v149, v112, v152
	v_fmac_f32_e32 v222, v111, v153
	ds_read_b128 v[150:153], v4 offset:416
	s_waitcnt lgkmcnt(1)
	v_fmac_f32_e32 v0, v110, v154
	v_fmac_f32_e32 v13, v109, v155
	v_fmac_f32_e32 v149, v108, v156
	v_fmac_f32_e32 v222, v107, v157
	ds_read_b128 v[154:157], v4 offset:432
	s_waitcnt lgkmcnt(1)
	v_fmac_f32_e32 v0, v114, v150
	v_fmac_f32_e32 v13, v127, v151
	v_fmac_f32_e32 v149, v126, v152
	v_fmac_f32_e32 v222, v125, v153
	ds_read_b128 v[150:153], v4 offset:448
	s_waitcnt lgkmcnt(1)
	v_fmac_f32_e32 v0, v124, v154
	v_fmac_f32_e32 v13, v123, v155
	v_fmac_f32_e32 v149, v140, v156
	v_fmac_f32_e32 v222, v139, v157
	ds_read_b128 v[154:157], v4 offset:464
	s_waitcnt lgkmcnt(1)
	v_fmac_f32_e32 v0, v122, v150
	v_fmac_f32_e32 v13, v121, v151
	v_fmac_f32_e32 v149, v120, v152
	v_fmac_f32_e32 v222, v119, v153
	ds_read_b128 v[150:153], v4 offset:480
	s_waitcnt lgkmcnt(1)
	v_fmac_f32_e32 v0, v118, v154
	v_fmac_f32_e32 v13, v117, v155
	v_fmac_f32_e32 v149, v116, v156
	v_fmac_f32_e32 v222, v115, v157
	ds_read_b128 v[154:157], v4 offset:496
	s_waitcnt lgkmcnt(1)
	v_fmac_f32_e32 v0, v133, v150
	v_fmac_f32_e32 v13, v132, v151
	v_fmac_f32_e32 v149, v131, v152
	v_fmac_f32_e32 v222, v130, v153
	s_waitcnt lgkmcnt(0)
	v_fmac_f32_e32 v0, v129, v154
	v_fmac_f32_e32 v13, v128, v155
	v_fmac_f32_e32 v149, v138, v156
	v_fmac_f32_e32 v222, v137, v157
	v_add_f32_e32 v0, v0, v13
	v_add_f32_e32 v13, v149, v222
	v_add_f32_e32 v0, v0, v13
	v_ashrrev_i32_e32 v13, 31, v12
	v_cvt_pk_bf16_f32 v149, v0, s0
	v_lshlrev_b64 v[12:13], 16, v[12:13]
	s_and_saveexec_b64 s[26:27], s[0:1]
	s_xor_b64 s[0:1], exec, s[26:27]
	s_cbranch_execz .LBB0_446
	v_lshlrev_b32_sdwa v0, v17, sext(v148) dst_sel:DWORD dst_unused:UNUSED_PAD src0_sel:DWORD src1_sel:WORD_0
	v_lshrrev_b32_sdwa v10, v18, sext(v148) dst_sel:DWORD dst_unused:UNUSED_PAD src0_sel:DWORD src1_sel:WORD_0
	v_and_b32_e32 v0, 24, v0
	v_and_b32_e32 v10, 4, v10
	v_and_b32_sdwa v11, sext(v148), s25 dst_sel:DWORD dst_unused:UNUSED_PAD src0_sel:WORD_0 src1_sel:DWORD
	v_or3_b32 v10, v0, v11, v10
	v_ashrrev_i32_e32 v11, 31, v10
	v_lshl_add_u64 v[12:13], v[8:9], 0, v[12:13]
	v_lshl_add_u64 v[10:11], v[10:11], 1, v[12:13]
	global_store_short v[10:11], v149, off

.Lnsa_prio_done:
	s_nop 0
	v_cmp_gt_i32_e32 vcc, s0, v2
	s_and_saveexec_b64 s[0:1], vcc
	v_readlane_b32 s12, v252, 32
	v_readlane_b32 s13, v252, 33
	v_readlane_b32 s14, v252, 34
	v_readlane_b32 s15, v252, 35
	v_readlane_b32 s16, v252, 36
	v_readlane_b32 s17, v252, 37
	v_readlane_b32 s18, v252, 38
	v_readlane_b32 s19, v252, 39
	v_readlane_b32 s20, v252, 40
	v_readlane_b32 s21, v252, 41
	v_readlane_b32 s22, v252, 42
	v_readlane_b32 s23, v252, 43
	v_readlane_b32 s24, v252, 44
	v_readlane_b32 s25, v252, 45
	v_readlane_b32 s26, v252, 46
	v_readlane_b32 s27, v252, 47
	s_cbranch_execz .LBB0_513
	v_and_b32_e32 v0, 0x7f, v2
	s_getpc_b64 s[2:3]
	s_add_u32 s2, s2, _ZL7kBucket@rel32@lo+4
	s_addc_u32 s3, s3, _ZL7kBucket@rel32@hi+12
	global_load_ubyte v0, v0, s[2:3]
	v_max_i32_e32 v1, 0x200, v2
	v_sub_u32_e32 v1, v1, v2
	s_movk_i32 s2, 0x1ff
	v_add_u32_e32 v4, 0x1ff, v1
	s_mov_b64 s[4:5], -1
	v_cmp_lt_u32_e32 vcc, s2, v4
	v_mov_b32_e32 v3, v2
	s_waitcnt vmcnt(0)
	v_lshlrev_b32_e32 v1, 3, v0
	s_and_saveexec_b64 s[2:3], vcc
	s_cbranch_execz .LBB0_510
	v_lshrrev_b32_e32 v6, 9, v4
	v_add_u32_e32 v0, -1, v6
	v_add_u32_e32 v3, 0x200, v2
	v_lshrrev_b32_e32 v4, 1, v0
	v_add_u32_e32 v7, 1, v4
	v_cmp_lt_u32_e32 vcc, 5, v0
	v_mov_b32_e32 v10, 0
	v_mov_b64_e32 v[4:5], v[2:3]
	s_and_saveexec_b64 s[4:5], vcc
	s_cbranch_execz .LBB0_506
	v_readlane_b32 s12, v252, 32
	v_readlane_b32 s13, v252, 33
	v_readlane_b32 s14, v252, 34
	v_readlane_b32 s15, v252, 35
	v_readlane_b32 s20, v252, 40
	v_readlane_b32 s21, v252, 41
	v_lshl_add_u32 v0, v2, 2, 0
	v_readlane_b32 s22, v252, 42
	v_readlane_b32 s23, v252, 43
	s_mov_b64 s[12:13], s[20:21]
	v_and_b32_e32 v8, -4, v7
	s_mov_b32 s9, 0
	v_add_u32_e32 v9, 0x10000, v0
	s_mov_b64 s[6:7], 0
	s_mov_b32 s8, 0x3fb8aa3b
	v_mov_b64_e32 v[4:5], v[2:3]
	s_mov_b64 s[14:15], s[22:23]
	v_readlane_b32 s16, v252, 36
	v_readlane_b32 s17, v252, 37
	v_readlane_b32 s18, v252, 38
	v_readlane_b32 s19, v252, 39
	v_readlane_b32 s24, v252, 44
	v_readlane_b32 s25, v252, 45
	v_readlane_b32 s26, v252, 46
	v_readlane_b32 s27, v252, 47
	s_nop 0
	s_nop 0
	s_nop 0
	s_nop 0
	s_nop 0
	s_nop 0
	s_nop 0
	s_nop 0
	s_nop 0
	s_nop 0
	s_nop 0
	s_nop 0
	s_nop 0

.LBB0_906:
	s_waitcnt lgkmcnt(0)
	s_or_b64 exec, exec, s[0:1]
	s_waitcnt lgkmcnt(0)
	s_barrier
	ds_read_b128 v[2:5], v144
	ds_read_b128 v[6:9], v144 offset:16
	ds_read_b128 v[10:13], v144 offset:32
	ds_read_b128 v[14:17], v144 offset:48
	s_bfe_u32 s37, s96, 0x20006
	s_waitcnt vmcnt(1)
	s_waitcnt lgkmcnt(3)
	v_mul_f32_e32 v0, v209, v3
	s_waitcnt vmcnt(0)
	v_fmac_f32_e32 v0, v208, v2
	s_waitcnt lgkmcnt(2)
	v_mul_f32_e32 v2, v204, v7
	v_fmac_f32_e32 v0, v207, v4
	v_fmac_f32_e32 v2, v205, v6
	v_fmac_f32_e32 v0, v206, v5
	v_fmac_f32_e32 v2, v203, v8
	v_add_f32_e32 v0, v197, v0
	v_fmac_f32_e32 v2, v202, v9
	v_add_f32_e32 v0, v0, v2
	s_waitcnt lgkmcnt(1)
	v_mul_f32_e32 v2, v200, v11
	v_fmac_f32_e32 v2, v201, v10
	v_fmac_f32_e32 v2, v199, v12
	v_fmac_f32_e32 v2, v198, v13
	v_add_f32_e32 v0, v0, v2
	s_waitcnt lgkmcnt(0)
	v_mul_f32_e32 v2, v195, v15
	v_fmac_f32_e32 v2, v196, v14
	v_fmac_f32_e32 v2, v194, v16
	v_fmac_f32_e32 v2, v193, v17
	v_add_f32_e32 v0, v0, v2
	v_mul_f32_e64 v2, |v0|, s81
	v_exp_f32_e32 v2, v2
	v_min_f32_e32 v0, 0, v0
	s_add_i32 m0, s78, 0
	v_mov_b32_e32 v34, 0
	v_add_f32_e32 v2, 1.0, v2
	v_cmp_gt_f32_e32 vcc, s82, v2
	v_mov_b32_e32 v35, 0
	v_mov_b32_e32 v36, 0
	v_cndmask_b32_e64 v3, 0, 32, vcc
	v_ldexp_f32 v2, v2, v3
	v_log_f32_e32 v10, v2
	ds_read_b128 v[2:5], v144 offset:64
	v_mov_b32_e32 v37, 0
	v_mul_f32_e32 v6, 0x3f317217, v10
	v_fma_f32 v11, v10, s83, -v6
	ds_read_b128 v[6:9], v144 offset:80
	s_waitcnt lgkmcnt(1)
	v_mul_f32_e32 v3, v209, v3
	v_fmac_f32_e32 v3, v208, v2
	v_fmac_f32_e32 v3, v207, v4
	v_fmac_f32_e32 v3, v206, v5
	v_add_f32_e32 v12, v197, v3
	s_waitcnt lgkmcnt(0)
	v_mul_f32_e32 v7, v204, v7
	ds_read_b128 v[2:5], v144 offset:96
	v_fmac_f32_e32 v7, v205, v6
	v_fmac_f32_e32 v7, v203, v8
	v_fmac_f32_e32 v7, v202, v9
	v_add_f32_e32 v12, v12, v7
	ds_read_b128 v[6:9], v144 offset:112
	s_waitcnt lgkmcnt(1)
	v_mul_f32_e32 v3, v200, v3
	v_fmac_f32_e32 v3, v201, v2
	v_fmac_f32_e32 v3, v199, v4
	v_fmac_f32_e32 v3, v198, v5
	v_add_f32_e32 v2, v12, v3
	s_waitcnt lgkmcnt(0)
	v_mul_f32_e32 v3, v195, v7
	v_fmac_f32_e32 v3, v196, v6
	v_fmac_f32_e32 v3, v194, v8
	v_fmac_f32_e32 v3, v193, v9
	v_add_f32_e32 v3, v2, v3
	v_mul_f32_e64 v2, |v3|, s81
	v_exp_f32_e32 v2, v2
	v_fmac_f32_e32 v11, 0x3377d1cf, v10
	v_fmac_f32_e32 v11, 0x3f317217, v10
	v_cmp_lt_f32_e64 s[0:1], |v10|, s84
	v_add_f32_e32 v2, 1.0, v2
	v_cndmask_b32_e32 v5, 0, v192, vcc
	v_cndmask_b32_e64 v4, v10, v11, s[0:1]
	v_cmp_gt_f32_e32 vcc, s82, v2
	v_sub_f32_e32 v4, v4, v5
	v_sub_f32_e32 v0, v0, v4
	v_cndmask_b32_e64 v5, 0, 32, vcc
	v_ldexp_f32 v2, v2, v5
	ds_read_b128 v[4:7], v144 offset:128
	ds_read_b128 v[8:11], v144 offset:144
	v_log_f32_e32 v12, v2
	s_mov_b32 s0, 0x3d800000
	v_fma_f32 v2, v0, s0, 0
	s_waitcnt lgkmcnt(1)
	v_mul_f32_e32 v5, v209, v5
	v_fmac_f32_e32 v5, v208, v4
	v_fmac_f32_e32 v5, v207, v6
	v_fmac_f32_e32 v5, v206, v7
	v_add_f32_e32 v13, v197, v5
	s_waitcnt lgkmcnt(0)
	v_mul_f32_e32 v9, v204, v9
	ds_read_b128 v[4:7], v144 offset:160
	v_fmac_f32_e32 v9, v205, v8
	v_fmac_f32_e32 v9, v203, v10
	v_fmac_f32_e32 v9, v202, v11
	v_add_f32_e32 v13, v13, v9
	ds_read_b128 v[8:11], v144 offset:176
	s_waitcnt lgkmcnt(1)
	v_mul_f32_e32 v5, v200, v5
	v_fmac_f32_e32 v5, v201, v4
	v_fmac_f32_e32 v5, v199, v6
	v_fmac_f32_e32 v5, v198, v7
	v_add_f32_e32 v4, v13, v5
	s_waitcnt lgkmcnt(0)
	v_mul_f32_e32 v5, v195, v9
	v_fmac_f32_e32 v5, v196, v8
	v_fmac_f32_e32 v5, v194, v10
	v_fmac_f32_e32 v5, v193, v11
	v_add_f32_e32 v4, v4, v5
	v_mul_f32_e64 v5, |v4|, s81
	v_exp_f32_e32 v5, v5
	v_min_f32_e32 v0, 0, v3
	v_mul_f32_e32 v3, 0x3f317217, v12
	v_fma_f32 v3, v12, s83, -v3
	v_fmac_f32_e32 v3, 0x3377d1cf, v12
	v_fmac_f32_e32 v3, 0x3f317217, v12
	v_cmp_lt_f32_e64 s[0:1], |v12|, s84
	v_add_f32_e32 v5, 1.0, v5
	v_cndmask_b32_e32 v6, 0, v192, vcc
	v_cndmask_b32_e64 v3, v12, v3, s[0:1]
	v_cmp_gt_f32_e32 vcc, s82, v5
	v_sub_f32_e32 v3, v3, v6
	v_sub_f32_e32 v0, v0, v3
	v_cndmask_b32_e64 v6, 0, 32, vcc
	v_ldexp_f32 v5, v5, v6
	v_log_f32_e32 v12, v5
	v_fmamk_f32 v3, v0, 0x3d800000, v2
	v_min_f32_e32 v0, 0, v4
	ds_read_b128 v[4:7], v144 offset:192
	v_mul_f32_e32 v8, 0x3f317217, v12
	v_fma_f32 v13, v12, s83, -v8
	ds_read_b128 v[8:11], v144 offset:208
	v_fmac_f32_e32 v13, 0x3377d1cf, v12
	s_waitcnt lgkmcnt(1)
	v_mul_f32_e32 v5, v209, v5
	v_fmac_f32_e32 v5, v208, v4
	v_fmac_f32_e32 v5, v207, v6
	v_fmac_f32_e32 v5, v206, v7
	v_add_f32_e32 v14, v197, v5
	s_waitcnt lgkmcnt(0)
	v_mul_f32_e32 v9, v204, v9
	ds_read_b128 v[4:7], v144 offset:224
	v_fmac_f32_e32 v9, v205, v8
	v_fmac_f32_e32 v9, v203, v10
	v_fmac_f32_e32 v9, v202, v11
	v_add_f32_e32 v14, v14, v9
	ds_read_b128 v[8:11], v144 offset:240
	s_waitcnt lgkmcnt(1)
	v_mul_f32_e32 v5, v200, v5
	v_fmac_f32_e32 v5, v201, v4
	v_fmac_f32_e32 v5, v199, v6
	v_fmac_f32_e32 v5, v198, v7
	v_add_f32_e32 v4, v14, v5
	s_waitcnt lgkmcnt(0)
	v_mul_f32_e32 v5, v195, v9
	v_fmac_f32_e32 v5, v196, v8
	v_fmac_f32_e32 v5, v194, v10
	v_fmac_f32_e32 v5, v193, v11
	v_add_f32_e32 v5, v4, v5
	v_mul_f32_e64 v4, |v5|, s81
	v_exp_f32_e32 v4, v4
	v_fmac_f32_e32 v13, 0x3f317217, v12
	v_cmp_lt_f32_e64 s[0:1], |v12|, s84
	v_cndmask_b32_e32 v7, 0, v192, vcc
	v_add_f32_e32 v4, 1.0, v4
	v_cndmask_b32_e64 v6, v12, v13, s[0:1]
	v_cmp_gt_f32_e32 vcc, s82, v4
	v_sub_f32_e32 v6, v6, v7
	v_sub_f32_e32 v0, v0, v6
	v_cndmask_b32_e64 v7, 0, 32, vcc
	v_ldexp_f32 v4, v4, v7
	ds_read_b128 v[6:9], v144 offset:256
	ds_read_b128 v[10:13], v144 offset:272
	v_log_f32_e32 v14, v4
	v_fmamk_f32 v4, v0, 0x3d800000, v3
	v_min_f32_e32 v0, 0, v5
	s_waitcnt lgkmcnt(1)
	v_mul_f32_e32 v7, v209, v7
	v_fmac_f32_e32 v7, v208, v6
	v_fmac_f32_e32 v7, v207, v8
	v_fmac_f32_e32 v7, v206, v9
	v_add_f32_e32 v15, v197, v7
	s_waitcnt lgkmcnt(0)
	v_mul_f32_e32 v11, v204, v11
	ds_read_b128 v[6:9], v144 offset:288
	v_fmac_f32_e32 v11, v205, v10
	v_fmac_f32_e32 v11, v203, v12
	v_fmac_f32_e32 v11, v202, v13
	v_add_f32_e32 v15, v15, v11
	ds_read_b128 v[10:13], v144 offset:304
	s_waitcnt lgkmcnt(1)
	v_mul_f32_e32 v7, v200, v7
	v_fmac_f32_e32 v7, v201, v6
	v_fmac_f32_e32 v7, v199, v8
	v_fmac_f32_e32 v7, v198, v9
	v_add_f32_e32 v6, v15, v7
	s_waitcnt lgkmcnt(0)
	v_mul_f32_e32 v7, v195, v11
	v_fmac_f32_e32 v7, v196, v10
	v_fmac_f32_e32 v7, v194, v12
	v_fmac_f32_e32 v7, v193, v13
	v_add_f32_e32 v6, v6, v7
	v_mul_f32_e64 v7, |v6|, s81
	v_exp_f32_e32 v7, v7
	v_mul_f32_e32 v5, 0x3f317217, v14
	v_fma_f32 v5, v14, s83, -v5
	v_fmac_f32_e32 v5, 0x3377d1cf, v14
	v_fmac_f32_e32 v5, 0x3f317217, v14
	v_cmp_lt_f32_e64 s[0:1], |v14|, s84
	v_add_f32_e32 v7, 1.0, v7
	v_cndmask_b32_e32 v8, 0, v192, vcc
	v_cndmask_b32_e64 v5, v14, v5, s[0:1]
	v_cmp_gt_f32_e32 vcc, s82, v7
	v_sub_f32_e32 v5, v5, v8
	v_sub_f32_e32 v0, v0, v5
	v_cndmask_b32_e64 v8, 0, 32, vcc
	v_ldexp_f32 v7, v7, v8
	v_log_f32_e32 v14, v7
	v_fmamk_f32 v5, v0, 0x3d800000, v4
	v_min_f32_e32 v0, 0, v6
	ds_read_b128 v[6:9], v144 offset:320
	v_mul_f32_e32 v10, 0x3f317217, v14
	v_fma_f32 v15, v14, s83, -v10
	ds_read_b128 v[10:13], v144 offset:336
	v_fmac_f32_e32 v15, 0x3377d1cf, v14
	s_waitcnt lgkmcnt(1)
	v_mul_f32_e32 v7, v209, v7
	v_fmac_f32_e32 v7, v208, v6
	v_fmac_f32_e32 v7, v207, v8
	v_fmac_f32_e32 v7, v206, v9
	v_add_f32_e32 v16, v197, v7
	s_waitcnt lgkmcnt(0)
	v_mul_f32_e32 v11, v204, v11
	ds_read_b128 v[6:9], v144 offset:352
	v_fmac_f32_e32 v11, v205, v10
	v_fmac_f32_e32 v11, v203, v12
	v_fmac_f32_e32 v11, v202, v13
	v_add_f32_e32 v16, v16, v11
	ds_read_b128 v[10:13], v144 offset:368
	s_waitcnt lgkmcnt(1)
	v_mul_f32_e32 v7, v200, v7
	v_fmac_f32_e32 v7, v201, v6
	v_fmac_f32_e32 v7, v199, v8
	v_fmac_f32_e32 v7, v198, v9
	v_add_f32_e32 v6, v16, v7
	s_waitcnt lgkmcnt(0)
	v_mul_f32_e32 v7, v195, v11
	v_fmac_f32_e32 v7, v196, v10
	v_fmac_f32_e32 v7, v194, v12
	v_fmac_f32_e32 v7, v193, v13
	v_add_f32_e32 v7, v6, v7
	v_mul_f32_e64 v6, |v7|, s81
	v_exp_f32_e32 v6, v6
	v_fmac_f32_e32 v15, 0x3f317217, v14
	v_cmp_lt_f32_e64 s[0:1], |v14|, s84
	v_cndmask_b32_e32 v9, 0, v192, vcc
	v_add_f32_e32 v6, 1.0, v6
	v_cndmask_b32_e64 v8, v14, v15, s[0:1]
	v_cmp_gt_f32_e32 vcc, s82, v6
	v_sub_f32_e32 v8, v8, v9
	v_sub_f32_e32 v0, v0, v8
	v_cndmask_b32_e64 v9, 0, 32, vcc
	v_ldexp_f32 v6, v6, v9
	ds_read_b128 v[8:11], v144 offset:384
	ds_read_b128 v[12:15], v144 offset:400
	v_log_f32_e32 v16, v6
	v_fmamk_f32 v6, v0, 0x3d800000, v5
	v_min_f32_e32 v0, 0, v7
	s_waitcnt lgkmcnt(1)
	v_mul_f32_e32 v9, v209, v9
	v_fmac_f32_e32 v9, v208, v8
	v_fmac_f32_e32 v9, v207, v10
	v_fmac_f32_e32 v9, v206, v11
	v_add_f32_e32 v17, v197, v9
	s_waitcnt lgkmcnt(0)
	v_mul_f32_e32 v13, v204, v13
	ds_read_b128 v[8:11], v144 offset:416
	v_fmac_f32_e32 v13, v205, v12
	v_fmac_f32_e32 v13, v203, v14
	v_fmac_f32_e32 v13, v202, v15
	v_add_f32_e32 v17, v17, v13
	ds_read_b128 v[12:15], v144 offset:432
	s_waitcnt lgkmcnt(1)
	v_mul_f32_e32 v9, v200, v9
	v_fmac_f32_e32 v9, v201, v8
	v_fmac_f32_e32 v9, v199, v10
	v_fmac_f32_e32 v9, v198, v11
	v_add_f32_e32 v8, v17, v9
	s_waitcnt lgkmcnt(0)
	v_mul_f32_e32 v9, v195, v13
	v_fmac_f32_e32 v9, v196, v12
	v_fmac_f32_e32 v9, v194, v14
	v_fmac_f32_e32 v9, v193, v15
	v_add_f32_e32 v8, v8, v9
	v_mul_f32_e64 v9, |v8|, s81
	v_exp_f32_e32 v9, v9
	v_mul_f32_e32 v7, 0x3f317217, v16
	v_fma_f32 v7, v16, s83, -v7
	v_fmac_f32_e32 v7, 0x3377d1cf, v16
	v_fmac_f32_e32 v7, 0x3f317217, v16
	v_cmp_lt_f32_e64 s[0:1], |v16|, s84
	v_add_f32_e32 v9, 1.0, v9
	v_cndmask_b32_e32 v10, 0, v192, vcc
	v_cndmask_b32_e64 v7, v16, v7, s[0:1]
	v_cmp_gt_f32_e32 vcc, s82, v9
	v_sub_f32_e32 v7, v7, v10
	v_sub_f32_e32 v0, v0, v7
	v_cndmask_b32_e64 v10, 0, 32, vcc
	v_ldexp_f32 v9, v9, v10
	v_log_f32_e32 v16, v9
	v_fmamk_f32 v7, v0, 0x3d800000, v6
	v_min_f32_e32 v0, 0, v8
	ds_read_b128 v[8:11], v144 offset:448
	v_mul_f32_e32 v12, 0x3f317217, v16
	v_fma_f32 v17, v16, s83, -v12
	ds_read_b128 v[12:15], v144 offset:464
	v_fmac_f32_e32 v17, 0x3377d1cf, v16
	s_waitcnt lgkmcnt(1)
	v_mul_f32_e32 v9, v209, v9
	v_fmac_f32_e32 v9, v208, v8
	v_fmac_f32_e32 v9, v207, v10
	v_fmac_f32_e32 v9, v206, v11
	v_add_f32_e32 v18, v197, v9
	s_waitcnt lgkmcnt(0)
	v_mul_f32_e32 v13, v204, v13
	ds_read_b128 v[8:11], v144 offset:480
	v_fmac_f32_e32 v13, v205, v12
	v_fmac_f32_e32 v13, v203, v14
	v_fmac_f32_e32 v13, v202, v15
	v_add_f32_e32 v18, v18, v13
	ds_read_b128 v[12:15], v144 offset:496
	s_waitcnt lgkmcnt(1)
	v_mul_f32_e32 v9, v200, v9
	v_fmac_f32_e32 v9, v201, v8
	v_fmac_f32_e32 v9, v199, v10
	v_fmac_f32_e32 v9, v198, v11
	v_add_f32_e32 v8, v18, v9
	s_waitcnt lgkmcnt(0)
	v_mul_f32_e32 v9, v195, v13
	v_fmac_f32_e32 v9, v196, v12
	v_fmac_f32_e32 v9, v194, v14
	v_fmac_f32_e32 v9, v193, v15
	v_add_f32_e32 v9, v8, v9
	v_mul_f32_e64 v8, |v9|, s81
	v_exp_f32_e32 v8, v8
	v_fmac_f32_e32 v17, 0x3f317217, v16
	v_cmp_lt_f32_e64 s[0:1], |v16|, s84
	v_cndmask_b32_e32 v11, 0, v192, vcc
	v_add_f32_e32 v8, 1.0, v8
	v_cndmask_b32_e64 v10, v16, v17, s[0:1]
	v_cmp_gt_f32_e32 vcc, s82, v8
	v_sub_f32_e32 v10, v10, v11
	v_sub_f32_e32 v0, v0, v10
	v_cndmask_b32_e64 v11, 0, 32, vcc
	v_ldexp_f32 v8, v8, v11
	ds_read_b128 v[10:13], v144 offset:512
	ds_read_b128 v[14:17], v144 offset:528
	v_log_f32_e32 v18, v8
	v_fmamk_f32 v8, v0, 0x3d800000, v7
	v_min_f32_e32 v0, 0, v9
	s_waitcnt lgkmcnt(1)
	v_mul_f32_e32 v11, v209, v11
	v_fmac_f32_e32 v11, v208, v10
	v_fmac_f32_e32 v11, v207, v12
	v_fmac_f32_e32 v11, v206, v13
	v_add_f32_e32 v19, v197, v11
	s_waitcnt lgkmcnt(0)
	v_mul_f32_e32 v15, v204, v15
	ds_read_b128 v[10:13], v144 offset:544
	v_fmac_f32_e32 v15, v205, v14
	v_fmac_f32_e32 v15, v203, v16
	v_fmac_f32_e32 v15, v202, v17
	v_add_f32_e32 v19, v19, v15
	ds_read_b128 v[14:17], v144 offset:560
	s_waitcnt lgkmcnt(1)
	v_mul_f32_e32 v11, v200, v11
	v_fmac_f32_e32 v11, v201, v10
	v_fmac_f32_e32 v11, v199, v12
	v_fmac_f32_e32 v11, v198, v13
	v_add_f32_e32 v10, v19, v11
	s_waitcnt lgkmcnt(0)
	v_mul_f32_e32 v11, v195, v15
	v_fmac_f32_e32 v11, v196, v14
	v_fmac_f32_e32 v11, v194, v16
	v_fmac_f32_e32 v11, v193, v17
	v_add_f32_e32 v10, v10, v11
	v_mul_f32_e64 v11, |v10|, s81
	v_exp_f32_e32 v11, v11
	v_mul_f32_e32 v9, 0x3f317217, v18
	v_fma_f32 v9, v18, s83, -v9
	v_fmac_f32_e32 v9, 0x3377d1cf, v18
	v_fmac_f32_e32 v9, 0x3f317217, v18
	v_cmp_lt_f32_e64 s[0:1], |v18|, s84
	v_add_f32_e32 v11, 1.0, v11
	v_cndmask_b32_e32 v12, 0, v192, vcc
	v_cndmask_b32_e64 v9, v18, v9, s[0:1]
	v_cmp_gt_f32_e32 vcc, s82, v11
	v_sub_f32_e32 v9, v9, v12
	v_sub_f32_e32 v0, v0, v9
	v_cndmask_b32_e64 v12, 0, 32, vcc
	v_ldexp_f32 v11, v11, v12
	v_log_f32_e32 v18, v11
	v_fmamk_f32 v9, v0, 0x3d800000, v8
	v_min_f32_e32 v0, 0, v10
	ds_read_b128 v[10:13], v144 offset:576
	v_mul_f32_e32 v14, 0x3f317217, v18
	v_fma_f32 v19, v18, s83, -v14
	ds_read_b128 v[14:17], v144 offset:592
	v_fmac_f32_e32 v19, 0x3377d1cf, v18
	s_waitcnt lgkmcnt(1)
	v_mul_f32_e32 v11, v209, v11
	v_fmac_f32_e32 v11, v208, v10
	v_fmac_f32_e32 v11, v207, v12
	v_fmac_f32_e32 v11, v206, v13
	v_add_f32_e32 v20, v197, v11
	s_waitcnt lgkmcnt(0)
	v_mul_f32_e32 v15, v204, v15
	ds_read_b128 v[10:13], v144 offset:608
	v_fmac_f32_e32 v15, v205, v14
	v_fmac_f32_e32 v15, v203, v16
	v_fmac_f32_e32 v15, v202, v17
	v_add_f32_e32 v20, v20, v15
	ds_read_b128 v[14:17], v144 offset:624
	s_waitcnt lgkmcnt(1)
	v_mul_f32_e32 v11, v200, v11
	v_fmac_f32_e32 v11, v201, v10
	v_fmac_f32_e32 v11, v199, v12
	v_fmac_f32_e32 v11, v198, v13
	v_add_f32_e32 v10, v20, v11
	s_waitcnt lgkmcnt(0)
	v_mul_f32_e32 v11, v195, v15
	v_fmac_f32_e32 v11, v196, v14
	v_fmac_f32_e32 v11, v194, v16
	v_fmac_f32_e32 v11, v193, v17
	v_add_f32_e32 v11, v10, v11
	v_mul_f32_e64 v10, |v11|, s81
	v_exp_f32_e32 v10, v10
	v_fmac_f32_e32 v19, 0x3f317217, v18
	v_cmp_lt_f32_e64 s[0:1], |v18|, s84
	v_cndmask_b32_e32 v13, 0, v192, vcc
	v_add_f32_e32 v10, 1.0, v10
	v_cndmask_b32_e64 v12, v18, v19, s[0:1]
	v_cmp_gt_f32_e32 vcc, s82, v10
	v_sub_f32_e32 v12, v12, v13
	v_sub_f32_e32 v0, v0, v12
	v_cndmask_b32_e64 v13, 0, 32, vcc
	v_ldexp_f32 v10, v10, v13
	ds_read_b128 v[12:15], v144 offset:640
	ds_read_b128 v[16:19], v144 offset:656
	v_log_f32_e32 v20, v10
	v_fmamk_f32 v10, v0, 0x3d800000, v9
	v_min_f32_e32 v0, 0, v11
	s_waitcnt lgkmcnt(1)
	v_mul_f32_e32 v13, v209, v13
	v_fmac_f32_e32 v13, v208, v12
	v_fmac_f32_e32 v13, v207, v14
	v_fmac_f32_e32 v13, v206, v15
	v_add_f32_e32 v21, v197, v13
	s_waitcnt lgkmcnt(0)
	v_mul_f32_e32 v17, v204, v17
	ds_read_b128 v[12:15], v144 offset:672
	v_fmac_f32_e32 v17, v205, v16
	v_fmac_f32_e32 v17, v203, v18
	v_fmac_f32_e32 v17, v202, v19
	v_add_f32_e32 v21, v21, v17
	ds_read_b128 v[16:19], v144 offset:688
	s_waitcnt lgkmcnt(1)
	v_mul_f32_e32 v13, v200, v13
	v_fmac_f32_e32 v13, v201, v12
	v_fmac_f32_e32 v13, v199, v14
	v_fmac_f32_e32 v13, v198, v15
	v_add_f32_e32 v12, v21, v13
	s_waitcnt lgkmcnt(0)
	v_mul_f32_e32 v13, v195, v17
	v_fmac_f32_e32 v13, v196, v16
	v_fmac_f32_e32 v13, v194, v18
	v_fmac_f32_e32 v13, v193, v19
	v_add_f32_e32 v12, v12, v13
	v_mul_f32_e64 v13, |v12|, s81
	v_exp_f32_e32 v13, v13
	v_mul_f32_e32 v11, 0x3f317217, v20
	v_fma_f32 v11, v20, s83, -v11
	v_fmac_f32_e32 v11, 0x3377d1cf, v20
	v_fmac_f32_e32 v11, 0x3f317217, v20
	v_cmp_lt_f32_e64 s[0:1], |v20|, s84
	v_add_f32_e32 v13, 1.0, v13
	v_cndmask_b32_e32 v14, 0, v192, vcc
	v_cndmask_b32_e64 v11, v20, v11, s[0:1]
	v_cmp_gt_f32_e32 vcc, s82, v13
	v_sub_f32_e32 v11, v11, v14
	v_sub_f32_e32 v0, v0, v11
	v_cndmask_b32_e64 v14, 0, 32, vcc
	v_ldexp_f32 v13, v13, v14
	v_log_f32_e32 v20, v13
	v_fmamk_f32 v11, v0, 0x3d800000, v10
	v_min_f32_e32 v0, 0, v12
	ds_read_b128 v[12:15], v144 offset:704
	v_mul_f32_e32 v16, 0x3f317217, v20
	v_fma_f32 v21, v20, s83, -v16
	ds_read_b128 v[16:19], v144 offset:720
	v_fmac_f32_e32 v21, 0x3377d1cf, v20
	s_waitcnt lgkmcnt(1)
	v_mul_f32_e32 v13, v209, v13
	v_fmac_f32_e32 v13, v208, v12
	v_fmac_f32_e32 v13, v207, v14
	v_fmac_f32_e32 v13, v206, v15
	v_add_f32_e32 v22, v197, v13
	s_waitcnt lgkmcnt(0)
	v_mul_f32_e32 v17, v204, v17
	ds_read_b128 v[12:15], v144 offset:736
	v_fmac_f32_e32 v17, v205, v16
	v_fmac_f32_e32 v17, v203, v18
	v_fmac_f32_e32 v17, v202, v19
	v_add_f32_e32 v22, v22, v17
	ds_read_b128 v[16:19], v144 offset:752
	s_waitcnt lgkmcnt(1)
	v_mul_f32_e32 v13, v200, v13
	v_fmac_f32_e32 v13, v201, v12
	v_fmac_f32_e32 v13, v199, v14
	v_fmac_f32_e32 v13, v198, v15
	v_add_f32_e32 v12, v22, v13
	s_waitcnt lgkmcnt(0)
	v_mul_f32_e32 v13, v195, v17
	v_fmac_f32_e32 v13, v196, v16
	v_fmac_f32_e32 v13, v194, v18
	v_fmac_f32_e32 v13, v193, v19
	v_add_f32_e32 v13, v12, v13
	v_mul_f32_e64 v12, |v13|, s81
	v_exp_f32_e32 v12, v12
	v_fmac_f32_e32 v21, 0x3f317217, v20
	v_cmp_lt_f32_e64 s[0:1], |v20|, s84
	v_cndmask_b32_e32 v15, 0, v192, vcc
	v_add_f32_e32 v12, 1.0, v12
	v_cndmask_b32_e64 v14, v20, v21, s[0:1]
	v_cmp_gt_f32_e32 vcc, s82, v12
	v_sub_f32_e32 v14, v14, v15
	v_sub_f32_e32 v0, v0, v14
	v_cndmask_b32_e64 v15, 0, 32, vcc
	v_ldexp_f32 v12, v12, v15
	ds_read_b128 v[14:17], v144 offset:768
	ds_read_b128 v[18:21], v144 offset:784
	v_log_f32_e32 v22, v12
	v_fmamk_f32 v12, v0, 0x3d800000, v11
	v_min_f32_e32 v0, 0, v13
	s_waitcnt lgkmcnt(1)
	v_mul_f32_e32 v15, v209, v15
	v_fmac_f32_e32 v15, v208, v14
	v_fmac_f32_e32 v15, v207, v16
	v_fmac_f32_e32 v15, v206, v17
	v_add_f32_e32 v23, v197, v15
	s_waitcnt lgkmcnt(0)
	v_mul_f32_e32 v19, v204, v19
	ds_read_b128 v[14:17], v144 offset:800
	v_fmac_f32_e32 v19, v205, v18
	v_fmac_f32_e32 v19, v203, v20
	v_fmac_f32_e32 v19, v202, v21
	v_add_f32_e32 v23, v23, v19
	ds_read_b128 v[18:21], v144 offset:816
	s_waitcnt lgkmcnt(1)
	v_mul_f32_e32 v15, v200, v15
	v_fmac_f32_e32 v15, v201, v14
	v_fmac_f32_e32 v15, v199, v16
	v_fmac_f32_e32 v15, v198, v17
	v_add_f32_e32 v14, v23, v15
	s_waitcnt lgkmcnt(0)
	v_mul_f32_e32 v15, v195, v19
	v_fmac_f32_e32 v15, v196, v18
	v_fmac_f32_e32 v15, v194, v20
	v_fmac_f32_e32 v15, v193, v21
	v_add_f32_e32 v14, v14, v15
	v_mul_f32_e64 v15, |v14|, s81
	v_exp_f32_e32 v15, v15
	v_mul_f32_e32 v13, 0x3f317217, v22
	v_fma_f32 v13, v22, s83, -v13
	v_fmac_f32_e32 v13, 0x3377d1cf, v22
	v_fmac_f32_e32 v13, 0x3f317217, v22
	v_cmp_lt_f32_e64 s[0:1], |v22|, s84
	v_add_f32_e32 v15, 1.0, v15
	v_cndmask_b32_e32 v16, 0, v192, vcc
	v_cndmask_b32_e64 v13, v22, v13, s[0:1]
	v_cmp_gt_f32_e32 vcc, s82, v15
	v_sub_f32_e32 v13, v13, v16
	v_sub_f32_e32 v0, v0, v13
	v_cndmask_b32_e64 v16, 0, 32, vcc
	v_ldexp_f32 v15, v15, v16
	v_log_f32_e32 v22, v15
	v_fmamk_f32 v13, v0, 0x3d800000, v12
	v_min_f32_e32 v0, 0, v14
	ds_read_b128 v[14:17], v144 offset:832
	v_mul_f32_e32 v18, 0x3f317217, v22
	v_fma_f32 v23, v22, s83, -v18
	ds_read_b128 v[18:21], v144 offset:848
	v_fmac_f32_e32 v23, 0x3377d1cf, v22
	s_waitcnt lgkmcnt(1)
	v_mul_f32_e32 v15, v209, v15
	v_fmac_f32_e32 v15, v208, v14
	v_fmac_f32_e32 v15, v207, v16
	v_fmac_f32_e32 v15, v206, v17
	v_add_f32_e32 v24, v197, v15
	s_waitcnt lgkmcnt(0)
	v_mul_f32_e32 v19, v204, v19
	ds_read_b128 v[14:17], v144 offset:864
	v_fmac_f32_e32 v19, v205, v18
	v_fmac_f32_e32 v19, v203, v20
	v_fmac_f32_e32 v19, v202, v21
	v_add_f32_e32 v24, v24, v19
	ds_read_b128 v[18:21], v144 offset:880
	s_waitcnt lgkmcnt(1)
	v_mul_f32_e32 v15, v200, v15
	v_fmac_f32_e32 v15, v201, v14
	v_fmac_f32_e32 v15, v199, v16
	v_fmac_f32_e32 v15, v198, v17
	v_add_f32_e32 v14, v24, v15
	s_waitcnt lgkmcnt(0)
	v_mul_f32_e32 v15, v195, v19
	v_fmac_f32_e32 v15, v196, v18
	v_fmac_f32_e32 v15, v194, v20
	v_fmac_f32_e32 v15, v193, v21
	v_add_f32_e32 v14, v14, v15
	v_mul_f32_e64 v15, |v14|, s81
	v_exp_f32_e32 v15, v15
	v_fmac_f32_e32 v23, 0x3f317217, v22
	v_cmp_lt_f32_e64 s[0:1], |v22|, s84
	v_cndmask_b32_e32 v17, 0, v192, vcc
	v_add_f32_e32 v15, 1.0, v15
	v_cndmask_b32_e64 v16, v22, v23, s[0:1]
	v_cmp_gt_f32_e32 vcc, s82, v15
	v_sub_f32_e32 v16, v16, v17
	v_sub_f32_e32 v0, v0, v16
	v_cndmask_b32_e64 v17, 0, 32, vcc
	v_ldexp_f32 v15, v15, v17
	v_log_f32_e32 v22, v15
	v_min_f32_e32 v23, 0, v14
	ds_read_b128 v[14:17], v144 offset:896
	v_fmamk_f32 v0, v0, 0x3d800000, v13
	v_mul_f32_e32 v18, 0x3f317217, v22
	v_fma_f32 v24, v22, s83, -v18
	ds_read_b128 v[18:21], v144 offset:912
	s_waitcnt lgkmcnt(1)
	v_mul_f32_e32 v15, v209, v15
	v_fmac_f32_e32 v15, v208, v14
	v_fmac_f32_e32 v15, v207, v16
	v_fmac_f32_e32 v15, v206, v17
	v_add_f32_e32 v25, v197, v15
	s_waitcnt lgkmcnt(0)
	v_mul_f32_e32 v19, v204, v19
	ds_read_b128 v[14:17], v144 offset:928
	v_fmac_f32_e32 v19, v205, v18
	v_fmac_f32_e32 v19, v203, v20
	v_fmac_f32_e32 v19, v202, v21
	v_add_f32_e32 v25, v25, v19
	ds_read_b128 v[18:21], v144 offset:944
	s_waitcnt lgkmcnt(1)
	v_mul_f32_e32 v15, v200, v15
	v_fmac_f32_e32 v15, v201, v14
	v_fmac_f32_e32 v15, v199, v16
	v_fmac_f32_e32 v15, v198, v17
	v_add_f32_e32 v14, v25, v15
	s_waitcnt lgkmcnt(0)
	v_mul_f32_e32 v15, v195, v19
	v_fmac_f32_e32 v15, v196, v18
	v_fmac_f32_e32 v15, v194, v20
	v_fmac_f32_e32 v15, v193, v21
	v_add_f32_e32 v14, v14, v15
	v_mul_f32_e64 v15, |v14|, s81
	v_exp_f32_e32 v15, v15
	v_fmac_f32_e32 v24, 0x3377d1cf, v22
	v_fmac_f32_e32 v24, 0x3f317217, v22
	v_cmp_lt_f32_e64 s[0:1], |v22|, s84
	v_add_f32_e32 v15, 1.0, v15
	v_cndmask_b32_e32 v17, 0, v192, vcc
	v_cndmask_b32_e64 v16, v22, v24, s[0:1]
	v_cmp_gt_f32_e32 vcc, s82, v15
	v_sub_f32_e32 v16, v16, v17
	v_min_f32_e32 v24, 0, v14
	v_cndmask_b32_e64 v17, 0, 32, vcc
	v_ldexp_f32 v15, v15, v17
	v_log_f32_e32 v22, v15
	v_sub_f32_e32 v15, v23, v16
	v_fmamk_f32 v23, v15, 0x3d800000, v0
	ds_read_b128 v[14:17], v144 offset:960
	v_mul_f32_e32 v18, 0x3f317217, v22
	v_fma_f32 v25, v22, s83, -v18
	ds_read_b128 v[18:21], v144 offset:976
	v_fmac_f32_e32 v25, 0x3377d1cf, v22
	s_waitcnt lgkmcnt(1)
	v_mul_f32_e32 v15, v209, v15
	v_fmac_f32_e32 v15, v208, v14
	v_fmac_f32_e32 v15, v207, v16
	v_fmac_f32_e32 v15, v206, v17
	v_add_f32_e32 v26, v197, v15
	s_waitcnt lgkmcnt(0)
	v_mul_f32_e32 v19, v204, v19
	ds_read_b128 v[14:17], v144 offset:992
	v_fmac_f32_e32 v19, v205, v18
	v_fmac_f32_e32 v19, v203, v20
	v_fmac_f32_e32 v19, v202, v21
	v_add_f32_e32 v26, v26, v19
	ds_read_b128 v[18:21], v144 offset:1008
	s_waitcnt lgkmcnt(1)
	v_mul_f32_e32 v15, v200, v15
	v_fmac_f32_e32 v15, v201, v14
	v_fmac_f32_e32 v15, v199, v16
	v_fmac_f32_e32 v15, v198, v17
	v_add_f32_e32 v14, v26, v15
	s_waitcnt lgkmcnt(0)
	v_mul_f32_e32 v15, v195, v19
	v_fmac_f32_e32 v15, v196, v18
	v_fmac_f32_e32 v15, v194, v20
	v_fmac_f32_e32 v15, v193, v21
	v_add_f32_e32 v14, v14, v15
	v_mul_f32_e64 v15, |v14|, s81
	v_exp_f32_e32 v15, v15
	v_fmac_f32_e32 v25, 0x3f317217, v22
	v_cmp_lt_f32_e64 s[0:1], |v22|, s84
	v_cndmask_b32_e32 v17, 0, v192, vcc
	v_add_f32_e32 v15, 1.0, v15
	v_cndmask_b32_e64 v16, v22, v25, s[0:1]
	v_cmp_gt_f32_e32 vcc, s82, v15
	v_sub_f32_e32 v16, v16, v17
	v_sub_f32_e32 v16, v24, v16
	v_cndmask_b32_e64 v17, 0, 32, vcc
	v_ldexp_f32 v15, v15, v17
	v_log_f32_e32 v15, v15
	v_fmamk_f32 v18, v16, 0x3d800000, v23
	v_min_f32_e32 v14, 0, v14
	v_mul_f32_e32 v16, 0x3f317217, v15
	v_fma_f32 v16, v15, s83, -v16
	v_fmac_f32_e32 v16, 0x3377d1cf, v15
	v_fmac_f32_e32 v16, 0x3f317217, v15
	v_cmp_lt_f32_e64 s[0:1], |v15|, s84
	s_nop 1
	v_cndmask_b32_e64 v15, v15, v16, s[0:1]
	v_cndmask_b32_e32 v16, 0, v192, vcc
	v_sub_f32_e32 v15, v15, v16
	v_sub_f32_e32 v14, v14, v15
	v_fmamk_f32 v19, v14, 0x3d800000, v18
	ds_write_b32 v145, v19
	s_waitcnt lgkmcnt(0)
	s_barrier
	ds_read2st64_b32 v[14:15], v146 offset1:2
	ds_read2st64_b32 v[16:17], v146 offset0:4 offset1:6
	v_readlane_b32 s0, v253, 4
	v_readlane_b32 s1, v253, 5
	s_waitcnt lgkmcnt(1)
	v_add_f32_e32 v14, 0, v14
	v_cndmask_b32_e64 v14, 0, v14, s[0:1]
	v_add_f32_e32 v15, v15, v14
	v_cndmask_b32_e64 v14, v14, v15, s[6:7]
	v_readlane_b32 s0, v253, 6
	s_waitcnt lgkmcnt(0)
	v_add_f32_e32 v15, v16, v14
	v_readlane_b32 s1, v253, 7
	s_nop 1
	v_cndmask_b32_e64 v14, v14, v15, s[0:1]
	v_add_f32_e32 v15, v17, v14
	v_cndmask_b32_e64 v14, v14, v15, s[74:75]
	v_add_f32_e32 v2, v2, v14
	ds_read_u16 v15, v180
	ds_read_u16 v16, v180 offset:16384
	v_mul_f32_e32 v17, 0x3fb8aa3b, v2
	v_exp_f32_e32 v17, v17
	v_mul_f32_e32 v2, 0xbfb8aa3b, v2
	v_exp_f32_e32 v2, v2
	s_waitcnt lgkmcnt(1)
	v_lshlrev_b32_e32 v15, 16, v15
	v_mul_f32_e32 v15, v17, v15
	s_waitcnt lgkmcnt(0)
	v_lshlrev_b32_e32 v16, 16, v16
	v_cvt_pk_bf16_f32 v15, v15, s0
	s_add_i32 s0, 0, 0x14000
	v_add_u32_e32 v17, s0, v151
	v_mul_f32_e32 v2, v2, v16
	ds_write_b16 v17, v15
	v_cvt_pk_bf16_f32 v2, v2, s0
	v_add_u32_e32 v15, s85, v151
	v_add_f32_e32 v3, v3, v14
	ds_write_b16 v15, v2
	ds_read_u16 v2, v180 offset:256
	ds_read_u16 v15, v180 offset:16640
	v_mul_f32_e32 v16, 0x3fb8aa3b, v3
	v_exp_f32_e32 v16, v16
	v_mul_f32_e32 v3, 0xbfb8aa3b, v3
	v_exp_f32_e32 v3, v3
	s_waitcnt lgkmcnt(1)
	v_lshlrev_b32_e32 v2, 16, v2
	v_mul_f32_e32 v2, v16, v2
	s_waitcnt lgkmcnt(0)
	v_lshlrev_b32_e32 v15, 16, v15
	v_cvt_pk_bf16_f32 v2, v2, s0
	v_add_u32_e32 v16, s0, v152
	ds_write_b16 v16, v2
	v_mul_f32_e32 v2, v3, v15
	v_cvt_pk_bf16_f32 v2, v2, s0
	v_add_u32_e32 v3, s85, v152
	v_add_f32_e32 v4, v4, v14
	ds_write_b16 v3, v2
	ds_read_u16 v2, v180 offset:512
	ds_read_u16 v3, v180 offset:16896
	v_mul_f32_e32 v15, 0x3fb8aa3b, v4
	v_exp_f32_e32 v15, v15
	v_mul_f32_e32 v4, 0xbfb8aa3b, v4
	v_exp_f32_e32 v4, v4
	s_waitcnt lgkmcnt(1)
	v_lshlrev_b32_e32 v2, 16, v2
	v_mul_f32_e32 v2, v15, v2
	s_waitcnt lgkmcnt(0)
	v_lshlrev_b32_e32 v3, 16, v3
	v_cvt_pk_bf16_f32 v2, v2, s0
	v_add_u32_e32 v15, s0, v153
	ds_write_b16 v15, v2
	v_mul_f32_e32 v2, v4, v3
	v_cvt_pk_bf16_f32 v2, v2, s0
	v_add_u32_e32 v3, s85, v153
	v_add_f32_e32 v5, v5, v14
	ds_write_b16 v3, v2
	ds_read_u16 v2, v180 offset:768
	ds_read_u16 v3, v180 offset:17152
	v_mul_f32_e32 v4, 0x3fb8aa3b, v5
	v_exp_f32_e32 v4, v4
	v_add_f32_e32 v6, v6, v14
	s_waitcnt lgkmcnt(1)
	v_lshlrev_b32_e32 v2, 16, v2
	s_waitcnt lgkmcnt(0)
	v_lshlrev_b32_e32 v3, 16, v3
	v_mul_f32_e32 v2, v4, v2
	v_mul_f32_e32 v4, 0xbfb8aa3b, v5
	v_exp_f32_e32 v4, v4
	v_cvt_pk_bf16_f32 v2, v2, s0
	v_add_u32_e32 v5, s0, v154
	ds_write_b16 v5, v2
	v_mul_f32_e32 v2, v4, v3
	v_cvt_pk_bf16_f32 v2, v2, s0
	v_add_u32_e32 v3, s85, v154
	ds_write_b16 v3, v2
	ds_read_u16 v2, v180 offset:1024
	ds_read_u16 v3, v180 offset:17408
	v_mul_f32_e32 v4, 0x3fb8aa3b, v6
	v_exp_f32_e32 v4, v4
	v_add_f32_e32 v5, v7, v14
	s_waitcnt lgkmcnt(1)
	v_lshlrev_b32_e32 v2, 16, v2
	s_waitcnt lgkmcnt(0)
	v_lshlrev_b32_e32 v3, 16, v3
	v_mul_f32_e32 v2, v4, v2
	v_mul_f32_e32 v4, 0xbfb8aa3b, v6
	v_exp_f32_e32 v4, v4
	v_cvt_pk_bf16_f32 v2, v2, s0
	v_add_u32_e32 v6, s0, v155
	ds_write_b16 v6, v2
	v_mul_f32_e32 v2, v4, v3
	v_cvt_pk_bf16_f32 v2, v2, s0
	v_add_u32_e32 v3, s85, v155
	ds_write_b16 v3, v2
	ds_read_u16 v2, v180 offset:1280
	ds_read_u16 v3, v180 offset:17664
	v_mul_f32_e32 v4, 0x3fb8aa3b, v5
	v_exp_f32_e32 v4, v4
	v_add_f32_e32 v6, v8, v14
	s_waitcnt lgkmcnt(1)
	v_lshlrev_b32_e32 v2, 16, v2
	s_waitcnt lgkmcnt(0)
	v_lshlrev_b32_e32 v3, 16, v3
	v_mul_f32_e32 v2, v4, v2
	v_mul_f32_e32 v4, 0xbfb8aa3b, v5
	v_exp_f32_e32 v4, v4
	v_cvt_pk_bf16_f32 v2, v2, s0
	v_add_u32_e32 v5, s0, v156
	ds_write_b16 v5, v2
	v_mul_f32_e32 v2, v4, v3
	v_cvt_pk_bf16_f32 v2, v2, s0
	v_add_u32_e32 v3, s85, v156
	ds_write_b16 v3, v2
	ds_read_u16 v2, v180 offset:1536
	ds_read_u16 v3, v180 offset:17920
	v_mul_f32_e32 v4, 0x3fb8aa3b, v6
	v_exp_f32_e32 v4, v4
	v_add_f32_e32 v5, v9, v14
	s_waitcnt lgkmcnt(1)
	v_lshlrev_b32_e32 v2, 16, v2
	s_waitcnt lgkmcnt(0)
	v_lshlrev_b32_e32 v3, 16, v3
	v_mul_f32_e32 v2, v4, v2
	v_mul_f32_e32 v4, 0xbfb8aa3b, v6
	v_exp_f32_e32 v4, v4
	v_cvt_pk_bf16_f32 v2, v2, s0
	v_add_u32_e32 v6, s0, v157
	ds_write_b16 v6, v2
	v_mul_f32_e32 v2, v4, v3
	v_cvt_pk_bf16_f32 v2, v2, s0
	v_add_u32_e32 v3, s85, v157
	ds_write_b16 v3, v2
	ds_read_u16 v2, v180 offset:1792
	ds_read_u16 v3, v180 offset:18176
	v_mul_f32_e32 v4, 0x3fb8aa3b, v5
	v_exp_f32_e32 v4, v4
	v_add_f32_e32 v6, v10, v14
	s_waitcnt lgkmcnt(1)
	v_lshlrev_b32_e32 v2, 16, v2
	s_waitcnt lgkmcnt(0)
	v_lshlrev_b32_e32 v3, 16, v3
	v_mul_f32_e32 v2, v4, v2
	v_mul_f32_e32 v4, 0xbfb8aa3b, v5
	v_exp_f32_e32 v4, v4
	v_cvt_pk_bf16_f32 v2, v2, s0
	v_add_u32_e32 v5, s0, v158
	ds_write_b16 v5, v2
	v_mul_f32_e32 v2, v4, v3
	v_cvt_pk_bf16_f32 v2, v2, s0
	v_add_u32_e32 v3, s85, v158
	ds_write_b16 v3, v2
	ds_read_u16 v2, v180 offset:2048
	ds_read_u16 v3, v180 offset:18432
	v_mul_f32_e32 v4, 0x3fb8aa3b, v6
	v_exp_f32_e32 v4, v4
	v_add_f32_e32 v5, v11, v14
	s_waitcnt lgkmcnt(1)
	v_lshlrev_b32_e32 v2, 16, v2
	s_waitcnt lgkmcnt(0)
	v_lshlrev_b32_e32 v3, 16, v3
	v_mul_f32_e32 v2, v4, v2
	v_mul_f32_e32 v4, 0xbfb8aa3b, v6
	v_exp_f32_e32 v4, v4
	v_cvt_pk_bf16_f32 v2, v2, s0
	v_add_u32_e32 v6, s0, v159
	ds_write_b16 v6, v2
	v_mul_f32_e32 v2, v4, v3
	v_cvt_pk_bf16_f32 v2, v2, s0
	v_add_u32_e32 v3, s85, v159
	ds_write_b16 v3, v2
	ds_read_u16 v2, v180 offset:2304
	ds_read_u16 v3, v180 offset:18688
	v_mul_f32_e32 v4, 0x3fb8aa3b, v5
	v_exp_f32_e32 v4, v4
	v_add_f32_e32 v6, v12, v14
	s_waitcnt lgkmcnt(1)
	v_lshlrev_b32_e32 v2, 16, v2
	s_waitcnt lgkmcnt(0)
	v_lshlrev_b32_e32 v3, 16, v3
	v_mul_f32_e32 v2, v4, v2
	v_mul_f32_e32 v4, 0xbfb8aa3b, v5
	v_exp_f32_e32 v4, v4
	v_cvt_pk_bf16_f32 v2, v2, s0
	v_add_u32_e32 v5, s0, v160
	ds_write_b16 v5, v2
	v_mul_f32_e32 v2, v4, v3
	v_cvt_pk_bf16_f32 v2, v2, s0
	v_add_u32_e32 v3, s85, v160
	ds_write_b16 v3, v2
	ds_read_u16 v2, v180 offset:2560
	ds_read_u16 v3, v180 offset:18944
	v_mul_f32_e32 v4, 0x3fb8aa3b, v6
	v_exp_f32_e32 v4, v4
	v_add_f32_e32 v5, v13, v14
	s_waitcnt lgkmcnt(1)
	v_lshlrev_b32_e32 v2, 16, v2
	s_waitcnt lgkmcnt(0)
	v_lshlrev_b32_e32 v3, 16, v3
	v_mul_f32_e32 v2, v4, v2
	v_mul_f32_e32 v4, 0xbfb8aa3b, v6
	v_exp_f32_e32 v4, v4
	v_cvt_pk_bf16_f32 v2, v2, s0
	v_add_u32_e32 v6, s0, v161
	ds_write_b16 v6, v2
	v_mul_f32_e32 v2, v4, v3
	v_cvt_pk_bf16_f32 v2, v2, s0
	v_add_u32_e32 v3, s85, v161
	ds_write_b16 v3, v2
	ds_read_u16 v2, v180 offset:2816
	ds_read_u16 v3, v180 offset:19200
	v_mul_f32_e32 v4, 0x3fb8aa3b, v5
	v_exp_f32_e32 v4, v4
	v_add_f32_e32 v0, v0, v14
	s_waitcnt lgkmcnt(1)
	v_lshlrev_b32_e32 v2, 16, v2
	s_waitcnt lgkmcnt(0)
	v_lshlrev_b32_e32 v3, 16, v3
	v_mul_f32_e32 v2, v4, v2
	v_mul_f32_e32 v4, 0xbfb8aa3b, v5
	v_exp_f32_e32 v4, v4
	v_cvt_pk_bf16_f32 v2, v2, s0
	v_add_u32_e32 v5, s0, v162
	ds_write_b16 v5, v2
	v_mul_f32_e32 v2, v4, v3
	v_cvt_pk_bf16_f32 v2, v2, s0
	v_add_u32_e32 v3, s85, v162
	ds_write_b16 v3, v2
	ds_read_u16 v2, v180 offset:3072
	ds_read_u16 v3, v180 offset:19456
	v_mul_f32_e32 v4, 0x3fb8aa3b, v0
	v_exp_f32_e32 v4, v4
	v_mul_f32_e32 v0, 0xbfb8aa3b, v0
	v_exp_f32_e32 v0, v0
	s_waitcnt lgkmcnt(1)
	v_lshlrev_b32_e32 v2, 16, v2
	s_waitcnt lgkmcnt(0)
	v_lshlrev_b32_e32 v3, 16, v3
	v_mul_f32_e32 v2, v4, v2
	v_cvt_pk_bf16_f32 v2, v2, s0
	v_add_u32_e32 v4, s0, v163
	v_mul_f32_e32 v0, v0, v3
	ds_write_b16 v4, v2
	v_cvt_pk_bf16_f32 v0, v0, s0
	v_add_u32_e32 v2, s85, v163
	v_add_f32_e32 v5, v23, v14
	ds_write_b16 v2, v0
	ds_read_u16 v0, v180 offset:3328
	ds_read_u16 v2, v180 offset:19712
	v_mul_f32_e32 v3, 0x3fb8aa3b, v5
	v_exp_f32_e32 v3, v3
	v_add_f32_e32 v4, v18, v14
	s_waitcnt lgkmcnt(1)
	v_lshlrev_b32_e32 v0, 16, v0
	s_waitcnt lgkmcnt(0)
	v_lshlrev_b32_e32 v2, 16, v2
	v_mul_f32_e32 v0, v3, v0
	v_mul_f32_e32 v3, 0xbfb8aa3b, v5
	v_exp_f32_e32 v3, v3
	v_cvt_pk_bf16_f32 v0, v0, s0
	v_add_u32_e32 v5, s0, v164
	ds_write_b16 v5, v0
	v_mul_f32_e32 v0, v3, v2
	v_cvt_pk_bf16_f32 v0, v0, s0
	v_add_u32_e32 v2, s85, v164
	ds_write_b16 v2, v0
	ds_read_u16 v0, v180 offset:3584
	ds_read_u16 v2, v180 offset:19968
	v_mul_f32_e32 v3, 0x3fb8aa3b, v4
	v_exp_f32_e32 v3, v3
	v_add_f32_e32 v5, v14, v19
	s_waitcnt lgkmcnt(1)
	v_lshlrev_b32_e32 v0, 16, v0
	s_waitcnt lgkmcnt(0)
	v_lshlrev_b32_e32 v2, 16, v2
	v_mul_f32_e32 v0, v3, v0
	v_mul_f32_e32 v3, 0xbfb8aa3b, v4
	v_exp_f32_e32 v3, v3
	v_cvt_pk_bf16_f32 v0, v0, s0
	v_add_u32_e32 v4, s0, v165
	ds_write_b16 v4, v0
	v_mul_f32_e32 v0, v3, v2
	v_cvt_pk_bf16_f32 v0, v0, s0
	v_add_u32_e32 v2, s85, v165
	ds_write_b16 v2, v0
	ds_read_u16 v0, v180 offset:3840
	ds_read_u16 v2, v180 offset:20224
	v_mul_f32_e32 v3, 0x3fb8aa3b, v5
	v_exp_f32_e32 v3, v3
	v_add_u32_e32 v4, s0, v166
	s_waitcnt lgkmcnt(1)
	v_lshlrev_b32_e32 v0, 16, v0
	s_waitcnt lgkmcnt(0)
	v_lshlrev_b32_e32 v2, 16, v2
	v_mul_f32_e32 v0, v3, v0
	v_mul_f32_e32 v3, 0xbfb8aa3b, v5
	v_exp_f32_e32 v3, v3
	v_cvt_pk_bf16_f32 v0, v0, s0
	ds_write_b16 v4, v0
	s_and_b32 s1, s36, 0xfc0
	v_mul_f32_e32 v0, v3, v2
	v_cvt_pk_bf16_f32 v0, v0, s0
	v_add_u32_e32 v2, s85, v166
	ds_write_b16 v2, v0
	ds_read_u16 v0, v181 offset:32768
	ds_read_u16 v3, v181 offset:33792
	ds_read_u16 v4, v181 offset:34816
	ds_read_u16 v5, v181 offset:35328
	ds_read_u16 v6, v181 offset:35840
	ds_read_u16 v7, v181 offset:34304
	ds_read_u16 v2, v181 offset:33280
	ds_read_u16 v8, v181 offset:36352
	s_waitcnt lgkmcnt(4)
	v_lshl_or_b32 v4, v5, 16, v4
	s_and_b32 s0, s33, 0x1ff000
	s_waitcnt lgkmcnt(2)
	v_lshl_or_b32 v3, v7, 16, v3
	s_waitcnt lgkmcnt(1)
	v_lshl_or_b32 v2, v2, 16, v0
	s_waitcnt lgkmcnt(0)
	v_lshl_or_b32 v5, v8, 16, v6
	ds_read_u16 v0, v181 offset:36864
	ds_read_u16 v6, v181 offset:37888
	ds_read_u16 v7, v181 offset:38912
	ds_read_u16 v8, v181 offset:39936
	ds_read_u16 v9, v181 offset:40448
	ds_read_u16 v10, v181 offset:39424
	ds_read_u16 v11, v181 offset:38400
	ds_read_u16 v12, v181 offset:37376
	ds_read_u16 v13, v181 offset:40960
	ds_read_u16 v14, v181 offset:41984
	ds_read_u16 v15, v181 offset:43008
	ds_read_u16 v16, v181 offset:44032
	ds_read_u16 v17, v181 offset:44544
	ds_read_u16 v18, v181 offset:43520
	ds_read_u16 v19, v181 offset:42496
	ds_read_u16 v20, v181 offset:41472
	ds_read_u16 v21, v181 offset:45056
	ds_read_u16 v22, v181 offset:46080
	ds_read_u16 v23, v181 offset:47104
	ds_read_u16 v24, v181 offset:48128
	ds_read_u16 v25, v181 offset:48640
	ds_read_u16 v26, v181 offset:47616
	ds_read_u16 v27, v181 offset:46592
	ds_read_u16 v28, v181 offset:45568
	ds_write_b128 v182, v[2:5]
	s_waitcnt lgkmcnt(15)
	v_lshl_or_b32 v2, v12, 16, v0
	v_lshl_or_b32 v3, v11, 16, v6
	v_lshl_or_b32 v4, v10, 16, v7
	v_lshl_or_b32 v5, v9, 16, v8
	ds_write_b128 v183, v[2:5]
	s_waitcnt lgkmcnt(10)
	v_lshl_or_b32 v2, v20, 16, v13
	v_lshl_or_b32 v3, v19, 16, v14
	v_lshl_or_b32 v4, v18, 16, v15
	v_lshl_or_b32 v5, v17, 16, v16
	ds_write_b128 v184, v[2:5]
	s_waitcnt lgkmcnt(3)
	v_lshl_or_b32 v2, v28, 16, v21
	v_lshl_or_b32 v3, v27, 16, v22
	v_lshl_or_b32 v4, v26, 16, v23
	v_lshl_or_b32 v5, v25, 16, v24
	s_or_b32 s0, s0, s1
	ds_write_b128 v185, v[2:5]
	v_lshl_add_u64 v[2:3], s[68:69], 0, v[100:101]
	v_or_b32_e32 v0, s0, v177
	s_waitcnt lgkmcnt(0)
	s_barrier
	global_load_lds_dwordx4 v[2:3], off
	v_lshl_add_u64 v[2:3], s[68:69], 0, v[102:103]
	s_mov_b32 m0, s86
	v_lshlrev_b32_e32 v210, 11, v0
	s_lshl_b32 s0, s37, 9
	global_load_lds_dwordx4 v[2:3], off
	v_lshl_add_u64 v[2:3], s[68:69], 0, v[104:105]
	s_mov_b32 m0, s87
	v_add3_u32 v0, v147, s0, v210
	v_readlane_b32 s0, v252, 6
	global_load_lds_dwordx4 v[2:3], off
	v_lshl_add_u64 v[2:3], s[68:69], 0, v[106:107]
	s_mov_b32 m0, s88
	s_add_i32 s97, s96, s0
	global_load_lds_dwordx4 v[2:3], off
	v_lshl_add_u64 v[2:3], s[68:69], 0, v[108:109]
	s_mov_b32 m0, s89
	s_cmpk_gt_i32 s97, 0x7ff
	global_load_lds_dwordx4 v[2:3], off
	v_lshl_add_u64 v[2:3], s[68:69], 0, v[110:111]
	s_mov_b32 m0, s90
	s_cselect_b64 s[72:73], -1, 0
	s_cmpk_lt_i32 s97, 0x800
	global_load_lds_dwordx4 v[2:3], off
	v_lshl_add_u64 v[2:3], s[68:69], 0, v[112:113]
	s_mov_b32 m0, s91
	v_readlane_b32 s1, v252, 7
	s_cselect_b32 s0, s97, s96
	global_load_lds_dwordx4 v[2:3], off
	v_lshl_add_u64 v[2:3], s[68:69], 0, v[114:115]
	s_mov_b32 m0, s92
	s_lshl_b32 s1, s0, 4
	s_lshl_b32 s44, s0, 6
	global_load_lds_dwordx4 v[2:3], off
	v_or_b32_e32 v2, 32, v0
	v_or_b32_e32 v3, 64, v0
	v_or_b32_e32 v4, 0x60, v0
	s_and_b32 s1, s1, 0xfffff000
	s_and_b32 s44, s44, 0xfc0
	global_load_dwordx2 v[130:131], v0, s[38:39]
	global_load_dwordx2 v[128:129], v2, s[38:39]
	global_load_dwordx2 v[126:127], v3, s[38:39]
	global_load_dwordx2 v[124:125], v4, s[38:39]
	v_or_b32_e32 v2, 0x80, v0
	v_or_b32_e32 v3, 0xa0, v0
	v_or_b32_e32 v4, 0xc0, v0
	v_or_b32_e32 v0, 0xe0, v0
	s_or_b32 vcc_lo, s1, s44
	s_bfe_u32 s96, s0, 0x20006
	global_load_dwordx2 v[122:123], v2, s[38:39]
	global_load_dwordx2 v[120:121], v3, s[38:39]
	global_load_dwordx2 v[118:119], v4, s[38:39]
	global_load_dwordx2 v[116:117], v0, s[38:39]
	v_lshl_or_b32 v0, s96, 8, v132
	v_add_u32_e32 v2, vcc_lo, v1
	v_lshl_or_b32 v6, v2, 10, v0
	v_add_u32_e32 v2, vcc_lo, v133
	v_lshl_or_b32 v0, v2, 10, v0
	s_waitcnt vmcnt(0)
	s_waitcnt vmcnt(0) lgkmcnt(0)
	s_barrier
	global_load_dwordx4 v[2:5], v6, s[28:29]
	s_nop 0
	global_load_dwordx4 v[6:9], v6, s[30:31]
	s_nop 0
	global_load_dwordx4 v[10:13], v0, s[28:29]
	global_load_dwordx4 v[14:17], v0, s[30:31]
	v_lshl_or_b32 v0, s96, 9, v134
	v_add_u32_e32 v18, vcc_lo, v135
	v_add_u32_e32 v19, vcc_lo, v136
	v_add_u32_e32 v26, vcc_lo, v137
	v_lshl_or_b32 v18, v18, 11, v0
	v_lshl_or_b32 v22, v19, 11, v0
	v_lshl_or_b32 v26, v26, 11, v0
	v_add_u32_e32 v27, vcc_lo, v138
	global_load_dwordx4 v[18:21], v18, s[34:35]
	s_nop 0
	global_load_dwordx4 v[22:25], v22, s[34:35]
	v_lshl_or_b32 v0, v27, 11, v0
	global_load_dwordx4 v[26:29], v26, s[34:35]
	s_nop 0
	global_load_dwordx4 v[30:33], v0, s[34:35]
	s_and_saveexec_b64 s[0:1], s[4:5]
	s_cbranch_execz .LBB0_908
	v_add_u32_e32 v0, vcc_lo, v140
	v_lshl_or_b32 v0, v0, 7, v139
	global_load_dwordx4 v[34:37], v0, s[26:27]

.LBB0_910:
	v_mul_f32_e32 v0, v67, v67
	v_mul_f32_e32 v70, v69, v69
	v_fmac_f32_e32 v0, v66, v66
	v_fmac_f32_e32 v70, v68, v68
	v_add_f32_e32 v0, v0, v70
	v_mul_f32_e32 v70, v63, v63
	v_mul_f32_e32 v71, v65, v65
	v_fmac_f32_e32 v70, v62, v62
	v_fmac_f32_e32 v71, v64, v64
	v_add_f32_e32 v70, v70, v71
	v_add_f32_e32 v0, v70, v0
	v_mul_f32_e32 v70, v59, v59
	v_mul_f32_e32 v71, v61, v61
	v_fmac_f32_e32 v70, v58, v58
	v_fmac_f32_e32 v71, v60, v60
	v_add_f32_e32 v70, v70, v71
	v_add_f32_e32 v0, v70, v0
	v_mul_f32_e32 v70, v55, v55
	v_mul_f32_e32 v71, v57, v57
	v_fmac_f32_e32 v70, v54, v54
	v_fmac_f32_e32 v71, v56, v56
	v_add_f32_e32 v70, v70, v71
	v_add_f32_e32 v0, v70, v0
	v_mul_f32_e32 v70, v51, v51
	v_mul_f32_e32 v71, v53, v53
	v_fmac_f32_e32 v70, v50, v50
	v_fmac_f32_e32 v71, v52, v52
	v_add_f32_e32 v70, v70, v71
	v_add_f32_e32 v0, v70, v0
	v_mul_f32_e32 v70, v47, v47
	v_mul_f32_e32 v71, v49, v49
	v_fmac_f32_e32 v70, v46, v46
	v_fmac_f32_e32 v71, v48, v48
	v_add_f32_e32 v70, v70, v71
	v_add_f32_e32 v0, v70, v0
	v_mul_f32_e32 v70, v43, v43
	v_mul_f32_e32 v71, v45, v45
	v_fmac_f32_e32 v70, v42, v42
	v_fmac_f32_e32 v71, v44, v44
	v_add_f32_e32 v70, v70, v71
	v_add_f32_e32 v0, v70, v0
	v_mul_f32_e32 v70, v39, v39
	v_mul_f32_e32 v71, v41, v41
	v_fmac_f32_e32 v70, v38, v38
	v_fmac_f32_e32 v71, v40, v40
	v_add_f32_e32 v70, v70, v71
	v_add_f32_e32 v0, v70, v0
	v_mov_b32_e32 v70, v0
	s_nop 1
	v_permlane16_swap_b32_e32 v0, v70
	v_add_f32_e32 v70, v0, v70
	v_mov_b32_e32 v71, v70
	s_nop 1
	v_permlane32_swap_b32_e32 v70, v71
	s_and_saveexec_b64 s[0:1], s[54:55]
	s_cbranch_execz .LBB0_903
	v_add_f32_e32 v0, v70, v71
	ds_write_b32 v148, v0
	s_waitcnt lgkmcnt(0)
	s_branch .LBB0_903

.LBB0_972:
	s_lshl_b32 s2, s2, 5
	s_and_b32 s10, s2, 0x60
	s_mov_b64 s[2:3], 0x80
	s_add_i32 m0, s17, 0x18000
	v_lshl_add_u64 v[8:9], v[8:9], 0, s[2:3]
	s_lshl_b32 s7, s6, 13
	s_lshl_b32 s11, s10, 7
	s_waitcnt vmcnt(2)
	s_barrier
	global_load_lds_dwordx4 v[8:9], off
	v_lshl_add_u64 v[6:7], v[6:7], 0, s[2:3]
	s_add_i32 m0, s17, 0x1a000
	s_add_i32 s35, s17, 0x8000
	s_add_i32 s36, s17, 0xa000
	global_load_lds_dwordx4 v[6:7], off
	v_lshl_add_u64 v[2:3], v[2:3], 0, s[2:3]
	s_mov_b32 m0, s35
	s_add_u32 s8, s20, 0x80080
	global_load_lds_dwordx4 v[2:3], off
	v_lshl_add_u64 v[2:3], v[4:5], 0, s[2:3]
	s_mov_b32 m0, s36
	s_addc_u32 s9, s21, 0
	global_load_lds_dwordx4 v[2:3], off
	s_add_i32 m0, s17, 0x1c000
	v_lshl_add_u64 v[2:3], s[8:9], 0, v[132:133]
	global_load_lds_dwordx4 v[2:3], off
	v_lshl_add_u64 v[2:3], s[8:9], 0, v[136:137]
	s_add_i32 m0, s17, 0x1e000
	v_and_b32_e32 v0, 15, v10
	global_load_lds_dwordx4 v[2:3], off
	v_lshrrev_b32_e32 v2, 1, v10
	v_and_b32_e32 v2, 24, v2
	v_lshlrev_b32_e32 v3, 1, v2
	v_lshl_or_b32 v1, s6, 6, v0
	v_lshl_or_b32 v0, v0, 6, v3
	v_lshlrev_b32_e32 v3, 2, v10
	v_and_b32_e32 v3, 32, v3
	v_bitop3_b32 v4, v0, s7, v3 bitop3:0xde
	v_bitop3_b32 v152, v0, s11, v3 bitop3:0xde
	v_lshlrev_b32_e32 v0, 15, v11
	v_and_b32_e32 v0, 0xffff0000, v0
	v_or_b32_e32 v153, s10, v2
	v_lshl_add_u32 v0, v12, 12, v0
	v_and_b32_e32 v2, 1, v11
	v_lshl_or_b32 v0, v2, 6, v0
	v_lshl_add_u32 v138, v13, 1, v0
	v_lshlrev_b32_e32 v0, 15, v14
	v_and_b32_e32 v0, 0xffff0000, v0
	s_waitcnt vmcnt(6)
	s_cmpk_lt_u32 s5, 0x100
	v_lshl_add_u32 v0, v15, 12, v0
	v_and_b32_e32 v2, 1, v14
	s_sext_i32_i8 s40, s4
	s_cselect_b64 s[6:7], -1, 0
	v_readlane_b32 s4, v252, 6
	v_lshl_or_b32 v0, v2, 6, v0
	s_add_i32 s38, 0, 0x10000
	s_add_i32 s39, 0, 0x14000
	s_ashr_i32 s37, s4, 31
	v_mov_b32_e32 v139, v133
	v_lshl_add_u32 v140, v16, 1, v0
	v_mov_b32_e32 v141, v133
	v_mov_b64_e32 v[142:143], 0x400
	v_mov_b64_e32 v[144:145], 0x3ff
	v_add_u32_e32 v154, s38, v152
	v_add_u32_e32 v155, s39, v152
	v_add_u32_e32 v156, 0, v4
	s_barrier
	v_readlane_b32 s5, v252, 7
	s_branch .LBB0_975
	s_nop 0
	s_nop 0
	s_nop 0
	s_nop 0
	s_nop 0
	s_nop 0
	s_nop 0
	s_nop 0
	s_nop 0
	s_nop 0
	s_nop 0
	s_nop 0
	s_nop 0

.LBB0_1051:
	s_or_b64 exec, exec, s[2:3]
	s_barrier
	ds_read_b128 v[130:133], v198
	ds_read_b128 v[134:137], v198 offset:16
	s_cmpk_lg_i32 s8, 0x80
	s_cselect_b32 s0, s8, 0x70
	v_readlane_b32 s2, v254, 23
	s_waitcnt lgkmcnt(1)
	v_cvt_pk_bf16_f32 v138, v130, v131
	v_cvt_pk_bf16_f32 v139, v132, v133
	s_waitcnt lgkmcnt(0)
	v_cvt_pk_bf16_f32 v140, v134, v135
	v_cvt_pk_bf16_f32 v141, v136, v137
	v_lshlrev_b32_e32 v142, 16, v138
	v_and_b32_e32 v143, 0xffff0000, v138
	v_pk_add_f32 v[130:131], v[130:131], v[142:143] neg_lo:[0,1] neg_hi:[0,1]
	v_lshlrev_b32_e32 v142, 16, v139
	v_and_b32_e32 v143, 0xffff0000, v139
	v_pk_add_f32 v[132:133], v[132:133], v[142:143] neg_lo:[0,1] neg_hi:[0,1]
	v_mfma_f32_16x16x32_bf16 v[142:145], v[138:141], v[2:5], 0
	v_cvt_pk_bf16_f32 v130, v130, v131
	v_cvt_pk_bf16_f32 v131, v132, v133
	v_lshlrev_b32_e32 v132, 16, v140
	v_and_b32_e32 v133, 0xffff0000, v140
	v_pk_add_f32 v[132:133], v[134:135], v[132:133] neg_lo:[0,1] neg_hi:[0,1]
	v_lshlrev_b32_e32 v134, 16, v141
	v_and_b32_e32 v135, 0xffff0000, v141
	v_pk_add_f32 v[146:147], v[136:137], v[134:135] neg_lo:[0,1] neg_hi:[0,1]
	v_mfma_f32_16x16x32_bf16 v[134:137], v[138:141], v[10:13], v[142:145]
	v_cvt_pk_bf16_f32 v132, v132, v133
	v_cvt_pk_bf16_f32 v133, v146, v147
	s_add_i32 s0, s0, s2
	v_mfma_f32_16x16x32_bf16 v[142:145], v[138:141], v[66:69], 0
	v_readlane_b32 s3, v254, 24
	s_ashr_i32 s1, s0, 31
	s_lshl_b64 s[2:3], s[0:1], 12
	v_mfma_f32_16x16x32_bf16 v[138:141], v[138:141], v[74:77], v[142:145]
	s_nop 3
	ds_read_b128 v[142:145], v198 offset:128
	ds_read_b128 v[146:149], v198 offset:144
	s_or_b32 s0, s0, 1
	s_ashr_i32 s1, s0, 31
	v_mfma_f32_16x16x32_bf16 v[134:137], v[130:133], v[2:5], v[134:137]
	s_lshl_b64 s[0:1], s[0:1], 12
	v_lshl_add_u64 v[186:187], v[166:167], 0, s[0:1]
	v_or_b32_e32 v164, 8, v203
	v_mfma_f32_16x16x32_bf16 v[130:133], v[130:133], v[66:69], v[138:141]
	v_writelane_b32 v253, s8, 6
	v_readlane_b32 s0, v254, 29
	v_readlane_b32 s1, v254, 30
	s_waitcnt lgkmcnt(1)
	v_cvt_pk_bf16_f32 v138, v142, v143
	v_cvt_pk_bf16_f32 v139, v144, v145
	s_waitcnt lgkmcnt(0)
	v_cvt_pk_bf16_f32 v140, v146, v147
	v_cvt_pk_bf16_f32 v141, v148, v149
	v_lshlrev_b32_e32 v150, 16, v138
	v_and_b32_e32 v151, 0xffff0000, v138
	v_pk_add_f32 v[142:143], v[142:143], v[150:151] neg_lo:[0,1] neg_hi:[0,1]
	v_lshlrev_b32_e32 v150, 16, v139
	v_and_b32_e32 v151, 0xffff0000, v139
	v_pk_add_f32 v[144:145], v[144:145], v[150:151] neg_lo:[0,1] neg_hi:[0,1]
	v_mfma_f32_16x16x32_bf16 v[134:137], v[138:141], v[6:9], v[134:137]
	v_cvt_pk_bf16_f32 v142, v142, v143
	v_cvt_pk_bf16_f32 v143, v144, v145
	v_lshlrev_b32_e32 v144, 16, v140
	v_mfma_f32_16x16x32_bf16 v[130:133], v[138:141], v[70:73], v[130:133]
	v_and_b32_e32 v145, 0xffff0000, v140
	v_pk_add_f32 v[144:145], v[146:147], v[144:145] neg_lo:[0,1] neg_hi:[0,1]
	v_lshlrev_b32_e32 v146, 16, v141
	v_and_b32_e32 v147, 0xffff0000, v141
	v_pk_add_f32 v[146:147], v[148:149], v[146:147] neg_lo:[0,1] neg_hi:[0,1]
	v_cvt_pk_bf16_f32 v144, v144, v145
	v_mfma_f32_16x16x32_bf16 v[134:137], v[138:141], v[14:17], v[134:137]
	v_cvt_pk_bf16_f32 v145, v146, v147
	v_or_b32_e32 v218, 0x50, v203
	v_or_b32_e32 v219, 0x54, v203
	v_mfma_f32_16x16x32_bf16 v[130:133], v[138:141], v[78:81], v[130:133]
	ds_read_b128 v[138:141], v198 offset:256
	ds_read_b128 v[146:149], v198 offset:272
	v_or_b32_e32 v220, 0x58, v203
	v_or_b32_e32 v221, 0x5c, v203
	v_mfma_f32_16x16x32_bf16 v[134:137], v[142:145], v[6:9], v[134:137]
	v_or_b32_e32 v222, 0x60, v203
	v_or_b32_e32 v223, 0x64, v203
	v_or_b32_e32 v224, 0x68, v203
	v_mfma_f32_16x16x32_bf16 v[130:133], v[142:145], v[70:73], v[130:133]
	s_waitcnt lgkmcnt(1)
	v_cvt_pk_bf16_f32 v142, v138, v139
	v_cvt_pk_bf16_f32 v143, v140, v141
	s_waitcnt lgkmcnt(0)
	v_cvt_pk_bf16_f32 v144, v146, v147
	v_cvt_pk_bf16_f32 v145, v148, v149
	v_lshlrev_b32_e32 v150, 16, v142
	v_and_b32_e32 v151, 0xffff0000, v142
	v_pk_add_f32 v[138:139], v[138:139], v[150:151] neg_lo:[0,1] neg_hi:[0,1]
	v_lshlrev_b32_e32 v150, 16, v143
	v_and_b32_e32 v151, 0xffff0000, v143
	v_pk_add_f32 v[140:141], v[140:141], v[150:151] neg_lo:[0,1] neg_hi:[0,1]
	v_mfma_f32_16x16x32_bf16 v[134:137], v[142:145], v[18:21], v[134:137]
	v_cvt_pk_bf16_f32 v138, v138, v139
	v_cvt_pk_bf16_f32 v139, v140, v141
	v_lshlrev_b32_e32 v140, 16, v144
	v_mfma_f32_16x16x32_bf16 v[130:133], v[142:145], v[82:85], v[130:133]
	v_and_b32_e32 v141, 0xffff0000, v144
	v_pk_add_f32 v[140:141], v[146:147], v[140:141] neg_lo:[0,1] neg_hi:[0,1]
	v_lshlrev_b32_e32 v146, 16, v145
	v_and_b32_e32 v147, 0xffff0000, v145
	v_pk_add_f32 v[146:147], v[148:149], v[146:147] neg_lo:[0,1] neg_hi:[0,1]
	v_cvt_pk_bf16_f32 v140, v140, v141
	v_mfma_f32_16x16x32_bf16 v[134:137], v[142:145], v[26:29], v[134:137]
	v_cvt_pk_bf16_f32 v141, v146, v147
	v_or_b32_e32 v225, 0x6c, v203
	v_or_b32_e32 v226, 0x70, v203
	v_mfma_f32_16x16x32_bf16 v[130:133], v[142:145], v[90:93], v[130:133]
	ds_read_b128 v[142:145], v198 offset:384
	ds_read_b128 v[146:149], v198 offset:400
	v_or_b32_e32 v227, 0x74, v203
	v_or_b32_e32 v228, 0x78, v203
	v_mfma_f32_16x16x32_bf16 v[134:137], v[138:141], v[18:21], v[134:137]
	v_or_b32_e32 v232, 0x7c, v203
	v_mfma_f32_16x16x32_bf16 v[130:133], v[138:141], v[82:85], v[130:133]
	s_waitcnt lgkmcnt(1)
	v_cvt_pk_bf16_f32 v138, v142, v143
	v_cvt_pk_bf16_f32 v139, v144, v145
	s_waitcnt lgkmcnt(0)
	v_cvt_pk_bf16_f32 v140, v146, v147
	v_cvt_pk_bf16_f32 v141, v148, v149
	v_lshlrev_b32_e32 v150, 16, v138
	v_and_b32_e32 v151, 0xffff0000, v138
	v_pk_add_f32 v[142:143], v[142:143], v[150:151] neg_lo:[0,1] neg_hi:[0,1]
	v_lshlrev_b32_e32 v150, 16, v139
	v_and_b32_e32 v151, 0xffff0000, v139
	v_pk_add_f32 v[144:145], v[144:145], v[150:151] neg_lo:[0,1] neg_hi:[0,1]
	v_mfma_f32_16x16x32_bf16 v[134:137], v[138:141], v[22:25], v[134:137]
	v_cvt_pk_bf16_f32 v142, v142, v143
	v_cvt_pk_bf16_f32 v143, v144, v145
	v_lshlrev_b32_e32 v144, 16, v140
	v_mfma_f32_16x16x32_bf16 v[130:133], v[138:141], v[86:89], v[130:133]
	v_and_b32_e32 v145, 0xffff0000, v140
	v_pk_add_f32 v[144:145], v[146:147], v[144:145] neg_lo:[0,1] neg_hi:[0,1]
	v_lshlrev_b32_e32 v146, 16, v141
	v_and_b32_e32 v147, 0xffff0000, v141
	v_pk_add_f32 v[146:147], v[148:149], v[146:147] neg_lo:[0,1] neg_hi:[0,1]
	v_cvt_pk_bf16_f32 v144, v144, v145
	v_mfma_f32_16x16x32_bf16 v[134:137], v[138:141], v[30:33], v[134:137]
	v_cvt_pk_bf16_f32 v145, v146, v147
	v_mfma_f32_16x16x32_bf16 v[130:133], v[138:141], v[94:97], v[130:133]
	ds_read_b128 v[138:141], v198 offset:512
	ds_read_b128 v[146:149], v198 offset:528
	v_mfma_f32_16x16x32_bf16 v[134:137], v[142:145], v[22:25], v[134:137]
	v_mfma_f32_16x16x32_bf16 v[130:133], v[142:145], v[86:89], v[130:133]
	s_waitcnt lgkmcnt(1)
	v_cvt_pk_bf16_f32 v142, v138, v139
	v_cvt_pk_bf16_f32 v143, v140, v141
	s_waitcnt lgkmcnt(0)
	v_cvt_pk_bf16_f32 v144, v146, v147
	v_cvt_pk_bf16_f32 v145, v148, v149
	v_lshlrev_b32_e32 v150, 16, v142
	v_and_b32_e32 v151, 0xffff0000, v142
	v_pk_add_f32 v[138:139], v[138:139], v[150:151] neg_lo:[0,1] neg_hi:[0,1]
	v_lshlrev_b32_e32 v150, 16, v143
	v_and_b32_e32 v151, 0xffff0000, v143
	v_pk_add_f32 v[140:141], v[140:141], v[150:151] neg_lo:[0,1] neg_hi:[0,1]
	v_mfma_f32_16x16x32_bf16 v[134:137], v[142:145], v[34:37], v[134:137]
	v_cvt_pk_bf16_f32 v138, v138, v139
	v_cvt_pk_bf16_f32 v139, v140, v141
	v_lshlrev_b32_e32 v140, 16, v144
	v_mfma_f32_16x16x32_bf16 v[130:133], v[142:145], v[98:101], v[130:133]
	v_and_b32_e32 v141, 0xffff0000, v144
	v_pk_add_f32 v[140:141], v[146:147], v[140:141] neg_lo:[0,1] neg_hi:[0,1]
	v_lshlrev_b32_e32 v146, 16, v145
	v_and_b32_e32 v147, 0xffff0000, v145
	v_pk_add_f32 v[146:147], v[148:149], v[146:147] neg_lo:[0,1] neg_hi:[0,1]
	v_cvt_pk_bf16_f32 v140, v140, v141
	v_mfma_f32_16x16x32_bf16 v[134:137], v[142:145], v[42:45], v[134:137]
	v_cvt_pk_bf16_f32 v141, v146, v147
	v_mfma_f32_16x16x32_bf16 v[130:133], v[142:145], v[106:109], v[130:133]
	ds_read_b128 v[142:145], v198 offset:640
	ds_read_b128 v[146:149], v198 offset:656
	v_mfma_f32_16x16x32_bf16 v[134:137], v[138:141], v[34:37], v[134:137]
	v_mfma_f32_16x16x32_bf16 v[130:133], v[138:141], v[98:101], v[130:133]
	s_waitcnt lgkmcnt(1)
	v_cvt_pk_bf16_f32 v138, v142, v143
	v_cvt_pk_bf16_f32 v139, v144, v145
	s_waitcnt lgkmcnt(0)
	v_cvt_pk_bf16_f32 v140, v146, v147
	v_cvt_pk_bf16_f32 v141, v148, v149
	v_lshlrev_b32_e32 v150, 16, v138
	v_and_b32_e32 v151, 0xffff0000, v138
	v_pk_add_f32 v[142:143], v[142:143], v[150:151] neg_lo:[0,1] neg_hi:[0,1]
	v_lshlrev_b32_e32 v150, 16, v139
	v_and_b32_e32 v151, 0xffff0000, v139
	v_pk_add_f32 v[144:145], v[144:145], v[150:151] neg_lo:[0,1] neg_hi:[0,1]
	v_mfma_f32_16x16x32_bf16 v[134:137], v[138:141], v[38:41], v[134:137]
	v_cvt_pk_bf16_f32 v142, v142, v143
	v_cvt_pk_bf16_f32 v143, v144, v145
	v_lshlrev_b32_e32 v144, 16, v140
	v_mfma_f32_16x16x32_bf16 v[130:133], v[138:141], v[102:105], v[130:133]
	v_and_b32_e32 v145, 0xffff0000, v140
	v_pk_add_f32 v[144:145], v[146:147], v[144:145] neg_lo:[0,1] neg_hi:[0,1]
	v_lshlrev_b32_e32 v146, 16, v141
	v_and_b32_e32 v147, 0xffff0000, v141
	v_pk_add_f32 v[146:147], v[148:149], v[146:147] neg_lo:[0,1] neg_hi:[0,1]
	v_cvt_pk_bf16_f32 v144, v144, v145
	v_mfma_f32_16x16x32_bf16 v[134:137], v[138:141], v[46:49], v[134:137]
	v_cvt_pk_bf16_f32 v145, v146, v147
	v_mfma_f32_16x16x32_bf16 v[130:133], v[138:141], v[110:113], v[130:133]
	ds_read_b128 v[138:141], v198 offset:768
	ds_read_b128 v[146:149], v198 offset:784
	v_mfma_f32_16x16x32_bf16 v[134:137], v[142:145], v[38:41], v[134:137]
	v_mfma_f32_16x16x32_bf16 v[130:133], v[142:145], v[102:105], v[130:133]
	s_waitcnt lgkmcnt(1)
	v_cvt_pk_bf16_f32 v142, v138, v139
	v_cvt_pk_bf16_f32 v143, v140, v141
	s_waitcnt lgkmcnt(0)
	v_cvt_pk_bf16_f32 v144, v146, v147
	v_cvt_pk_bf16_f32 v145, v148, v149
	v_lshlrev_b32_e32 v150, 16, v142
	v_and_b32_e32 v151, 0xffff0000, v142
	v_pk_add_f32 v[138:139], v[138:139], v[150:151] neg_lo:[0,1] neg_hi:[0,1]
	v_lshlrev_b32_e32 v150, 16, v143
	v_and_b32_e32 v151, 0xffff0000, v143
	v_pk_add_f32 v[140:141], v[140:141], v[150:151] neg_lo:[0,1] neg_hi:[0,1]
	v_mfma_f32_16x16x32_bf16 v[134:137], v[142:145], v[50:53], v[134:137]
	v_cvt_pk_bf16_f32 v138, v138, v139
	v_cvt_pk_bf16_f32 v139, v140, v141
	v_lshlrev_b32_e32 v140, 16, v144
	v_mfma_f32_16x16x32_bf16 v[130:133], v[142:145], v[114:117], v[130:133]
	v_and_b32_e32 v141, 0xffff0000, v144
	v_pk_add_f32 v[140:141], v[146:147], v[140:141] neg_lo:[0,1] neg_hi:[0,1]
	v_lshlrev_b32_e32 v146, 16, v145
	v_and_b32_e32 v147, 0xffff0000, v145
	v_pk_add_f32 v[146:147], v[148:149], v[146:147] neg_lo:[0,1] neg_hi:[0,1]
	v_cvt_pk_bf16_f32 v140, v140, v141
	v_mfma_f32_16x16x32_bf16 v[134:137], v[142:145], v[58:61], v[134:137]
	v_cvt_pk_bf16_f32 v141, v146, v147
	ds_read_b128 v[146:149], v198 offset:912
	v_mfma_f32_16x16x32_bf16 v[130:133], v[142:145], v[122:125], v[130:133]
	ds_read_b128 v[142:145], v198 offset:896
	v_mfma_f32_16x16x32_bf16 v[134:137], v[138:141], v[50:53], v[134:137]
	v_mfma_f32_16x16x32_bf16 v[130:133], v[138:141], v[114:117], v[130:133]
	s_waitcnt lgkmcnt(0)
	v_cvt_pk_bf16_f32 v138, v142, v143
	v_cvt_pk_bf16_f32 v139, v144, v145
	v_cvt_pk_bf16_f32 v140, v146, v147
	v_cvt_pk_bf16_f32 v141, v148, v149
	v_lshlrev_b32_e32 v150, 16, v138
	v_and_b32_e32 v151, 0xffff0000, v138
	v_pk_add_f32 v[142:143], v[142:143], v[150:151] neg_lo:[0,1] neg_hi:[0,1]
	v_mfma_f32_16x16x32_bf16 v[134:137], v[138:141], v[54:57], v[134:137]
	v_cvt_pk_bf16_f32 v206, v142, v143
	v_lshlrev_b32_e32 v142, 16, v139
	v_and_b32_e32 v143, 0xffff0000, v139
	v_pk_add_f32 v[142:143], v[144:145], v[142:143] neg_lo:[0,1] neg_hi:[0,1]
	v_mfma_f32_16x16x32_bf16 v[130:133], v[138:141], v[118:121], v[130:133]
	v_cvt_pk_bf16_f32 v207, v142, v143
	v_lshlrev_b32_e32 v142, 16, v140
	v_and_b32_e32 v143, 0xffff0000, v140
	v_pk_add_f32 v[142:143], v[146:147], v[142:143] neg_lo:[0,1] neg_hi:[0,1]
	v_mfma_f32_16x16x32_bf16 v[134:137], v[138:141], v[62:65], v[134:137]
	v_cvt_pk_bf16_f32 v208, v142, v143
	v_lshlrev_b32_e32 v142, 16, v141
	v_and_b32_e32 v143, 0xffff0000, v141
	v_pk_add_f32 v[142:143], v[148:149], v[142:143] neg_lo:[0,1] neg_hi:[0,1]
	v_mfma_f32_16x16x32_bf16 v[214:217], v[138:141], v[126:129], v[130:133]
	v_cvt_pk_bf16_f32 v209, v142, v143
	v_lshl_add_u64 v[142:143], v[166:167], 0, s[2:3]
	global_load_dwordx4 v[150:153], v[142:143], off
	global_load_dwordx4 v[158:161], v[142:143], off offset:1024
	v_mfma_f32_16x16x32_bf16 v[210:213], v[206:209], v[54:57], v[134:137]
	global_load_dwordx4 v[154:157], v[142:143], off offset:2048
	global_load_dwordx4 v[146:149], v[142:143], off offset:3072
	s_nop 0
	global_load_dwordx4 v[134:137], v[186:187], off
	global_load_dwordx4 v[142:145], v[186:187], off offset:1024
	global_load_dwordx4 v[138:141], v[186:187], off offset:2048
	global_load_dwordx4 v[130:133], v[186:187], off offset:3072
	v_mfma_f32_16x16x32_bf16 v[206:209], v[206:209], v[118:121], v[214:217]
	s_nop 7
	ds_write2_b32 v199, v210, v206 offset1:16
	ds_write2_b32 v199, v211, v207 offset0:32 offset1:48
	ds_write2_b32 v199, v212, v208 offset0:64 offset1:80
	ds_write2_b32 v199, v213, v209 offset0:96 offset1:112
	s_waitcnt lgkmcnt(0)
	s_barrier
	global_load_dword v0, v[170:171], off
	ds_read2st64_b32 v[186:187], v200 offset1:8
	ds_read2st64_b32 v[188:189], v200 offset0:16 offset1:24
	ds_read2st64_b32 v[206:207], v200 offset0:32 offset1:40
	v_or_b32_e32 v212, 56, v203
	v_or_b32_e32 v213, 60, v203
	v_or_b32_e32 v214, 64, v203
	v_or_b32_e32 v215, 0x44, v203
	v_or_b32_e32 v216, 0x48, v203
	v_or_b32_e32 v217, 0x4c, v203
	s_waitcnt vmcnt(0)
	s_waitcnt lgkmcnt(2)
	v_add_f32_e32 v0, v0, v186
	v_add_f32_e32 v0, v0, v187
	ds_read2st64_b32 v[186:187], v200 offset0:48 offset1:56
	s_waitcnt lgkmcnt(2)
	v_add_f32_e32 v0, v0, v188
	v_add_f32_e32 v0, v0, v189
	s_waitcnt lgkmcnt(1)
	v_add_f32_e32 v0, v0, v206
	v_add_f32_e32 v0, v0, v207
	s_waitcnt lgkmcnt(0)
	v_add_f32_e32 v0, v0, v186
	v_add_f32_e32 v163, v0, v187
	v_or_b32_e32 v0, 4, v203
	ds_bpermute_b32 v0, v0, v163
	ds_bpermute_b32 v186, v164, v163
	v_or_b32_e32 v187, 44, v203
	ds_bpermute_b32 v187, v187, v163
	v_or_b32_e32 v188, 48, v203
	s_waitcnt lgkmcnt(2)
	v_cmp_lt_f32_e64 s[2:3], v163, v0
	v_cmp_eq_f32_e32 vcc, v163, v0
	s_and_b64 s[0:1], vcc, s[0:1]
	v_writelane_b32 v253, s2, 8
	v_or_b32_e32 v0, 12, v203
	ds_bpermute_b32 v0, v0, v163
	v_writelane_b32 v253, s3, 9
	v_writelane_b32 v253, s0, 12
	s_waitcnt lgkmcnt(2)
	v_cmp_eq_f32_e32 vcc, v163, v186
	ds_bpermute_b32 v188, v188, v163
	v_writelane_b32 v253, s1, 13
	s_or_b64 s[0:1], s[2:3], s[0:1]
	v_cndmask_b32_e64 v164, 0, 1, s[0:1]
	v_cmp_lt_f32_e64 s[2:3], v163, v186
	v_readlane_b32 s0, v254, 31
	v_readlane_b32 s1, v254, 32
	v_writelane_b32 v253, s2, 10
	s_and_b64 s[0:1], vcc, s[0:1]
	v_or_b32_e32 v186, 16, v203
	v_writelane_b32 v253, s3, 11
	v_writelane_b32 v253, s0, 14
	ds_bpermute_b32 v186, v186, v163
	s_waitcnt lgkmcnt(2)
	v_cmp_eq_f32_e32 vcc, v163, v0
	v_writelane_b32 v253, s1, 15
	s_or_b64 s[0:1], s[2:3], s[0:1]
	v_cndmask_b32_e64 v205, 0, 1, s[0:1]
	v_cmp_lt_f32_e64 s[2:3], v163, v0
	v_readlane_b32 s0, v254, 33
	v_readlane_b32 s1, v254, 34
	v_writelane_b32 v253, s2, 16
	s_and_b64 s[0:1], vcc, s[0:1]
	v_or_b32_e32 v0, 20, v203
	v_writelane_b32 v253, s3, 17
	v_writelane_b32 v253, s0, 18
	ds_bpermute_b32 v0, v0, v163
	s_waitcnt lgkmcnt(1)
	v_cmp_eq_f32_e32 vcc, v163, v186
	v_writelane_b32 v253, s1, 19
	s_or_b64 s[0:1], s[2:3], s[0:1]
	v_cndmask_b32_e64 v206, 0, 1, s[0:1]
	v_cmp_lt_f32_e64 s[2:3], v163, v186
	v_readlane_b32 s0, v254, 35
	v_readlane_b32 s1, v254, 36
	v_writelane_b32 v253, s2, 20
	s_and_b64 s[0:1], vcc, s[0:1]
	v_or_b32_e32 v186, 24, v203
	v_writelane_b32 v253, s3, 21
	v_writelane_b32 v253, s0, 22
	ds_bpermute_b32 v186, v186, v163
	s_waitcnt lgkmcnt(1)
	v_cmp_eq_f32_e32 vcc, v163, v0
	v_writelane_b32 v253, s1, 23
	s_or_b64 s[0:1], s[2:3], s[0:1]
	v_cndmask_b32_e64 v207, 0, 1, s[0:1]
	v_cmp_lt_f32_e64 s[2:3], v163, v0
	v_readlane_b32 s0, v254, 37
	v_readlane_b32 s1, v254, 38
	v_writelane_b32 v253, s2, 24
	s_and_b64 s[0:1], vcc, s[0:1]
	v_or_b32_e32 v0, 28, v203
	v_writelane_b32 v253, s3, 25
	v_writelane_b32 v253, s0, 28
	ds_bpermute_b32 v0, v0, v163
	s_waitcnt lgkmcnt(1)
	v_cmp_eq_f32_e32 vcc, v163, v186
	v_writelane_b32 v253, s1, 29
	s_or_b64 s[0:1], s[2:3], s[0:1]
	v_cndmask_b32_e64 v208, 0, 1, s[0:1]
	v_cmp_lt_f32_e64 s[2:3], v163, v186
	v_readlane_b32 s0, v254, 39
	v_readlane_b32 s1, v254, 40
	v_writelane_b32 v253, s2, 26
	s_and_b64 s[0:1], vcc, s[0:1]
	v_or_b32_e32 v186, 32, v203
	v_writelane_b32 v253, s3, 27
	v_writelane_b32 v253, s0, 30
	ds_bpermute_b32 v186, v186, v163
	s_waitcnt lgkmcnt(1)
	v_cmp_eq_f32_e32 vcc, v163, v0
	v_writelane_b32 v253, s1, 31
	s_or_b64 s[0:1], s[2:3], s[0:1]
	v_cndmask_b32_e64 v209, 0, 1, s[0:1]
	v_cmp_lt_f32_e64 s[2:3], v163, v0
	v_readlane_b32 s0, v254, 41
	v_readlane_b32 s1, v254, 42
	v_writelane_b32 v253, s2, 38
	s_and_b64 s[0:1], vcc, s[0:1]
	s_waitcnt lgkmcnt(0)
	v_cmp_eq_f32_e32 vcc, v163, v186
	v_writelane_b32 v253, s3, 39
	v_writelane_b32 v253, s0, 36
	v_or_b32_e32 v0, 36, v203
	ds_bpermute_b32 v0, v0, v163
	v_writelane_b32 v253, s1, 37
	s_or_b64 s[0:1], s[2:3], s[0:1]
	v_cndmask_b32_e64 v210, 0, 1, s[0:1]
	v_readlane_b32 s0, v254, 43
	v_readlane_b32 s1, v254, 44
	s_and_b64 s[2:3], vcc, s[0:1]
	v_cmp_lt_f32_e64 s[0:1], v163, v186
	v_or_b32_e32 v186, 40, v203
	ds_bpermute_b32 v186, v186, v163
	v_writelane_b32 v253, s0, 32
	s_waitcnt lgkmcnt(1)
	v_cmp_eq_f32_e32 vcc, v163, v0
	v_cmp_lt_f32_e64 s[86:87], v163, v0
	v_writelane_b32 v253, s1, 33
	v_writelane_b32 v253, s2, 34
	s_or_b64 s[0:1], s[0:1], s[2:3]
	v_cndmask_b32_e64 v211, 0, 1, s[0:1]
	v_readlane_b32 s0, v254, 45
	v_readlane_b32 s1, v254, 46
	s_and_b64 s[60:61], vcc, s[0:1]
	s_or_b64 s[0:1], s[86:87], s[60:61]
	v_cndmask_b32_e64 v0, 0, 1, s[0:1]
	v_readlane_b32 s0, v254, 47
	s_waitcnt lgkmcnt(0)
	v_cmp_eq_f32_e32 vcc, v163, v186
	v_readlane_b32 s1, v254, 48
	s_and_b64 s[62:63], vcc, s[0:1]
	v_cmp_lt_f32_e64 s[88:89], v163, v186
	s_or_b64 s[0:1], s[88:89], s[62:63]
	v_cndmask_b32_e64 v186, 0, 1, s[0:1]
	v_readlane_b32 s0, v254, 49
	v_cmp_eq_f32_e32 vcc, v163, v187
	v_readlane_b32 s1, v254, 50
	s_and_b64 s[64:65], vcc, s[0:1]
	v_cmp_lt_f32_e64 s[90:91], v163, v187
	s_or_b64 s[0:1], s[90:91], s[64:65]
	v_or_b32_e32 v189, 52, v203
	v_cndmask_b32_e64 v187, 0, 1, s[0:1]
	v_readlane_b32 s0, v254, 51
	ds_bpermute_b32 v189, v189, v163
	v_cmp_eq_f32_e32 vcc, v163, v188
	v_readlane_b32 s1, v254, 52
	s_and_b64 s[66:67], vcc, s[0:1]
	v_cmp_lt_f32_e64 s[92:93], v163, v188
	s_or_b64 s[0:1], s[92:93], s[66:67]
	v_cndmask_b32_e64 v188, 0, 1, s[0:1]
	v_readlane_b32 s0, v254, 53
	ds_bpermute_b32 v212, v212, v163
	s_waitcnt lgkmcnt(1)
	v_cmp_eq_f32_e32 vcc, v163, v189
	v_readlane_b32 s1, v254, 54
	s_and_b64 s[68:69], vcc, s[0:1]
	v_cmp_lt_f32_e64 s[94:95], v163, v189
	s_or_b64 s[0:1], s[94:95], s[68:69]
	v_cndmask_b32_e64 v189, 0, 1, s[0:1]
	v_readlane_b32 s0, v254, 55
	ds_bpermute_b32 v213, v213, v163
	s_waitcnt lgkmcnt(1)
	v_cmp_eq_f32_e32 vcc, v163, v212
	v_readlane_b32 s1, v254, 56
	s_and_b64 s[70:71], vcc, s[0:1]
	v_cmp_lt_f32_e64 s[96:97], v163, v212
	s_or_b64 s[0:1], s[96:97], s[70:71]
	v_cndmask_b32_e64 v212, 0, 1, s[0:1]
	v_readlane_b32 s0, v254, 57
	ds_bpermute_b32 v214, v214, v163
	s_waitcnt lgkmcnt(1)
	v_cmp_eq_f32_e32 vcc, v163, v213
	v_readlane_b32 s1, v254, 58
	s_and_b64 s[42:43], vcc, s[0:1]
	v_cmp_lt_f32_e64 s[6:7], v163, v213
	s_or_b64 s[0:1], s[6:7], s[42:43]
	v_cndmask_b32_e64 v213, 0, 1, s[0:1]
	v_readlane_b32 s0, v254, 59
	ds_bpermute_b32 v215, v215, v163
	s_waitcnt lgkmcnt(1)
	v_cmp_eq_f32_e32 vcc, v163, v214
	v_readlane_b32 s1, v254, 60
	v_writelane_b32 v253, s3, 35
	s_and_b64 s[4:5], vcc, s[0:1]
	v_cmp_lt_f32_e64 s[2:3], v163, v214
	s_or_b64 s[0:1], s[2:3], s[4:5]
	v_cndmask_b32_e64 v214, 0, 1, s[0:1]
	v_readlane_b32 s0, v254, 61
	ds_bpermute_b32 v216, v216, v163
	s_waitcnt lgkmcnt(1)
	v_cmp_eq_f32_e32 vcc, v163, v215
	v_readlane_b32 s1, v254, 62
	s_and_b64 s[72:73], vcc, s[0:1]
	v_cmp_lt_f32_e64 s[8:9], v163, v215
	s_or_b64 s[0:1], s[8:9], s[72:73]
	v_cndmask_b32_e64 v215, 0, 1, s[0:1]
	v_readlane_b32 s0, v254, 63
	ds_bpermute_b32 v217, v217, v163
	s_waitcnt lgkmcnt(1)
	v_cmp_eq_f32_e32 vcc, v163, v216
	v_readlane_b32 s1, v255, 0
	s_and_b64 s[0:1], vcc, s[0:1]
	v_cmp_lt_f32_e64 s[10:11], v163, v216
	s_or_b64 s[12:13], s[10:11], s[0:1]
	v_cndmask_b32_e64 v216, 0, 1, s[12:13]
	v_readlane_b32 s12, v255, 1
	ds_bpermute_b32 v218, v218, v163
	s_waitcnt lgkmcnt(1)
	v_cmp_eq_f32_e32 vcc, v163, v217
	v_readlane_b32 s13, v255, 2
	s_and_b64 s[44:45], vcc, s[12:13]
	v_cmp_lt_f32_e64 s[12:13], v163, v217
	s_or_b64 s[14:15], s[12:13], s[44:45]
	v_cndmask_b32_e64 v217, 0, 1, s[14:15]
	v_readlane_b32 s14, v255, 3
	ds_bpermute_b32 v219, v219, v163
	s_waitcnt lgkmcnt(1)
	v_cmp_eq_f32_e32 vcc, v163, v218
	v_readlane_b32 s15, v255, 4
	s_and_b64 s[46:47], vcc, s[14:15]
	v_cmp_lt_f32_e64 s[14:15], v163, v218
	s_or_b64 s[16:17], s[14:15], s[46:47]
	v_cndmask_b32_e64 v218, 0, 1, s[16:17]
	v_readlane_b32 s16, v255, 5
	ds_bpermute_b32 v220, v220, v163
	s_waitcnt lgkmcnt(1)
	v_cmp_eq_f32_e32 vcc, v163, v219
	v_readlane_b32 s17, v255, 6
	s_and_b64 s[74:75], vcc, s[16:17]
	v_cmp_lt_f32_e64 s[16:17], v163, v219
	s_or_b64 s[18:19], s[16:17], s[74:75]
	v_cndmask_b32_e64 v219, 0, 1, s[18:19]
	v_readlane_b32 s18, v255, 7
	ds_bpermute_b32 v221, v221, v163
	s_waitcnt lgkmcnt(1)
	v_cmp_eq_f32_e32 vcc, v163, v220
	v_readlane_b32 s19, v255, 8
	s_and_b64 s[48:49], vcc, s[18:19]
	v_cmp_lt_f32_e64 s[18:19], v163, v220
	s_or_b64 s[20:21], s[18:19], s[48:49]
	v_cndmask_b32_e64 v220, 0, 1, s[20:21]
	v_readlane_b32 s20, v255, 9
	ds_bpermute_b32 v222, v222, v163
	s_waitcnt lgkmcnt(1)
	v_cmp_eq_f32_e32 vcc, v163, v221
	v_readlane_b32 s21, v255, 10
	s_and_b64 s[76:77], vcc, s[20:21]
	v_cmp_lt_f32_e64 s[20:21], v163, v221
	s_or_b64 s[22:23], s[20:21], s[76:77]
	v_cndmask_b32_e64 v221, 0, 1, s[22:23]
	v_readlane_b32 s22, v255, 11
	ds_bpermute_b32 v223, v223, v163
	s_waitcnt lgkmcnt(1)
	v_cmp_eq_f32_e32 vcc, v163, v222
	v_readlane_b32 s23, v255, 12
	s_and_b64 s[50:51], vcc, s[22:23]
	v_cmp_lt_f32_e64 s[22:23], v163, v222
	s_or_b64 s[24:25], s[22:23], s[50:51]
	v_cndmask_b32_e64 v222, 0, 1, s[24:25]
	v_readlane_b32 s24, v255, 13
	ds_bpermute_b32 v224, v224, v163
	s_waitcnt lgkmcnt(1)
	v_cmp_eq_f32_e32 vcc, v163, v223
	v_readlane_b32 s25, v255, 14
	s_and_b64 s[78:79], vcc, s[24:25]
	v_cmp_lt_f32_e64 s[24:25], v163, v223
	s_or_b64 s[26:27], s[24:25], s[78:79]
	v_cndmask_b32_e64 v223, 0, 1, s[26:27]
	v_readlane_b32 s26, v255, 15
	ds_bpermute_b32 v225, v225, v163
	s_waitcnt lgkmcnt(1)
	v_cmp_eq_f32_e32 vcc, v163, v224
	v_readlane_b32 s27, v255, 16
	ds_bpermute_b32 v230, v192, v163
	s_and_b64 s[80:81], vcc, s[26:27]
	v_cmp_lt_f32_e64 s[26:27], v163, v224
	s_or_b64 s[28:29], s[26:27], s[80:81]
	v_cndmask_b32_e64 v224, 0, 1, s[28:29]
	v_readlane_b32 s28, v255, 17
	ds_bpermute_b32 v226, v226, v163
	s_waitcnt lgkmcnt(2)
	v_cmp_eq_f32_e32 vcc, v163, v225
	v_readlane_b32 s29, v255, 18
	s_and_b64 s[52:53], vcc, s[28:29]
	v_cmp_lt_f32_e64 s[28:29], v163, v225
	s_waitcnt lgkmcnt(1)
	v_max_f32_e32 v230, v230, v230
	s_or_b64 s[30:31], s[28:29], s[52:53]
	v_max_f32_e32 v230, v163, v230
	v_cndmask_b32_e64 v225, 0, 1, s[30:31]
	v_readlane_b32 s30, v255, 19
	ds_bpermute_b32 v227, v227, v163
	ds_bpermute_b32 v231, v193, v230
	s_waitcnt lgkmcnt(2)
	v_cmp_eq_f32_e32 vcc, v163, v226
	v_readlane_b32 s31, v255, 20
	s_and_b64 s[54:55], vcc, s[30:31]
	v_cmp_lt_f32_e64 s[30:31], v163, v226
	s_or_b64 s[34:35], s[30:31], s[54:55]
	v_cndmask_b32_e64 v226, 0, 1, s[34:35]
	v_readlane_b32 s34, v255, 21
	ds_bpermute_b32 v228, v228, v163
	s_waitcnt lgkmcnt(2)
	v_cmp_eq_f32_e32 vcc, v163, v227
	v_readlane_b32 s35, v255, 22
	s_waitcnt lgkmcnt(1)
	v_max_f32_e32 v231, v231, v231
	s_and_b64 s[82:83], vcc, s[34:35]
	v_cmp_lt_f32_e64 s[34:35], v163, v227
	v_max_f32_e32 v230, v230, v231
	s_or_b64 s[36:37], s[34:35], s[82:83]
	ds_bpermute_b32 v231, v194, v230
	v_cndmask_b32_e64 v227, 0, 1, s[36:37]
	v_readlane_b32 s36, v255, 23
	ds_bpermute_b32 v229, v203, v163
	s_waitcnt lgkmcnt(2)
	v_cmp_eq_f32_e32 vcc, v163, v228
	v_readlane_b32 s37, v255, 24
	s_and_b64 s[56:57], vcc, s[36:37]
	v_cmp_lt_f32_e64 s[36:37], v163, v228
	s_or_b64 s[38:39], s[36:37], s[56:57]
	v_cndmask_b32_e64 v228, 0, 1, s[38:39]
	v_readlane_b32 s38, v254, 27
	s_waitcnt lgkmcnt(1)
	v_max_f32_e32 v231, v231, v231
	s_waitcnt lgkmcnt(0)
	v_cmp_eq_f32_e32 vcc, v163, v229
	v_readlane_b32 s39, v254, 28
	v_max_f32_e32 v230, v230, v231
	s_and_b64 s[58:59], vcc, s[38:39]
	v_cmp_lt_f32_e64 s[38:39], v163, v229
	ds_bpermute_b32 v231, v195, v230
	s_or_b64 s[40:41], s[38:39], s[58:59]
	v_cndmask_b32_e64 v229, 0, 1, s[40:41]
	v_add3_u32 v164, v164, v229, v205
	v_add3_u32 v164, v164, v206, v207
	s_waitcnt lgkmcnt(0)
	v_max_f32_e32 v231, v231, v231
	v_add3_u32 v164, v164, v208, v209
	v_max_f32_e32 v230, v230, v231
	v_add3_u32 v164, v164, v210, v211
	ds_bpermute_b32 v231, v196, v230
	v_add3_u32 v0, v164, v0, v186
	v_add3_u32 v0, v0, v187, v188
	v_add3_u32 v0, v0, v189, v212
	v_add3_u32 v0, v0, v213, v214
	ds_bpermute_b32 v232, v232, v163
	v_add3_u32 v0, v0, v215, v216
	s_waitcnt lgkmcnt(1)
	v_max_f32_e32 v231, v231, v231
	v_add3_u32 v0, v0, v217, v218
	v_max_f32_e32 v230, v230, v231
	v_add3_u32 v0, v0, v219, v220
	v_add3_u32 v0, v0, v221, v222
	v_sub_f32_e32 v164, v163, v230
	v_add3_u32 v0, v0, v223, v224
	v_mul_f32_e32 v164, 0x3fb8aa3b, v164
	v_add3_u32 v0, v0, v225, v226
	v_exp_f32_e32 v164, v164
	s_waitcnt lgkmcnt(0)
	v_cmp_lt_f32_e64 s[40:41], v163, v232
	s_nop 1
	v_addc_co_u32_e64 v0, vcc, v0, v227, s[40:41]
	v_add_u32_e32 v0, v0, v228
	v_cmp_gt_u32_e32 vcc, 4, v0
	s_nop 1
	v_cndmask_b32_e32 v0, 0, v164, vcc
	ds_bpermute_b32 v163, v192, v0
	v_cndmask_b32_e64 v205, 0, 1, vcc
	ds_bpermute_b32 v206, v197, v205
	s_waitcnt lgkmcnt(1)
	v_add_f32_e32 v0, v0, v163
	ds_bpermute_b32 v163, v193, v0
	s_waitcnt lgkmcnt(0)
	v_add_f32_e32 v0, v0, v163
	ds_bpermute_b32 v163, v194, v0
	s_waitcnt lgkmcnt(0)
	v_add_f32_e32 v0, v0, v163
	ds_bpermute_b32 v163, v195, v0
	s_waitcnt lgkmcnt(0)
	v_add_f32_e32 v163, v0, v163
	ds_bpermute_b32 v207, v196, v163
	s_and_saveexec_b64 s[84:85], vcc
	s_waitcnt lgkmcnt(0)
	s_cbranch_execz .LBB0_1046
	v_cndmask_b32_e64 v0, 0, 1, s[40:41]
	v_readlane_b32 s40, v253, 12
	v_readlane_b32 vcc_lo, v253, 8
	v_readlane_b32 s41, v253, 13
	v_readlane_b32 vcc_hi, v253, 9
	s_xor_b64 s[40:41], s[40:41], -1
	s_xor_b64 vcc, vcc, -1
	s_and_b64 s[40:41], s[40:41], vcc
	s_xor_b64 s[40:41], s[40:41], -1
	v_add_f32_e32 v186, v163, v207
	v_cndmask_b32_e64 v163, 0, 1, s[40:41]
	s_xor_b64 s[40:41], s[58:59], -1
	s_xor_b64 s[38:39], s[38:39], -1
	s_and_b64 s[38:39], s[40:41], s[38:39]
	s_xor_b64 s[38:39], s[38:39], -1
	v_cndmask_b32_e64 v187, 0, 1, s[38:39]
	v_readlane_b32 s38, v253, 14
	v_readlane_b32 s40, v253, 10
	v_readlane_b32 s39, v253, 15
	v_readlane_b32 s41, v253, 11
	s_xor_b64 s[38:39], s[38:39], -1
	s_xor_b64 s[40:41], s[40:41], -1
	s_and_b64 s[38:39], s[38:39], s[40:41]
	s_xor_b64 s[38:39], s[38:39], -1
	v_add3_u32 v0, v0, v163, v187
	v_cndmask_b32_e64 v163, 0, 1, s[38:39]
	v_readlane_b32 s38, v253, 18
	v_readlane_b32 s40, v253, 16
	v_readlane_b32 s39, v253, 19
	v_readlane_b32 s41, v253, 17
	s_xor_b64 s[38:39], s[38:39], -1
	s_xor_b64 s[40:41], s[40:41], -1
	s_and_b64 s[38:39], s[38:39], s[40:41]
	s_xor_b64 s[38:39], s[38:39], -1
	v_cndmask_b32_e64 v187, 0, 1, s[38:39]
	v_readlane_b32 s38, v253, 22
	v_readlane_b32 s40, v253, 20
	v_readlane_b32 s39, v253, 23
	v_readlane_b32 s41, v253, 21
	s_xor_b64 s[38:39], s[38:39], -1
	s_xor_b64 s[40:41], s[40:41], -1
	s_and_b64 s[38:39], s[38:39], s[40:41]
	s_xor_b64 s[38:39], s[38:39], -1
	v_add3_u32 v0, v0, v163, v187
	v_cndmask_b32_e64 v163, 0, 1, s[38:39]
	v_readlane_b32 s38, v253, 28
	v_readlane_b32 s40, v253, 24
	v_readlane_b32 s39, v253, 29
	v_readlane_b32 s41, v253, 25
	s_xor_b64 s[38:39], s[38:39], -1
	s_xor_b64 s[40:41], s[40:41], -1
	s_and_b64 s[38:39], s[38:39], s[40:41]
	s_xor_b64 s[38:39], s[38:39], -1
	v_cndmask_b32_e64 v187, 0, 1, s[38:39]
	v_readlane_b32 s38, v253, 30
	v_readlane_b32 s40, v253, 26
	v_readlane_b32 s39, v253, 31
	v_readlane_b32 s41, v253, 27
	s_xor_b64 s[38:39], s[38:39], -1
	s_xor_b64 s[40:41], s[40:41], -1
	s_and_b64 s[38:39], s[38:39], s[40:41]
	s_xor_b64 s[38:39], s[38:39], -1
	v_add3_u32 v0, v0, v163, v187
	v_cndmask_b32_e64 v163, 0, 1, s[38:39]
	v_readlane_b32 s38, v253, 36
	v_readlane_b32 s40, v253, 38
	v_readlane_b32 s39, v253, 37
	v_readlane_b32 s41, v253, 39
	s_xor_b64 s[38:39], s[38:39], -1
	s_xor_b64 s[40:41], s[40:41], -1
	s_and_b64 s[38:39], s[38:39], s[40:41]
	s_xor_b64 s[38:39], s[38:39], -1
	v_cndmask_b32_e64 v187, 0, 1, s[38:39]
	v_readlane_b32 s38, v253, 34
	v_readlane_b32 s40, v253, 32
	v_readlane_b32 s39, v253, 35
	v_readlane_b32 s41, v253, 33
	s_xor_b64 s[38:39], s[38:39], -1
	s_xor_b64 s[40:41], s[40:41], -1
	s_and_b64 s[38:39], s[38:39], s[40:41]
	s_xor_b64 s[38:39], s[38:39], -1
	v_add3_u32 v0, v0, v163, v187
	v_cndmask_b32_e64 v163, 0, 1, s[38:39]
	s_xor_b64 s[38:39], s[60:61], -1
	s_xor_b64 s[40:41], s[86:87], -1
	s_and_b64 s[38:39], s[38:39], s[40:41]
	s_xor_b64 s[38:39], s[38:39], -1
	v_cndmask_b32_e64 v187, 0, 1, s[38:39]
	s_xor_b64 s[38:39], s[62:63], -1
	s_xor_b64 s[40:41], s[88:89], -1
	s_and_b64 s[38:39], s[38:39], s[40:41]
	s_xor_b64 s[38:39], s[38:39], -1
	v_add3_u32 v0, v0, v163, v187
	v_cndmask_b32_e64 v163, 0, 1, s[38:39]
	s_xor_b64 s[38:39], s[64:65], -1
	s_xor_b64 s[40:41], s[90:91], -1
	s_and_b64 s[38:39], s[38:39], s[40:41]
	s_xor_b64 s[38:39], s[38:39], -1
	v_cndmask_b32_e64 v187, 0, 1, s[38:39]
	s_xor_b64 s[38:39], s[66:67], -1
	s_xor_b64 s[40:41], s[92:93], -1
	s_and_b64 s[38:39], s[38:39], s[40:41]
	s_xor_b64 s[38:39], s[38:39], -1
	v_add3_u32 v0, v0, v163, v187
	v_cndmask_b32_e64 v163, 0, 1, s[38:39]
	s_xor_b64 s[38:39], s[68:69], -1
	s_xor_b64 s[40:41], s[94:95], -1
	s_and_b64 s[38:39], s[38:39], s[40:41]
	s_xor_b64 s[38:39], s[38:39], -1
	v_cndmask_b32_e64 v187, 0, 1, s[38:39]
	s_xor_b64 s[38:39], s[70:71], -1
	s_xor_b64 s[40:41], s[96:97], -1
	s_and_b64 s[38:39], s[38:39], s[40:41]
	s_xor_b64 s[38:39], s[38:39], -1
	v_add3_u32 v0, v0, v163, v187
	v_cndmask_b32_e64 v163, 0, 1, s[38:39]
	s_xor_b64 s[38:39], s[42:43], -1
	s_xor_b64 s[6:7], s[6:7], -1
	s_and_b64 s[6:7], s[38:39], s[6:7]
	s_xor_b64 s[4:5], s[4:5], -1
	s_xor_b64 s[2:3], s[2:3], -1
	s_xor_b64 s[6:7], s[6:7], -1
	s_and_b64 s[2:3], s[4:5], s[2:3]
	v_cndmask_b32_e64 v187, 0, 1, s[6:7]
	s_xor_b64 s[2:3], s[2:3], -1
	v_add3_u32 v0, v0, v163, v187
	v_cndmask_b32_e64 v163, 0, 1, s[2:3]
	s_xor_b64 s[2:3], s[72:73], -1
	s_xor_b64 s[4:5], s[8:9], -1
	s_and_b64 s[2:3], s[2:3], s[4:5]
	s_xor_b64 s[2:3], s[2:3], -1
	v_cndmask_b32_e64 v187, 0, 1, s[2:3]
	s_xor_b64 s[0:1], s[0:1], -1
	s_xor_b64 s[2:3], s[10:11], -1
	s_and_b64 s[0:1], s[0:1], s[2:3]
	s_xor_b64 s[0:1], s[0:1], -1
	v_add3_u32 v0, v0, v163, v187
	v_cndmask_b32_e64 v163, 0, 1, s[0:1]
	s_xor_b64 s[0:1], s[44:45], -1
	s_xor_b64 s[2:3], s[12:13], -1
	s_and_b64 s[0:1], s[0:1], s[2:3]
	s_xor_b64 s[0:1], s[0:1], -1
	v_cndmask_b32_e64 v187, 0, 1, s[0:1]
	s_xor_b64 s[0:1], s[46:47], -1
	s_xor_b64 s[2:3], s[14:15], -1
	s_and_b64 s[0:1], s[0:1], s[2:3]
	s_xor_b64 s[0:1], s[0:1], -1
	v_add3_u32 v0, v0, v163, v187
	v_cndmask_b32_e64 v163, 0, 1, s[0:1]
	s_xor_b64 s[0:1], s[74:75], -1
	s_xor_b64 s[2:3], s[16:17], -1
	s_and_b64 s[0:1], s[0:1], s[2:3]
	s_xor_b64 s[0:1], s[0:1], -1
	v_cndmask_b32_e64 v187, 0, 1, s[0:1]
	s_xor_b64 s[0:1], s[48:49], -1
	s_xor_b64 s[2:3], s[18:19], -1
	s_and_b64 s[0:1], s[0:1], s[2:3]
	s_xor_b64 s[0:1], s[0:1], -1
	v_add3_u32 v0, v0, v163, v187
	v_cndmask_b32_e64 v163, 0, 1, s[0:1]
	s_xor_b64 s[0:1], s[76:77], -1
	s_xor_b64 s[2:3], s[20:21], -1
	s_and_b64 s[0:1], s[0:1], s[2:3]
	s_xor_b64 s[0:1], s[0:1], -1
	v_cndmask_b32_e64 v187, 0, 1, s[0:1]
	s_xor_b64 s[0:1], s[50:51], -1
	s_xor_b64 s[2:3], s[22:23], -1
	s_and_b64 s[0:1], s[0:1], s[2:3]
	s_xor_b64 s[0:1], s[0:1], -1
	v_add3_u32 v0, v0, v163, v187
	v_cndmask_b32_e64 v163, 0, 1, s[0:1]
	s_xor_b64 s[0:1], s[78:79], -1
	s_xor_b64 s[2:3], s[24:25], -1
	s_and_b64 s[0:1], s[0:1], s[2:3]
	s_xor_b64 s[0:1], s[0:1], -1
	v_cndmask_b32_e64 v187, 0, 1, s[0:1]
	s_xor_b64 s[0:1], s[80:81], -1
	s_xor_b64 s[2:3], s[26:27], -1
	s_and_b64 s[0:1], s[0:1], s[2:3]
	s_xor_b64 s[0:1], s[0:1], -1
	v_add3_u32 v0, v0, v163, v187
	v_cndmask_b32_e64 v163, 0, 1, s[0:1]
	s_xor_b64 s[0:1], s[52:53], -1
	s_xor_b64 s[2:3], s[28:29], -1
	s_and_b64 s[0:1], s[0:1], s[2:3]
	s_xor_b64 s[0:1], s[0:1], -1
	v_cndmask_b32_e64 v187, 0, 1, s[0:1]
	s_xor_b64 s[0:1], s[54:55], -1
	s_xor_b64 s[2:3], s[30:31], -1
	s_and_b64 s[0:1], s[0:1], s[2:3]
	s_xor_b64 s[0:1], s[0:1], -1
	v_add3_u32 v0, v0, v163, v187
	v_cndmask_b32_e64 v163, 0, 1, s[0:1]
	s_xor_b64 s[0:1], s[82:83], -1
	s_xor_b64 s[2:3], s[34:35], -1
	s_and_b64 s[0:1], s[0:1], s[2:3]
	s_xor_b64 s[0:1], s[0:1], -1
	v_cndmask_b32_e64 v187, 0, 1, s[0:1]
	s_xor_b64 s[0:1], s[56:57], -1
	s_xor_b64 s[2:3], s[36:37], -1
	s_and_b64 s[0:1], s[0:1], s[2:3]
	s_xor_b64 s[0:1], s[0:1], -1
	v_add3_u32 v0, v0, v163, v187
	v_cndmask_b32_e64 v163, 0, 1, s[0:1]
	v_add3_u32 v0, v0, v163, v201
	v_readlane_b32 s0, v253, 51
	s_nop 1
	v_lshl_add_u32 v0, v0, 4, s0
	v_readlane_b32 s0, v254, 25
	v_readlane_b32 s1, v254, 26
	s_nop 1
	v_cndmask_b32_e64 v163, v206, 0, s[0:1]
	v_div_scale_f32 v187, s[0:1], v186, v186, v164
	v_rcp_f32_e32 v188, v187
	v_add_u32_e32 v163, v163, v204
	v_fma_f32 v189, -v187, v188, 1.0
	v_fmac_f32_e32 v188, v189, v188
	v_div_scale_f32 v189, vcc, v164, v186, v164
	v_mul_f32_e32 v207, v189, v188
	v_fma_f32 v208, -v187, v207, v189
	v_fmac_f32_e32 v207, v208, v188
	v_fma_f32 v187, -v187, v207, v189
	v_div_fmas_f32 v187, v187, v188, v207
	v_div_fixup_f32 v164, v187, v186, v164
	ds_write_b96 v0, v[162:164]
	s_waitcnt lgkmcnt(0)
	s_branch .LBB0_1046

.LBB0_1121:
	s_or_b64 exec, exec, s[0:1]
	v_readlane_b32 s0, v253, 42
	v_readlane_b32 s1, v253, 43
	s_waitcnt lgkmcnt(0)
	v_mov_b32_e32 v1, v226
	s_andn2_b64 vcc, exec, s[0:1]
	s_barrier
	s_cbranch_vccnz .LBB0_1147
	v_readlane_b32 s2, v252, 2
	v_readlane_b32 s3, v252, 3
	s_add_u32 s6, s2, 0x100000
	s_addc_u32 s7, s3, 0
	s_add_u32 s8, s2, 0x108000
	s_addc_u32 s9, s3, 0
	s_add_u32 s10, s2, 0x20750a00
	s_addc_u32 s11, s3, 0
	s_add_u32 s12, s2, 0x20770a00
	s_addc_u32 s13, s3, 0
	s_add_u32 s14, s2, 0x108a00
	s_addc_u32 s15, s3, 0
	s_add_u32 s16, s2, 0x188a00
	s_addc_u32 s17, s3, 0
	s_add_u32 s18, s2, 0x208a00
	s_addc_u32 s19, s3, 0
	s_add_u32 s20, s2, 0x288a00
	s_addc_u32 s21, s3, 0
	v_ashrrev_i32_e32 v0, 1, v1
	s_add_u32 s22, s2, 0x308a00
	v_and_b32_e32 v4, -16, v0
	v_or_b32_e32 v3, 15, v0
	s_addc_u32 s23, s3, 0
	v_and_b32_e32 v2, 31, v1
	v_lshl_add_u32 v8, v1, 2, 0
	v_cmp_eq_u32_e64 s[0:1], 0, v1
	s_add_u32 s24, s2, 0x80000
	v_ashrrev_i32_e32 v9, 2, v1
	v_and_b32_e32 v10, 3, v1
	v_max_i32_e32 v1, v3, v4
	v_lshlrev_b32_e32 v0, 5, v0
	s_movk_i32 s2, 0xfe00
	v_sub_u32_e32 v5, v1, v4
	v_and_or_b32 v0, v0, s2, v2
	s_brev_b32 s2, 16
	s_addc_u32 s25, s3, 0
	v_add_u32_e32 v1, 1, v1
	v_cmp_gt_u32_e64 s[2:3], s2, v5
	v_lshl_add_u32 v5, v5, 5, v0
	v_sub_u32_e32 v6, v1, v4
	v_cmp_ge_i32_e64 s[4:5], v5, v0
	v_cmp_lt_u32_e32 vcc, 13, v6
	s_and_b64 s[4:5], s[4:5], s[2:3]
	v_and_b32_e32 v0, 1, v1
	s_and_b64 s[26:27], vcc, s[4:5]
	v_readlane_b32 s4, v252, 0
	v_sub_u32_e32 v11, v6, v0
	v_and_b32_e32 v12, -2, v1
	v_mov_b32_e32 v1, v2
	v_or_b32_e32 v5, 1, v4
	v_cmp_eq_u32_e64 s[2:3], 1, v0
	v_mov_b32_e32 v13, 0
	s_mov_b32 s33, s4
	v_readlane_b32 s5, v252, 1
	s_branch .LBB0_1125
	s_nop 0
	s_nop 0
	s_nop 0
	s_nop 0
	s_nop 0
	s_nop 0
	s_nop 0
	s_nop 0
	s_nop 0
	s_nop 0
	s_nop 0
	s_nop 0
	s_nop 0
	s_nop 0
